# v43 + fused-loop compute segment trims (redundant lgkmcnt wait, trailing pad behind last MFMA block)
# baseline (speedup 1.0000x reference)
; #define PG8_STAGE(bufoff, gbase, voff) do { _Pragma("unroll") for (int _i = 0; _i < 2; ++_i) \
;         __builtin_amdgcn_global_load_lds((const unsigned*)((const char*)(gbase) + (voff)[_i]), (PG8_LAS unsigned*)(lds + (bufoff) + ldsw + _i * 8192), 16, 0, 0); } while (0)
; #define PG8_WAIT_V(n) asm volatile("s_waitcnt vmcnt(" #n ")" ::: "memory")
; #define PG8_WAIT_L(n) asm volatile("s_waitcnt lgkmcnt(" #n ")" ::: "memory")
; #define PG8_BAR __builtin_amdgcn_s_barrier()
; #define PG8_SCHED __builtin_amdgcn_sched_barrier(0)
; template <class Epi, class Sched, bool ALIGN_EPI = true, bool F8 = false>
; __device__ __forceinline__ void gemm_phase(PG8_LAS unsigned char* lds, const Sched& S, const Epi& E) {
;     ...
;             PG8_LDB(B0, 0, 0); PG8_LDB(B1, 0, 1); PG8_SCHED; PG8_LDA(At, 0, 0); PG8_STAGE(PG8_SA(1, 1), a1, voffA[1]);
;             PG8_WAIT_V(8); PG8_WAIT_L(0); PG8_BAR; PG8_MMA(0, 0, At, B0); PG8_MMA(0, 1, At, B1); PG8_BAR; PG8_SCHED;
;             PG8_LDA(At, 0, 1); PG8_STAGE(PG8_SB(0, 0), b2, voffB[0]); PG8_STAGE(PG8_SB(0, 1), b2, voffB[1]); PG8_STAGE(PG8_SA(0, 0), a2, vA2[0]);
;             PG8_WAIT_V(8); PG8_WAIT_L(0); PG8_BAR; PG8_MMA(1, 0, At, B0); PG8_MMA(1, 1, At, B1); PG8_BAR; PG8_SCHED;
;             PG8_LDB(B0, 1, 0); PG8_LDB(B1, 1, 1); PG8_SCHED; PG8_LDA(At, 1, 0); PG8_STAGE(PG8_SA(0, 1), a2, vA2[1]);
;             PG8_WAIT_V(8); PG8_WAIT_L(0); PG8_BAR; PG8_MMA(0, 0, At, B0); PG8_MMA(0, 1, At, B1); PG8_BAR; PG8_SCHED;
;             PG8_LDA(At, 1, 1); PG8_STAGE(PG8_SB(1, 0), b3, voffB[0]); PG8_STAGE(PG8_SB(1, 1), b3, voffB[1]); PG8_STAGE(PG8_SA(1, 0), a3, vA2[0]);
;             PG8_WAIT_V(8); PG8_WAIT_L(0); PG8_BAR; PG8_MMA(1, 0, At, B0); PG8_MMA(1, 1, At, B1); PG8_BAR; PG8_SCHED;
.LBB0_372:
	ds_read_b128 v[18:21], v207
	ds_read_b128 v[22:25], v207 offset:1024
	ds_read_b128 v[26:29], v207 offset:2048
	ds_read_b128 v[30:33], v207 offset:3072
	ds_read_b128 v[2:5], v208
	ds_read_b128 v[6:9], v208 offset:1024
	ds_read_b128 v[10:13], v208 offset:2048
	ds_read_b128 v[14:17], v208 offset:3072
	s_add_u32 s28, s26, 0x8000
	s_addc_u32 s29, s27, 0
	s_cmp_eq_u32 s21, 12
	s_cselect_b32 s40, s22, s28
	s_cselect_b32 s41, s23, s29
	s_cselect_b32 s30, s24, s5
	s_cselect_b32 s31, s25, s19
	s_add_u32 s28, s40, 0x8000
	s_addc_u32 s29, s41, 0
	v_lshl_add_u64 v[244:245], s[26:27], 0, v[190:191]
	s_add_i32 m0, s46, 0xc000
	ds_read_b128 v[212:215], v209
	ds_read_b128 v[216:219], v209 offset:1024
	ds_read_b128 v[220:223], v209 offset:2048
	ds_read_b128 v[224:227], v209 offset:3072
	ds_read_b128 v[228:231], v209 offset:4096
	ds_read_b128 v[232:235], v209 offset:5120
	ds_read_b128 v[236:239], v209 offset:6144
	ds_read_b128 v[240:243], v209 offset:7168
	global_load_lds_dwordx4 v[244:245], off
	v_lshl_add_u64 v[244:245], s[26:27], 0, v[188:189]
	s_add_i32 m0, s46, 0xe000
	s_nop 0
	global_load_lds_dwordx4 v[244:245], off
	s_waitcnt vmcnt(8)
	s_waitcnt lgkmcnt(0)
	s_setprio 1
	v_mfma_scale_f32_16x16x128_f8f6f4 v[158:161], v[18:25], v[212:219], v[158:161], v210, v210 op_sel_hi:[0,0,0]
	v_mfma_scale_f32_16x16x128_f8f6f4 v[154:157], v[26:33], v[212:219], v[154:157], v210, v210 op_sel_hi:[0,0,0]
	v_mfma_scale_f32_16x16x128_f8f6f4 v[142:145], v[18:25], v[220:227], v[142:145], v210, v210 op_sel_hi:[0,0,0]
	v_mfma_scale_f32_16x16x128_f8f6f4 v[138:141], v[26:33], v[220:227], v[138:141], v210, v210 op_sel_hi:[0,0,0]
	v_mfma_scale_f32_16x16x128_f8f6f4 v[126:129], v[18:25], v[228:235], v[126:129], v210, v210 op_sel_hi:[0,0,0]
	v_mfma_scale_f32_16x16x128_f8f6f4 v[122:125], v[26:33], v[228:235], v[122:125], v210, v210 op_sel_hi:[0,0,0]
	v_mfma_scale_f32_16x16x128_f8f6f4 v[110:113], v[18:25], v[236:243], v[110:113], v210, v210 op_sel_hi:[0,0,0]
	v_mfma_scale_f32_16x16x128_f8f6f4 v[106:109], v[26:33], v[236:243], v[106:109], v210, v210 op_sel_hi:[0,0,0]
	s_nop 3
	s_setprio 0
	s_setprio 1
	v_mfma_scale_f32_16x16x128_f8f6f4 v[150:153], v[2:9], v[212:219], v[150:153], v210, v210 op_sel_hi:[0,0,0]
	v_mfma_scale_f32_16x16x128_f8f6f4 v[146:149], v[10:17], v[212:219], v[146:149], v210, v210 op_sel_hi:[0,0,0]
	v_mfma_scale_f32_16x16x128_f8f6f4 v[134:137], v[2:9], v[220:227], v[134:137], v210, v210 op_sel_hi:[0,0,0]
	v_mfma_scale_f32_16x16x128_f8f6f4 v[130:133], v[10:17], v[220:227], v[130:133], v210, v210 op_sel_hi:[0,0,0]
	v_mfma_scale_f32_16x16x128_f8f6f4 v[118:121], v[2:9], v[228:235], v[118:121], v210, v210 op_sel_hi:[0,0,0]
	v_mfma_scale_f32_16x16x128_f8f6f4 v[114:117], v[10:17], v[228:235], v[114:117], v210, v210 op_sel_hi:[0,0,0]
	v_mfma_scale_f32_16x16x128_f8f6f4 v[102:105], v[2:9], v[236:243], v[102:105], v210, v210 op_sel_hi:[0,0,0]
	v_mfma_scale_f32_16x16x128_f8f6f4 v[98:101], v[10:17], v[236:243], v[98:101], v210, v210 op_sel_hi:[0,0,0]
	s_setprio 0
	s_barrier
	s_add_i32 s67, s62, s45
	v_lshl_add_u64 v[244:245], s[30:31], 0, v[164:165]
	s_mov_b32 m0, s67
	ds_read_b128 v[212:215], v209 offset:16384
	ds_read_b128 v[216:219], v209 offset:17408
	ds_read_b128 v[220:223], v209 offset:18432
	ds_read_b128 v[224:227], v209 offset:19456
	ds_read_b128 v[228:231], v209 offset:20480
	ds_read_b128 v[232:235], v209 offset:21504
	ds_read_b128 v[236:239], v209 offset:22528
	ds_read_b128 v[240:243], v209 offset:23552
	global_load_lds_dwordx4 v[244:245], off
	v_lshl_add_u64 v[246:247], s[30:31], 0, v[166:167]
	s_add_i32 m0, s67, 0x2000
	s_add_i32 s67, s63, s45
	global_load_lds_dwordx4 v[246:247], off
	v_lshl_add_u64 v[244:245], v[244:245], 0, s[8:9]
	s_mov_b32 m0, s67
	s_nop 0
	global_load_lds_dwordx4 v[244:245], off
	v_lshl_add_u64 v[244:245], v[246:247], 0, s[8:9]
	s_add_i32 m0, s67, 0x2000
	s_nop 0
	global_load_lds_dwordx4 v[244:245], off
	v_lshl_add_u64 v[244:245], s[40:41], 0, v[174:175]
	s_mov_b32 m0, s46
	s_nop 0
	global_load_lds_dwordx4 v[244:245], off
	v_lshl_add_u64 v[244:245], s[40:41], 0, v[176:177]
	s_mov_b32 m0, s47
	s_nop 0
	global_load_lds_dwordx4 v[244:245], off
	s_waitcnt vmcnt(8)
	s_waitcnt lgkmcnt(0)
	s_setprio 1
	v_mfma_scale_f32_16x16x128_f8f6f4 v[94:97], v[18:25], v[212:219], v[94:97], v210, v210 op_sel_hi:[0,0,0]
	v_mfma_scale_f32_16x16x128_f8f6f4 v[90:93], v[26:33], v[212:219], v[90:93], v210, v210 op_sel_hi:[0,0,0]
	v_mfma_scale_f32_16x16x128_f8f6f4 v[78:81], v[18:25], v[220:227], v[78:81], v210, v210 op_sel_hi:[0,0,0]
	v_mfma_scale_f32_16x16x128_f8f6f4 v[74:77], v[26:33], v[220:227], v[74:77], v210, v210 op_sel_hi:[0,0,0]
	v_mfma_scale_f32_16x16x128_f8f6f4 v[62:65], v[18:25], v[228:235], v[62:65], v210, v210 op_sel_hi:[0,0,0]
	v_mfma_scale_f32_16x16x128_f8f6f4 v[58:61], v[26:33], v[228:235], v[58:61], v210, v210 op_sel_hi:[0,0,0]
	v_mfma_scale_f32_16x16x128_f8f6f4 v[46:49], v[18:25], v[236:243], v[46:49], v210, v210 op_sel_hi:[0,0,0]
	v_mfma_scale_f32_16x16x128_f8f6f4 v[42:45], v[26:33], v[236:243], v[42:45], v210, v210 op_sel_hi:[0,0,0]
	s_nop 3
	s_setprio 0
	s_setprio 1
	v_mfma_scale_f32_16x16x128_f8f6f4 v[86:89], v[2:9], v[212:219], v[86:89], v210, v210 op_sel_hi:[0,0,0]
	v_mfma_scale_f32_16x16x128_f8f6f4 v[82:85], v[10:17], v[212:219], v[82:85], v210, v210 op_sel_hi:[0,0,0]
	v_mfma_scale_f32_16x16x128_f8f6f4 v[70:73], v[2:9], v[220:227], v[70:73], v210, v210 op_sel_hi:[0,0,0]
	v_mfma_scale_f32_16x16x128_f8f6f4 v[66:69], v[10:17], v[220:227], v[66:69], v210, v210 op_sel_hi:[0,0,0]
	v_mfma_scale_f32_16x16x128_f8f6f4 v[54:57], v[2:9], v[228:235], v[54:57], v210, v210 op_sel_hi:[0,0,0]
	v_mfma_scale_f32_16x16x128_f8f6f4 v[50:53], v[10:17], v[228:235], v[50:53], v210, v210 op_sel_hi:[0,0,0]
	v_mfma_scale_f32_16x16x128_f8f6f4 v[38:41], v[2:9], v[236:243], v[38:41], v210, v210 op_sel_hi:[0,0,0]
	v_mfma_scale_f32_16x16x128_f8f6f4 v[34:37], v[10:17], v[236:243], v[34:37], v210, v210 op_sel_hi:[0,0,0]
	s_setprio 0
	s_barrier
; #define PG8_STAGE(bufoff, gbase, voff) do { _Pragma("unroll") for (int _i = 0; _i < 2; ++_i) \
;         __builtin_amdgcn_global_load_lds((const unsigned*)((const char*)(gbase) + (voff)[_i]), (PG8_LAS unsigned*)(lds + (bufoff) + ldsw + _i * 8192), 16, 0, 0); } while (0)
; #define PG8_WAIT_V(n) asm volatile("s_waitcnt vmcnt(" #n ")" ::: "memory")
; #define PG8_WAIT_L(n) asm volatile("s_waitcnt lgkmcnt(" #n ")" ::: "memory")
; #define PG8_BAR __builtin_amdgcn_s_barrier()
; #define PG8_SCHED __builtin_amdgcn_sched_barrier(0)
; template <class Epi, class Sched, bool ALIGN_EPI = true, bool F8 = false>
; __device__ __forceinline__ void gemm_phase(PG8_LAS unsigned char* lds, const Sched& S, const Epi& E) {
;     ...
;         for (int t = 0; t < nt; t += 2) {
;             const bool last = (t == nt - 2);
;             if constexpr (Sched::GATHER) { if (last && has_next) S.a_off(nxt, Rs, Cs, voffAn); }
;             const char* a1 = cA + (size_t)(t + 1) * kstep;
;             const char* a2 = last ? nA : cA + (size_t)(t + 2) * kstep; const char* b2 = last ? nB : cB + (size_t)(t + 2) * kstepB;
;             const char* a3 = a2 + kstep; const char* b3 = b2 + kstepB;
;     ...
;             PG8_LDB(B0, 0, 0); PG8_LDB(B1, 0, 1); PG8_SCHED; PG8_LDA(At, 0, 0); PG8_STAGE(PG8_SA(1, 1), a1, voffA[1]);
;             PG8_WAIT_V(8); PG8_WAIT_L(0); PG8_BAR; PG8_MMA(0, 0, At, B0); PG8_MMA(0, 1, At, B1); PG8_BAR; PG8_SCHED;
;             PG8_LDA(At, 0, 1); PG8_STAGE(PG8_SB(0, 0), b2, voffB[0]); PG8_STAGE(PG8_SB(0, 1), b2, voffB[1]); PG8_STAGE(PG8_SA(0, 0), a2, vA2[0]);
;             PG8_WAIT_V(8); PG8_WAIT_L(0); PG8_BAR; PG8_MMA(1, 0, At, B0); PG8_MMA(1, 1, At, B1); PG8_BAR; PG8_SCHED;
;             PG8_LDB(B0, 1, 0); PG8_LDB(B1, 1, 1); PG8_SCHED; PG8_LDA(At, 1, 0); PG8_STAGE(PG8_SA(0, 1), a2, vA2[1]);
;             PG8_WAIT_V(8); PG8_WAIT_L(0); PG8_BAR; PG8_MMA(0, 0, At, B0); PG8_MMA(0, 1, At, B1); PG8_BAR; PG8_SCHED;
;             PG8_LDA(At, 1, 1); PG8_STAGE(PG8_SB(1, 0), b3, voffB[0]); PG8_STAGE(PG8_SB(1, 1), b3, voffB[1]); PG8_STAGE(PG8_SA(1, 0), a3, vA2[0]);
;             PG8_WAIT_V(8); PG8_WAIT_L(0); PG8_BAR; PG8_MMA(1, 0, At, B0); PG8_MMA(1, 1, At, B1); PG8_BAR; PG8_SCHED;
	s_add_i32 s67, 0, 0x18000
	s_add_i32 s68, 0, 0x1c000
	v_add_u32_e32 v14, s67, v202
	v_add_u32_e32 v30, s68, v202
	ds_read_b128 v[2:5], v14
	ds_read_b128 v[6:9], v14 offset:1024
	ds_read_b128 v[10:13], v14 offset:2048
	ds_read_b128 v[14:17], v14 offset:3072
	ds_read_b128 v[18:21], v30
	ds_read_b128 v[22:25], v30 offset:1024
	ds_read_b128 v[26:29], v30 offset:2048
	ds_read_b128 v[30:33], v30 offset:3072
	s_mov_b32 m0, s48
	v_lshl_add_u64 v[244:245], s[40:41], 0, v[178:179]
	ds_read_b128 v[212:215], v209 offset:32768
	ds_read_b128 v[216:219], v209 offset:33792
	ds_read_b128 v[220:223], v209 offset:34816
	ds_read_b128 v[224:227], v209 offset:35840
	ds_read_b128 v[228:231], v209 offset:36864
	ds_read_b128 v[232:235], v209 offset:37888
	ds_read_b128 v[236:239], v209 offset:38912
	ds_read_b128 v[240:243], v209 offset:39936
	global_load_lds_dwordx4 v[244:245], off
	v_lshl_add_u64 v[244:245], s[40:41], 0, v[180:181]
	s_mov_b32 m0, s49
	s_nop 0
	global_load_lds_dwordx4 v[244:245], off
	s_waitcnt vmcnt(8)
	s_waitcnt lgkmcnt(0)
	s_setprio 1
	v_mfma_scale_f32_16x16x128_f8f6f4 v[158:161], v[2:9], v[212:219], v[158:161], v210, v210 op_sel_hi:[0,0,0]
	v_mfma_scale_f32_16x16x128_f8f6f4 v[154:157], v[10:17], v[212:219], v[154:157], v210, v210 op_sel_hi:[0,0,0]
	v_mfma_scale_f32_16x16x128_f8f6f4 v[142:145], v[2:9], v[220:227], v[142:145], v210, v210 op_sel_hi:[0,0,0]
	v_mfma_scale_f32_16x16x128_f8f6f4 v[138:141], v[10:17], v[220:227], v[138:141], v210, v210 op_sel_hi:[0,0,0]
	v_mfma_scale_f32_16x16x128_f8f6f4 v[126:129], v[2:9], v[228:235], v[126:129], v210, v210 op_sel_hi:[0,0,0]
	v_mfma_scale_f32_16x16x128_f8f6f4 v[122:125], v[10:17], v[228:235], v[122:125], v210, v210 op_sel_hi:[0,0,0]
	v_mfma_scale_f32_16x16x128_f8f6f4 v[110:113], v[2:9], v[236:243], v[110:113], v210, v210 op_sel_hi:[0,0,0]
	v_mfma_scale_f32_16x16x128_f8f6f4 v[106:109], v[10:17], v[236:243], v[106:109], v210, v210 op_sel_hi:[0,0,0]
	s_nop 3
	s_setprio 0
	s_setprio 1
	v_mfma_scale_f32_16x16x128_f8f6f4 v[150:153], v[18:25], v[212:219], v[150:153], v210, v210 op_sel_hi:[0,0,0]
	v_mfma_scale_f32_16x16x128_f8f6f4 v[146:149], v[26:33], v[212:219], v[146:149], v210, v210 op_sel_hi:[0,0,0]
	v_mfma_scale_f32_16x16x128_f8f6f4 v[134:137], v[18:25], v[220:227], v[134:137], v210, v210 op_sel_hi:[0,0,0]
	v_mfma_scale_f32_16x16x128_f8f6f4 v[130:133], v[26:33], v[220:227], v[130:133], v210, v210 op_sel_hi:[0,0,0]
	v_mfma_scale_f32_16x16x128_f8f6f4 v[118:121], v[18:25], v[228:235], v[118:121], v210, v210 op_sel_hi:[0,0,0]
	v_mfma_scale_f32_16x16x128_f8f6f4 v[114:117], v[26:33], v[228:235], v[114:117], v210, v210 op_sel_hi:[0,0,0]
	v_mfma_scale_f32_16x16x128_f8f6f4 v[102:105], v[18:25], v[236:243], v[102:105], v210, v210 op_sel_hi:[0,0,0]
	v_mfma_scale_f32_16x16x128_f8f6f4 v[98:101], v[26:33], v[236:243], v[98:101], v210, v210 op_sel_hi:[0,0,0]
	s_setprio 0
	s_barrier
	s_add_u32 s30, s30, 0x8000
	s_addc_u32 s31, s31, 0
	s_add_i32 s40, s67, s45
	v_lshl_add_u64 v[244:245], s[30:31], 0, v[164:165]
	s_mov_b32 m0, s40
	ds_read_b128 v[212:215], v209 offset:49152
	ds_read_b128 v[216:219], v209 offset:50176
	ds_read_b128 v[220:223], v209 offset:51200
	ds_read_b128 v[224:227], v209 offset:52224
	ds_read_b128 v[228:231], v209 offset:53248
	ds_read_b128 v[232:235], v209 offset:54272
	ds_read_b128 v[236:239], v209 offset:55296
	ds_read_b128 v[240:243], v209 offset:56320
	global_load_lds_dwordx4 v[244:245], off
	v_lshl_add_u64 v[244:245], s[30:31], 0, v[166:167]
	s_add_i32 m0, s40, 0x2000
	s_add_i32 s40, s68, s45
	global_load_lds_dwordx4 v[244:245], off
	v_lshl_add_u64 v[244:245], s[30:31], 0, v[168:169]
	s_mov_b32 m0, s40
	s_nop 0
	global_load_lds_dwordx4 v[244:245], off
	v_lshl_add_u64 v[244:245], s[30:31], 0, v[172:173]
	s_add_i32 m0, s40, 0x2000
	s_nop 0
	global_load_lds_dwordx4 v[244:245], off
	v_lshl_add_u64 v[244:245], s[28:29], 0, v[174:175]
	s_mov_b32 m0, s52
	s_nop 0
	global_load_lds_dwordx4 v[244:245], off
	v_lshl_add_u64 v[244:245], s[28:29], 0, v[176:177]
	s_mov_b32 m0, s53
	s_nop 0
	global_load_lds_dwordx4 v[244:245], off
	s_waitcnt vmcnt(8)
	s_waitcnt lgkmcnt(0)
	s_setprio 1
	v_mfma_scale_f32_16x16x128_f8f6f4 v[94:97], v[2:9], v[212:219], v[94:97], v210, v210 op_sel_hi:[0,0,0]
	v_mfma_scale_f32_16x16x128_f8f6f4 v[90:93], v[10:17], v[212:219], v[90:93], v210, v210 op_sel_hi:[0,0,0]
	v_mfma_scale_f32_16x16x128_f8f6f4 v[78:81], v[2:9], v[220:227], v[78:81], v210, v210 op_sel_hi:[0,0,0]
	v_mfma_scale_f32_16x16x128_f8f6f4 v[74:77], v[10:17], v[220:227], v[74:77], v210, v210 op_sel_hi:[0,0,0]
	v_mfma_scale_f32_16x16x128_f8f6f4 v[62:65], v[2:9], v[228:235], v[62:65], v210, v210 op_sel_hi:[0,0,0]
	v_mfma_scale_f32_16x16x128_f8f6f4 v[58:61], v[10:17], v[228:235], v[58:61], v210, v210 op_sel_hi:[0,0,0]
	v_mfma_scale_f32_16x16x128_f8f6f4 v[46:49], v[2:9], v[236:243], v[46:49], v210, v210 op_sel_hi:[0,0,0]
	v_mfma_scale_f32_16x16x128_f8f6f4 v[42:45], v[10:17], v[236:243], v[42:45], v210, v210 op_sel_hi:[0,0,0]
	s_nop 3
	s_setprio 0
	s_setprio 1
	v_mfma_scale_f32_16x16x128_f8f6f4 v[86:89], v[18:25], v[212:219], v[86:89], v210, v210 op_sel_hi:[0,0,0]
	v_mfma_scale_f32_16x16x128_f8f6f4 v[82:85], v[26:33], v[212:219], v[82:85], v210, v210 op_sel_hi:[0,0,0]
	v_mfma_scale_f32_16x16x128_f8f6f4 v[70:73], v[18:25], v[220:227], v[70:73], v210, v210 op_sel_hi:[0,0,0]
	v_mfma_scale_f32_16x16x128_f8f6f4 v[66:69], v[26:33], v[220:227], v[66:69], v210, v210 op_sel_hi:[0,0,0]
	v_mfma_scale_f32_16x16x128_f8f6f4 v[54:57], v[18:25], v[228:235], v[54:57], v210, v210 op_sel_hi:[0,0,0]
	v_mfma_scale_f32_16x16x128_f8f6f4 v[50:53], v[26:33], v[228:235], v[50:53], v210, v210 op_sel_hi:[0,0,0]
	v_mfma_scale_f32_16x16x128_f8f6f4 v[38:41], v[18:25], v[236:243], v[38:41], v210, v210 op_sel_hi:[0,0,0]
	v_mfma_scale_f32_16x16x128_f8f6f4 v[34:37], v[26:33], v[236:243], v[34:37], v210, v210 op_sel_hi:[0,0,0]
	s_setprio 0
	s_barrier
	s_add_i32 s21, s21, 2
	s_add_u32 s5, s5, 0x10000
	s_addc_u32 s19, s19, 0
	s_add_u32 s26, s26, 0x10000
	s_addc_u32 s27, s27, 0
	s_cmp_gt_u32 s21, 13
	s_cbranch_scc0 .LBB0_372
	s_branch .Lfx_9967
; #define PG8_STAGE(bufoff, gbase, voff) do { _Pragma("unroll") for (int _i = 0; _i < 2; ++_i) \
;         __builtin_amdgcn_global_load_lds((const unsigned*)((const char*)(gbase) + (voff)[_i]), (PG8_LAS unsigned*)(lds + (bufoff) + ldsw + _i * 8192), 16, 0, 0); } while (0)
; #define PG8_WAIT_V(n) asm volatile("s_waitcnt vmcnt(" #n ")" ::: "memory")
; #define PG8_WAIT_L(n) asm volatile("s_waitcnt lgkmcnt(" #n ")" ::: "memory")
; #define PG8_BAR __builtin_amdgcn_s_barrier()
; #define PG8_SCHED __builtin_amdgcn_sched_barrier(0)
; template <class Epi, class Sched, bool ALIGN_EPI = true, bool F8 = false>
; __device__ __forceinline__ void gemm_phase(PG8_LAS unsigned char* lds, const Sched& S, const Epi& E) {
;     ...
;             PG8_LDB(B0, 0, 0); PG8_LDB(B1, 0, 1); PG8_SCHED; PG8_LDA(At, 0, 0); PG8_STAGE(PG8_SA(1, 1), a1, voffA[1]);
;             PG8_WAIT_V(8); PG8_WAIT_L(0); PG8_BAR; PG8_MMA(0, 0, At, B0); PG8_MMA(0, 1, At, B1); PG8_BAR; PG8_SCHED;
;             PG8_LDA(At, 0, 1); PG8_STAGE(PG8_SB(0, 0), b2, voffB[0]); PG8_STAGE(PG8_SB(0, 1), b2, voffB[1]); PG8_STAGE(PG8_SA(0, 0), a2, vA2[0]);
;             PG8_WAIT_V(8); PG8_WAIT_L(0); PG8_BAR; PG8_MMA(1, 0, At, B0); PG8_MMA(1, 1, At, B1); PG8_BAR; PG8_SCHED;
;             PG8_LDB(B0, 1, 0); PG8_LDB(B1, 1, 1); PG8_SCHED; PG8_LDA(At, 1, 0); PG8_STAGE(PG8_SA(0, 1), a2, vA2[1]);
;             PG8_WAIT_V(8); PG8_WAIT_L(0); PG8_BAR; PG8_MMA(0, 0, At, B0); PG8_MMA(0, 1, At, B1); PG8_BAR; PG8_SCHED;
;             PG8_LDA(At, 1, 1); PG8_STAGE(PG8_SB(1, 0), b3, voffB[0]); PG8_STAGE(PG8_SB(1, 1), b3, voffB[1]); PG8_STAGE(PG8_SA(1, 0), a3, vA2[0]);
;             PG8_WAIT_V(8); PG8_WAIT_L(0); PG8_BAR; PG8_MMA(1, 0, At, B0); PG8_MMA(1, 1, At, B1); PG8_BAR; PG8_SCHED;
.Lh1e_9967:
.Lh1_372:
	ds_read_b128 v[18:21], v207
	ds_read_b128 v[22:25], v207 offset:1024
	ds_read_b128 v[26:29], v207 offset:2048
	ds_read_b128 v[30:33], v207 offset:3072
	ds_read_b128 v[2:5], v208
	ds_read_b128 v[6:9], v208 offset:1024
	ds_read_b128 v[10:13], v208 offset:2048
	ds_read_b128 v[14:17], v208 offset:3072
	s_add_u32 s28, s26, 0x8000
	s_addc_u32 s29, s27, 0
	s_cmp_eq_u32 s21, 12
	s_cselect_b32 s40, s22, s28
	s_cselect_b32 s41, s23, s29
	s_cselect_b32 s30, s24, s5
	s_cselect_b32 s31, s25, s19
	s_add_u32 s28, s40, 0x8000
	s_addc_u32 s29, s41, 0
	v_lshl_add_u64 v[244:245], s[26:27], 0, v[190:191]
	s_add_i32 m0, s46, 0xc000
	ds_read_b128 v[212:215], v209
	ds_read_b128 v[216:219], v209 offset:1024
	ds_read_b128 v[220:223], v209 offset:2048
	ds_read_b128 v[224:227], v209 offset:3072
	ds_read_b128 v[228:231], v209 offset:4096
	ds_read_b128 v[232:235], v209 offset:5120
	ds_read_b128 v[236:239], v209 offset:6144
	ds_read_b128 v[240:243], v209 offset:7168
	global_load_lds_dwordx4 v[244:245], off
	v_lshl_add_u64 v[244:245], s[26:27], 0, v[188:189]
	s_add_i32 m0, s46, 0xe000
	s_nop 0
	global_load_lds_dwordx4 v[244:245], off
	s_waitcnt vmcnt(8)
	s_waitcnt lgkmcnt(0)
	s_barrier
	s_setprio 2
	v_mfma_scale_f32_16x16x128_f8f6f4 v[158:161], v[18:25], v[212:219], v[158:161], v210, v210 op_sel_hi:[0,0,0]
	v_mfma_scale_f32_16x16x128_f8f6f4 v[154:157], v[26:33], v[212:219], v[154:157], v210, v210 op_sel_hi:[0,0,0]
	v_mfma_scale_f32_16x16x128_f8f6f4 v[142:145], v[18:25], v[220:227], v[142:145], v210, v210 op_sel_hi:[0,0,0]
	v_mfma_scale_f32_16x16x128_f8f6f4 v[138:141], v[26:33], v[220:227], v[138:141], v210, v210 op_sel_hi:[0,0,0]
	v_mfma_scale_f32_16x16x128_f8f6f4 v[126:129], v[18:25], v[228:235], v[126:129], v210, v210 op_sel_hi:[0,0,0]
	v_mfma_scale_f32_16x16x128_f8f6f4 v[122:125], v[26:33], v[228:235], v[122:125], v210, v210 op_sel_hi:[0,0,0]
	v_mfma_scale_f32_16x16x128_f8f6f4 v[110:113], v[18:25], v[236:243], v[110:113], v210, v210 op_sel_hi:[0,0,0]
	v_mfma_scale_f32_16x16x128_f8f6f4 v[106:109], v[26:33], v[236:243], v[106:109], v210, v210 op_sel_hi:[0,0,0]
	s_nop 3
	s_setprio 0
	s_setprio 2
	v_mfma_scale_f32_16x16x128_f8f6f4 v[150:153], v[2:9], v[212:219], v[150:153], v210, v210 op_sel_hi:[0,0,0]
	v_mfma_scale_f32_16x16x128_f8f6f4 v[146:149], v[10:17], v[212:219], v[146:149], v210, v210 op_sel_hi:[0,0,0]
	v_mfma_scale_f32_16x16x128_f8f6f4 v[134:137], v[2:9], v[220:227], v[134:137], v210, v210 op_sel_hi:[0,0,0]
	v_mfma_scale_f32_16x16x128_f8f6f4 v[130:133], v[10:17], v[220:227], v[130:133], v210, v210 op_sel_hi:[0,0,0]
	v_mfma_scale_f32_16x16x128_f8f6f4 v[118:121], v[2:9], v[228:235], v[118:121], v210, v210 op_sel_hi:[0,0,0]
	v_mfma_scale_f32_16x16x128_f8f6f4 v[114:117], v[10:17], v[228:235], v[114:117], v210, v210 op_sel_hi:[0,0,0]
	v_mfma_scale_f32_16x16x128_f8f6f4 v[102:105], v[2:9], v[236:243], v[102:105], v210, v210 op_sel_hi:[0,0,0]
	v_mfma_scale_f32_16x16x128_f8f6f4 v[98:101], v[10:17], v[236:243], v[98:101], v210, v210 op_sel_hi:[0,0,0]
	s_setprio 0
	s_add_i32 s67, s62, s45
	v_lshl_add_u64 v[244:245], s[30:31], 0, v[164:165]
	s_mov_b32 m0, s67
	ds_read_b128 v[212:215], v209 offset:16384
	ds_read_b128 v[216:219], v209 offset:17408
	ds_read_b128 v[220:223], v209 offset:18432
	ds_read_b128 v[224:227], v209 offset:19456
	ds_read_b128 v[228:231], v209 offset:20480
	ds_read_b128 v[232:235], v209 offset:21504
	ds_read_b128 v[236:239], v209 offset:22528
	ds_read_b128 v[240:243], v209 offset:23552
	global_load_lds_dwordx4 v[244:245], off
	v_lshl_add_u64 v[246:247], s[30:31], 0, v[166:167]
	s_add_i32 m0, s67, 0x2000
	s_add_i32 s67, s63, s45
	global_load_lds_dwordx4 v[246:247], off
	v_lshl_add_u64 v[244:245], v[244:245], 0, s[8:9]
	s_mov_b32 m0, s67
	s_nop 0
	global_load_lds_dwordx4 v[244:245], off
	v_lshl_add_u64 v[244:245], v[246:247], 0, s[8:9]
	s_add_i32 m0, s67, 0x2000
	s_nop 0
	global_load_lds_dwordx4 v[244:245], off
	v_lshl_add_u64 v[244:245], s[40:41], 0, v[174:175]
	s_mov_b32 m0, s46
	s_nop 0
	global_load_lds_dwordx4 v[244:245], off
	v_lshl_add_u64 v[244:245], s[40:41], 0, v[176:177]
	s_mov_b32 m0, s47
	s_nop 0
	global_load_lds_dwordx4 v[244:245], off
	s_waitcnt vmcnt(8)
	s_waitcnt lgkmcnt(0)
	s_barrier
	s_setprio 2
	v_mfma_scale_f32_16x16x128_f8f6f4 v[94:97], v[18:25], v[212:219], v[94:97], v210, v210 op_sel_hi:[0,0,0]
	v_mfma_scale_f32_16x16x128_f8f6f4 v[90:93], v[26:33], v[212:219], v[90:93], v210, v210 op_sel_hi:[0,0,0]
	v_mfma_scale_f32_16x16x128_f8f6f4 v[78:81], v[18:25], v[220:227], v[78:81], v210, v210 op_sel_hi:[0,0,0]
	v_mfma_scale_f32_16x16x128_f8f6f4 v[74:77], v[26:33], v[220:227], v[74:77], v210, v210 op_sel_hi:[0,0,0]
	v_mfma_scale_f32_16x16x128_f8f6f4 v[62:65], v[18:25], v[228:235], v[62:65], v210, v210 op_sel_hi:[0,0,0]
	v_mfma_scale_f32_16x16x128_f8f6f4 v[58:61], v[26:33], v[228:235], v[58:61], v210, v210 op_sel_hi:[0,0,0]
	v_mfma_scale_f32_16x16x128_f8f6f4 v[46:49], v[18:25], v[236:243], v[46:49], v210, v210 op_sel_hi:[0,0,0]
	v_mfma_scale_f32_16x16x128_f8f6f4 v[42:45], v[26:33], v[236:243], v[42:45], v210, v210 op_sel_hi:[0,0,0]
	s_nop 3
	s_setprio 0
	s_setprio 2
	v_mfma_scale_f32_16x16x128_f8f6f4 v[86:89], v[2:9], v[212:219], v[86:89], v210, v210 op_sel_hi:[0,0,0]
	v_mfma_scale_f32_16x16x128_f8f6f4 v[82:85], v[10:17], v[212:219], v[82:85], v210, v210 op_sel_hi:[0,0,0]
	v_mfma_scale_f32_16x16x128_f8f6f4 v[70:73], v[2:9], v[220:227], v[70:73], v210, v210 op_sel_hi:[0,0,0]
	v_mfma_scale_f32_16x16x128_f8f6f4 v[66:69], v[10:17], v[220:227], v[66:69], v210, v210 op_sel_hi:[0,0,0]
	v_mfma_scale_f32_16x16x128_f8f6f4 v[54:57], v[2:9], v[228:235], v[54:57], v210, v210 op_sel_hi:[0,0,0]
	v_mfma_scale_f32_16x16x128_f8f6f4 v[50:53], v[10:17], v[228:235], v[50:53], v210, v210 op_sel_hi:[0,0,0]
	v_mfma_scale_f32_16x16x128_f8f6f4 v[38:41], v[2:9], v[236:243], v[38:41], v210, v210 op_sel_hi:[0,0,0]
	v_mfma_scale_f32_16x16x128_f8f6f4 v[34:37], v[10:17], v[236:243], v[34:37], v210, v210 op_sel_hi:[0,0,0]
	s_setprio 0
	s_add_i32 s67, 0, 0x18000
	s_add_i32 s68, 0, 0x1c000
	v_add_u32_e32 v14, s67, v202
	v_add_u32_e32 v30, s68, v202
	ds_read_b128 v[2:5], v14
	ds_read_b128 v[6:9], v14 offset:1024
	ds_read_b128 v[10:13], v14 offset:2048
	ds_read_b128 v[14:17], v14 offset:3072
	ds_read_b128 v[18:21], v30
	ds_read_b128 v[22:25], v30 offset:1024
	ds_read_b128 v[26:29], v30 offset:2048
	ds_read_b128 v[30:33], v30 offset:3072
	s_mov_b32 m0, s48
	v_lshl_add_u64 v[244:245], s[40:41], 0, v[178:179]
	ds_read_b128 v[212:215], v209 offset:32768
	ds_read_b128 v[216:219], v209 offset:33792
	ds_read_b128 v[220:223], v209 offset:34816
	ds_read_b128 v[224:227], v209 offset:35840
	ds_read_b128 v[228:231], v209 offset:36864
	ds_read_b128 v[232:235], v209 offset:37888
	ds_read_b128 v[236:239], v209 offset:38912
	ds_read_b128 v[240:243], v209 offset:39936
	global_load_lds_dwordx4 v[244:245], off
	v_lshl_add_u64 v[244:245], s[40:41], 0, v[180:181]
	s_mov_b32 m0, s49
	s_nop 0
	global_load_lds_dwordx4 v[244:245], off
	s_waitcnt vmcnt(8)
	s_waitcnt lgkmcnt(0)
	s_barrier
; #define PG8_STAGE(bufoff, gbase, voff) do { _Pragma("unroll") for (int _i = 0; _i < 2; ++_i) \
;         __builtin_amdgcn_global_load_lds((const unsigned*)((const char*)(gbase) + (voff)[_i]), (PG8_LAS unsigned*)(lds + (bufoff) + ldsw + _i * 8192), 16, 0, 0); } while (0)
; #define PG8_WAIT_V(n) asm volatile("s_waitcnt vmcnt(" #n ")" ::: "memory")
; #define PG8_WAIT_L(n) asm volatile("s_waitcnt lgkmcnt(" #n ")" ::: "memory")
; #define PG8_BAR __builtin_amdgcn_s_barrier()
; #define PG8_SCHED __builtin_amdgcn_sched_barrier(0)
; template <class Epi, class Sched, bool ALIGN_EPI = true, bool F8 = false>
; __device__ __forceinline__ void gemm_phase(PG8_LAS unsigned char* lds, const Sched& S, const Epi& E) {
;     ...
;         for (int t = 0; t < nt; t += 2) {
;             const bool last = (t == nt - 2);
;             if constexpr (Sched::GATHER) { if (last && has_next) S.a_off(nxt, Rs, Cs, voffAn); }
;             const char* a1 = cA + (size_t)(t + 1) * kstep;
;             const char* a2 = last ? nA : cA + (size_t)(t + 2) * kstep; const char* b2 = last ? nB : cB + (size_t)(t + 2) * kstepB;
;             const char* a3 = a2 + kstep; const char* b3 = b2 + kstepB;
;     ...
;             PG8_LDB(B0, 0, 0); PG8_LDB(B1, 0, 1); PG8_SCHED; PG8_LDA(At, 0, 0); PG8_STAGE(PG8_SA(1, 1), a1, voffA[1]);
;             PG8_WAIT_V(8); PG8_WAIT_L(0); PG8_BAR; PG8_MMA(0, 0, At, B0); PG8_MMA(0, 1, At, B1); PG8_BAR; PG8_SCHED;
;             PG8_LDA(At, 0, 1); PG8_STAGE(PG8_SB(0, 0), b2, voffB[0]); PG8_STAGE(PG8_SB(0, 1), b2, voffB[1]); PG8_STAGE(PG8_SA(0, 0), a2, vA2[0]);
;             PG8_WAIT_V(8); PG8_WAIT_L(0); PG8_BAR; PG8_MMA(1, 0, At, B0); PG8_MMA(1, 1, At, B1); PG8_BAR; PG8_SCHED;
;             PG8_LDB(B0, 1, 0); PG8_LDB(B1, 1, 1); PG8_SCHED; PG8_LDA(At, 1, 0); PG8_STAGE(PG8_SA(0, 1), a2, vA2[1]);
;             PG8_WAIT_V(8); PG8_WAIT_L(0); PG8_BAR; PG8_MMA(0, 0, At, B0); PG8_MMA(0, 1, At, B1); PG8_BAR; PG8_SCHED;
;             PG8_LDA(At, 1, 1); PG8_STAGE(PG8_SB(1, 0), b3, voffB[0]); PG8_STAGE(PG8_SB(1, 1), b3, voffB[1]); PG8_STAGE(PG8_SA(1, 0), a3, vA2[0]);
;             PG8_WAIT_V(8); PG8_WAIT_L(0); PG8_BAR; PG8_MMA(1, 0, At, B0); PG8_MMA(1, 1, At, B1); PG8_BAR; PG8_SCHED;
	s_setprio 2
	v_mfma_scale_f32_16x16x128_f8f6f4 v[158:161], v[2:9], v[212:219], v[158:161], v210, v210 op_sel_hi:[0,0,0]
	v_mfma_scale_f32_16x16x128_f8f6f4 v[154:157], v[10:17], v[212:219], v[154:157], v210, v210 op_sel_hi:[0,0,0]
	v_mfma_scale_f32_16x16x128_f8f6f4 v[142:145], v[2:9], v[220:227], v[142:145], v210, v210 op_sel_hi:[0,0,0]
	v_mfma_scale_f32_16x16x128_f8f6f4 v[138:141], v[10:17], v[220:227], v[138:141], v210, v210 op_sel_hi:[0,0,0]
	v_mfma_scale_f32_16x16x128_f8f6f4 v[126:129], v[2:9], v[228:235], v[126:129], v210, v210 op_sel_hi:[0,0,0]
	v_mfma_scale_f32_16x16x128_f8f6f4 v[122:125], v[10:17], v[228:235], v[122:125], v210, v210 op_sel_hi:[0,0,0]
	v_mfma_scale_f32_16x16x128_f8f6f4 v[110:113], v[2:9], v[236:243], v[110:113], v210, v210 op_sel_hi:[0,0,0]
	v_mfma_scale_f32_16x16x128_f8f6f4 v[106:109], v[10:17], v[236:243], v[106:109], v210, v210 op_sel_hi:[0,0,0]
	s_nop 3
	s_setprio 0
	s_setprio 2
	v_mfma_scale_f32_16x16x128_f8f6f4 v[150:153], v[18:25], v[212:219], v[150:153], v210, v210 op_sel_hi:[0,0,0]
	v_mfma_scale_f32_16x16x128_f8f6f4 v[146:149], v[26:33], v[212:219], v[146:149], v210, v210 op_sel_hi:[0,0,0]
	v_mfma_scale_f32_16x16x128_f8f6f4 v[134:137], v[18:25], v[220:227], v[134:137], v210, v210 op_sel_hi:[0,0,0]
	v_mfma_scale_f32_16x16x128_f8f6f4 v[130:133], v[26:33], v[220:227], v[130:133], v210, v210 op_sel_hi:[0,0,0]
	v_mfma_scale_f32_16x16x128_f8f6f4 v[118:121], v[18:25], v[228:235], v[118:121], v210, v210 op_sel_hi:[0,0,0]
	v_mfma_scale_f32_16x16x128_f8f6f4 v[114:117], v[26:33], v[228:235], v[114:117], v210, v210 op_sel_hi:[0,0,0]
	v_mfma_scale_f32_16x16x128_f8f6f4 v[102:105], v[18:25], v[236:243], v[102:105], v210, v210 op_sel_hi:[0,0,0]
	v_mfma_scale_f32_16x16x128_f8f6f4 v[98:101], v[26:33], v[236:243], v[98:101], v210, v210 op_sel_hi:[0,0,0]
	s_setprio 0
	s_add_u32 s30, s30, 0x8000
	s_addc_u32 s31, s31, 0
	s_add_i32 s40, s67, s45
	v_lshl_add_u64 v[244:245], s[30:31], 0, v[164:165]
	s_mov_b32 m0, s40
	ds_read_b128 v[212:215], v209 offset:49152
	ds_read_b128 v[216:219], v209 offset:50176
	ds_read_b128 v[220:223], v209 offset:51200
	ds_read_b128 v[224:227], v209 offset:52224
	ds_read_b128 v[228:231], v209 offset:53248
	ds_read_b128 v[232:235], v209 offset:54272
	ds_read_b128 v[236:239], v209 offset:55296
	ds_read_b128 v[240:243], v209 offset:56320
	global_load_lds_dwordx4 v[244:245], off
	v_lshl_add_u64 v[244:245], s[30:31], 0, v[166:167]
	s_add_i32 m0, s40, 0x2000
	s_add_i32 s40, s68, s45
	global_load_lds_dwordx4 v[244:245], off
	v_lshl_add_u64 v[244:245], s[30:31], 0, v[168:169]
	s_mov_b32 m0, s40
	s_nop 0
	global_load_lds_dwordx4 v[244:245], off
	v_lshl_add_u64 v[244:245], s[30:31], 0, v[172:173]
	s_add_i32 m0, s40, 0x2000
	s_nop 0
	global_load_lds_dwordx4 v[244:245], off
	v_lshl_add_u64 v[244:245], s[28:29], 0, v[174:175]
	s_mov_b32 m0, s52
	s_nop 0
	global_load_lds_dwordx4 v[244:245], off
	v_lshl_add_u64 v[244:245], s[28:29], 0, v[176:177]
	s_mov_b32 m0, s53
	s_nop 0
	global_load_lds_dwordx4 v[244:245], off
	s_waitcnt vmcnt(8)
	s_waitcnt lgkmcnt(0)
	s_barrier
	s_setprio 2
	v_mfma_scale_f32_16x16x128_f8f6f4 v[94:97], v[2:9], v[212:219], v[94:97], v210, v210 op_sel_hi:[0,0,0]
	v_mfma_scale_f32_16x16x128_f8f6f4 v[90:93], v[10:17], v[212:219], v[90:93], v210, v210 op_sel_hi:[0,0,0]
	v_mfma_scale_f32_16x16x128_f8f6f4 v[78:81], v[2:9], v[220:227], v[78:81], v210, v210 op_sel_hi:[0,0,0]
	v_mfma_scale_f32_16x16x128_f8f6f4 v[74:77], v[10:17], v[220:227], v[74:77], v210, v210 op_sel_hi:[0,0,0]
	v_mfma_scale_f32_16x16x128_f8f6f4 v[62:65], v[2:9], v[228:235], v[62:65], v210, v210 op_sel_hi:[0,0,0]
	v_mfma_scale_f32_16x16x128_f8f6f4 v[58:61], v[10:17], v[228:235], v[58:61], v210, v210 op_sel_hi:[0,0,0]
	v_mfma_scale_f32_16x16x128_f8f6f4 v[46:49], v[2:9], v[236:243], v[46:49], v210, v210 op_sel_hi:[0,0,0]
	v_mfma_scale_f32_16x16x128_f8f6f4 v[42:45], v[10:17], v[236:243], v[42:45], v210, v210 op_sel_hi:[0,0,0]
	s_nop 3
	s_setprio 0
	s_setprio 2
	v_mfma_scale_f32_16x16x128_f8f6f4 v[86:89], v[18:25], v[212:219], v[86:89], v210, v210 op_sel_hi:[0,0,0]
	v_mfma_scale_f32_16x16x128_f8f6f4 v[82:85], v[26:33], v[212:219], v[82:85], v210, v210 op_sel_hi:[0,0,0]
	v_mfma_scale_f32_16x16x128_f8f6f4 v[70:73], v[18:25], v[220:227], v[70:73], v210, v210 op_sel_hi:[0,0,0]
	v_mfma_scale_f32_16x16x128_f8f6f4 v[66:69], v[26:33], v[220:227], v[66:69], v210, v210 op_sel_hi:[0,0,0]
	v_mfma_scale_f32_16x16x128_f8f6f4 v[54:57], v[18:25], v[228:235], v[54:57], v210, v210 op_sel_hi:[0,0,0]
	v_mfma_scale_f32_16x16x128_f8f6f4 v[50:53], v[26:33], v[228:235], v[50:53], v210, v210 op_sel_hi:[0,0,0]
	v_mfma_scale_f32_16x16x128_f8f6f4 v[38:41], v[18:25], v[236:243], v[38:41], v210, v210 op_sel_hi:[0,0,0]
	v_mfma_scale_f32_16x16x128_f8f6f4 v[34:37], v[26:33], v[236:243], v[34:37], v210, v210 op_sel_hi:[0,0,0]
	s_setprio 0
	s_add_i32 s21, s21, 2
	s_add_u32 s5, s5, 0x10000
	s_addc_u32 s19, s19, 0
	s_add_u32 s26, s26, 0x10000
	s_addc_u32 s27, s27, 0
	s_cmp_gt_u32 s21, 13
	s_cbranch_scc0 .Lh1_372

; #define PG8_STAGE(bufoff, gbase, voff) do { _Pragma("unroll") for (int _i = 0; _i < 2; ++_i) \
;         __builtin_amdgcn_global_load_lds((const unsigned*)((const char*)(gbase) + (voff)[_i]), (PG8_LAS unsigned*)(lds + (bufoff) + ldsw + _i * 8192), 16, 0, 0); } while (0)
; #define PG8_WAIT_V(n) asm volatile("s_waitcnt vmcnt(" #n ")" ::: "memory")
; #define PG8_WAIT_L(n) asm volatile("s_waitcnt lgkmcnt(" #n ")" ::: "memory")
; #define PG8_BAR __builtin_amdgcn_s_barrier()
; #define PG8_SCHED __builtin_amdgcn_sched_barrier(0)
; template <class Epi, class Sched, bool ALIGN_EPI = true, bool F8 = false>
; __device__ __forceinline__ void gemm_phase(PG8_LAS unsigned char* lds, const Sched& S, const Epi& E) {
;     ...
;             PG8_LDB(B0, 0, 0); PG8_LDB(B1, 0, 1); PG8_SCHED; PG8_LDA(At, 0, 0); PG8_STAGE(PG8_SA(1, 1), a1, voffA[1]);
;             PG8_WAIT_V(8); PG8_WAIT_L(0); PG8_BAR; PG8_MMA(0, 0, At, B0); PG8_MMA(0, 1, At, B1); PG8_BAR; PG8_SCHED;
;             PG8_LDA(At, 0, 1); PG8_STAGE(PG8_SB(0, 0), b2, voffB[0]); PG8_STAGE(PG8_SB(0, 1), b2, voffB[1]); PG8_STAGE(PG8_SA(0, 0), a2, vA2[0]);
;             PG8_WAIT_V(8); PG8_WAIT_L(0); PG8_BAR; PG8_MMA(1, 0, At, B0); PG8_MMA(1, 1, At, B1); PG8_BAR; PG8_SCHED;
;             PG8_LDB(B0, 1, 0); PG8_LDB(B1, 1, 1); PG8_SCHED; PG8_LDA(At, 1, 0); PG8_STAGE(PG8_SA(0, 1), a2, vA2[1]);
;             PG8_WAIT_V(8); PG8_WAIT_L(0); PG8_BAR; PG8_MMA(0, 0, At, B0); PG8_MMA(0, 1, At, B1); PG8_BAR; PG8_SCHED;
;             PG8_LDA(At, 1, 1); PG8_STAGE(PG8_SB(1, 0), b3, voffB[0]); PG8_STAGE(PG8_SB(1, 1), b3, voffB[1]); PG8_STAGE(PG8_SA(1, 0), a3, vA2[0]);
;             PG8_WAIT_V(8); PG8_WAIT_L(0); PG8_BAR; PG8_MMA(1, 0, At, B0); PG8_MMA(1, 1, At, B1); PG8_BAR; PG8_SCHED;
.LBB0_428:
	ds_read_b128 v[18:21], v192
	ds_read_b128 v[22:25], v192 offset:1024
	ds_read_b128 v[26:29], v192 offset:2048
	ds_read_b128 v[30:33], v192 offset:3072
	ds_read_b128 v[2:5], v193
	ds_read_b128 v[6:9], v193 offset:1024
	ds_read_b128 v[10:13], v193 offset:2048
	ds_read_b128 v[14:17], v193 offset:3072
	s_add_u32 s26, s24, 0x8000
	s_addc_u32 s27, s25, 0
	s_cmp_eq_u32 s74, 12
	s_cselect_b32 s30, s20, s26
	s_cselect_b32 s31, s21, s27
	s_cselect_b32 s28, s22, s17
	s_cselect_b32 s29, s23, s19
	s_add_u32 s26, s30, 0x8000
	s_addc_u32 s27, s31, 0
	v_lshl_add_u64 v[230:231], s[24:25], 0, v[184:185]
	s_add_i32 m0, s48, 0xc000
	ds_read_b128 v[198:201], v194
	ds_read_b128 v[202:205], v194 offset:1024
	ds_read_b128 v[206:209], v194 offset:2048
	ds_read_b128 v[210:213], v194 offset:3072
	ds_read_b128 v[214:217], v194 offset:4096
	ds_read_b128 v[218:221], v194 offset:5120
	ds_read_b128 v[222:225], v194 offset:6144
	ds_read_b128 v[226:229], v194 offset:7168
	global_load_lds_dwordx4 v[230:231], off
	v_lshl_add_u64 v[230:231], s[24:25], 0, v[182:183]
	s_add_i32 m0, s48, 0xe000
	s_nop 0
	global_load_lds_dwordx4 v[230:231], off
	s_waitcnt vmcnt(8)
	s_waitcnt lgkmcnt(0)
	s_setprio 1
	v_mfma_scale_f32_16x16x128_f8f6f4 v[158:161], v[18:25], v[198:205], v[158:161], v195, v195 op_sel_hi:[0,0,0]
	v_mfma_scale_f32_16x16x128_f8f6f4 v[154:157], v[26:33], v[198:205], v[154:157], v195, v195 op_sel_hi:[0,0,0]
	v_mfma_scale_f32_16x16x128_f8f6f4 v[142:145], v[18:25], v[206:213], v[142:145], v195, v195 op_sel_hi:[0,0,0]
	v_mfma_scale_f32_16x16x128_f8f6f4 v[138:141], v[26:33], v[206:213], v[138:141], v195, v195 op_sel_hi:[0,0,0]
	v_mfma_scale_f32_16x16x128_f8f6f4 v[126:129], v[18:25], v[214:221], v[126:129], v195, v195 op_sel_hi:[0,0,0]
	v_mfma_scale_f32_16x16x128_f8f6f4 v[122:125], v[26:33], v[214:221], v[122:125], v195, v195 op_sel_hi:[0,0,0]
	v_mfma_scale_f32_16x16x128_f8f6f4 v[110:113], v[18:25], v[222:229], v[110:113], v195, v195 op_sel_hi:[0,0,0]
	v_mfma_scale_f32_16x16x128_f8f6f4 v[106:109], v[26:33], v[222:229], v[106:109], v195, v195 op_sel_hi:[0,0,0]
	s_nop 3
	s_setprio 0
	s_setprio 1
	v_mfma_scale_f32_16x16x128_f8f6f4 v[150:153], v[2:9], v[198:205], v[150:153], v195, v195 op_sel_hi:[0,0,0]
	v_mfma_scale_f32_16x16x128_f8f6f4 v[146:149], v[10:17], v[198:205], v[146:149], v195, v195 op_sel_hi:[0,0,0]
	v_mfma_scale_f32_16x16x128_f8f6f4 v[134:137], v[2:9], v[206:213], v[134:137], v195, v195 op_sel_hi:[0,0,0]
	v_mfma_scale_f32_16x16x128_f8f6f4 v[130:133], v[10:17], v[206:213], v[130:133], v195, v195 op_sel_hi:[0,0,0]
	v_mfma_scale_f32_16x16x128_f8f6f4 v[118:121], v[2:9], v[214:221], v[118:121], v195, v195 op_sel_hi:[0,0,0]
	v_mfma_scale_f32_16x16x128_f8f6f4 v[114:117], v[10:17], v[214:221], v[114:117], v195, v195 op_sel_hi:[0,0,0]
	v_mfma_scale_f32_16x16x128_f8f6f4 v[102:105], v[2:9], v[222:229], v[102:105], v195, v195 op_sel_hi:[0,0,0]
	v_mfma_scale_f32_16x16x128_f8f6f4 v[98:101], v[10:17], v[222:229], v[98:101], v195, v195 op_sel_hi:[0,0,0]
	s_setprio 0
	s_barrier
	s_add_i32 s75, s65, s47
	v_lshl_add_u64 v[230:231], s[28:29], 0, v[164:165]
	s_mov_b32 m0, s75
	ds_read_b128 v[198:201], v194 offset:16384
	ds_read_b128 v[202:205], v194 offset:17408
	ds_read_b128 v[206:209], v194 offset:18432
	ds_read_b128 v[210:213], v194 offset:19456
	ds_read_b128 v[214:217], v194 offset:20480
	ds_read_b128 v[218:221], v194 offset:21504
	ds_read_b128 v[222:225], v194 offset:22528
	ds_read_b128 v[226:229], v194 offset:23552
	global_load_lds_dwordx4 v[230:231], off
	v_lshl_add_u64 v[232:233], s[28:29], 0, v[166:167]
	s_add_i32 m0, s75, 0x2000
	s_add_i32 s75, s66, s47
	global_load_lds_dwordx4 v[232:233], off
	v_lshl_add_u64 v[230:231], v[230:231], 0, s[4:5]
	s_mov_b32 m0, s75
	s_nop 0
	global_load_lds_dwordx4 v[230:231], off
	v_lshl_add_u64 v[230:231], v[232:233], 0, s[4:5]
	s_add_i32 m0, s75, 0x2000
	s_nop 0
	global_load_lds_dwordx4 v[230:231], off
	v_lshl_add_u64 v[230:231], s[30:31], 0, v[174:175]
	s_mov_b32 m0, s48
	s_nop 0
	global_load_lds_dwordx4 v[230:231], off
	v_lshl_add_u64 v[230:231], s[30:31], 0, v[176:177]
	s_mov_b32 m0, s49
	s_nop 0
	global_load_lds_dwordx4 v[230:231], off
	s_waitcnt vmcnt(8)
	s_waitcnt lgkmcnt(0)
	s_setprio 1
	v_mfma_scale_f32_16x16x128_f8f6f4 v[94:97], v[18:25], v[198:205], v[94:97], v195, v195 op_sel_hi:[0,0,0]
	v_mfma_scale_f32_16x16x128_f8f6f4 v[90:93], v[26:33], v[198:205], v[90:93], v195, v195 op_sel_hi:[0,0,0]
	v_mfma_scale_f32_16x16x128_f8f6f4 v[78:81], v[18:25], v[206:213], v[78:81], v195, v195 op_sel_hi:[0,0,0]
	v_mfma_scale_f32_16x16x128_f8f6f4 v[74:77], v[26:33], v[206:213], v[74:77], v195, v195 op_sel_hi:[0,0,0]
	v_mfma_scale_f32_16x16x128_f8f6f4 v[62:65], v[18:25], v[214:221], v[62:65], v195, v195 op_sel_hi:[0,0,0]
	v_mfma_scale_f32_16x16x128_f8f6f4 v[58:61], v[26:33], v[214:221], v[58:61], v195, v195 op_sel_hi:[0,0,0]
	v_mfma_scale_f32_16x16x128_f8f6f4 v[46:49], v[18:25], v[222:229], v[46:49], v195, v195 op_sel_hi:[0,0,0]
	v_mfma_scale_f32_16x16x128_f8f6f4 v[42:45], v[26:33], v[222:229], v[42:45], v195, v195 op_sel_hi:[0,0,0]
	s_nop 3
	s_setprio 0
	s_setprio 1
	v_mfma_scale_f32_16x16x128_f8f6f4 v[86:89], v[2:9], v[198:205], v[86:89], v195, v195 op_sel_hi:[0,0,0]
	v_mfma_scale_f32_16x16x128_f8f6f4 v[82:85], v[10:17], v[198:205], v[82:85], v195, v195 op_sel_hi:[0,0,0]
	v_mfma_scale_f32_16x16x128_f8f6f4 v[70:73], v[2:9], v[206:213], v[70:73], v195, v195 op_sel_hi:[0,0,0]
	v_mfma_scale_f32_16x16x128_f8f6f4 v[66:69], v[10:17], v[206:213], v[66:69], v195, v195 op_sel_hi:[0,0,0]
	v_mfma_scale_f32_16x16x128_f8f6f4 v[54:57], v[2:9], v[214:221], v[54:57], v195, v195 op_sel_hi:[0,0,0]
	v_mfma_scale_f32_16x16x128_f8f6f4 v[50:53], v[10:17], v[214:221], v[50:53], v195, v195 op_sel_hi:[0,0,0]
	v_mfma_scale_f32_16x16x128_f8f6f4 v[38:41], v[2:9], v[222:229], v[38:41], v195, v195 op_sel_hi:[0,0,0]
	v_mfma_scale_f32_16x16x128_f8f6f4 v[34:37], v[10:17], v[222:229], v[34:37], v195, v195 op_sel_hi:[0,0,0]
	s_setprio 0
	s_barrier
; #define PG8_STAGE(bufoff, gbase, voff) do { _Pragma("unroll") for (int _i = 0; _i < 2; ++_i) \
;         __builtin_amdgcn_global_load_lds((const unsigned*)((const char*)(gbase) + (voff)[_i]), (PG8_LAS unsigned*)(lds + (bufoff) + ldsw + _i * 8192), 16, 0, 0); } while (0)
; #define PG8_WAIT_V(n) asm volatile("s_waitcnt vmcnt(" #n ")" ::: "memory")
; #define PG8_WAIT_L(n) asm volatile("s_waitcnt lgkmcnt(" #n ")" ::: "memory")
; #define PG8_BAR __builtin_amdgcn_s_barrier()
; #define PG8_SCHED __builtin_amdgcn_sched_barrier(0)
; template <class Epi, class Sched, bool ALIGN_EPI = true, bool F8 = false>
; __device__ __forceinline__ void gemm_phase(PG8_LAS unsigned char* lds, const Sched& S, const Epi& E) {
;     ...
;         for (int t = 0; t < nt; t += 2) {
;             const bool last = (t == nt - 2);
;             if constexpr (Sched::GATHER) { if (last && has_next) S.a_off(nxt, Rs, Cs, voffAn); }
;             const char* a1 = cA + (size_t)(t + 1) * kstep;
;             const char* a2 = last ? nA : cA + (size_t)(t + 2) * kstep; const char* b2 = last ? nB : cB + (size_t)(t + 2) * kstepB;
;             const char* a3 = a2 + kstep; const char* b3 = b2 + kstepB;
;     ...
;             PG8_LDB(B0, 0, 0); PG8_LDB(B1, 0, 1); PG8_SCHED; PG8_LDA(At, 0, 0); PG8_STAGE(PG8_SA(1, 1), a1, voffA[1]);
;             PG8_WAIT_V(8); PG8_WAIT_L(0); PG8_BAR; PG8_MMA(0, 0, At, B0); PG8_MMA(0, 1, At, B1); PG8_BAR; PG8_SCHED;
;             PG8_LDA(At, 0, 1); PG8_STAGE(PG8_SB(0, 0), b2, voffB[0]); PG8_STAGE(PG8_SB(0, 1), b2, voffB[1]); PG8_STAGE(PG8_SA(0, 0), a2, vA2[0]);
;             PG8_WAIT_V(8); PG8_WAIT_L(0); PG8_BAR; PG8_MMA(1, 0, At, B0); PG8_MMA(1, 1, At, B1); PG8_BAR; PG8_SCHED;
;             PG8_LDB(B0, 1, 0); PG8_LDB(B1, 1, 1); PG8_SCHED; PG8_LDA(At, 1, 0); PG8_STAGE(PG8_SA(0, 1), a2, vA2[1]);
;             PG8_WAIT_V(8); PG8_WAIT_L(0); PG8_BAR; PG8_MMA(0, 0, At, B0); PG8_MMA(0, 1, At, B1); PG8_BAR; PG8_SCHED;
;             PG8_LDA(At, 1, 1); PG8_STAGE(PG8_SB(1, 0), b3, voffB[0]); PG8_STAGE(PG8_SB(1, 1), b3, voffB[1]); PG8_STAGE(PG8_SA(1, 0), a3, vA2[0]);
;             PG8_WAIT_V(8); PG8_WAIT_L(0); PG8_BAR; PG8_MMA(1, 0, At, B0); PG8_MMA(1, 1, At, B1); PG8_BAR; PG8_SCHED;
	s_add_i32 s75, 0, 0x18000
	s_add_i32 s76, 0, 0x1c000
	v_add_u32_e32 v14, s75, v191
	v_add_u32_e32 v30, s76, v191
	ds_read_b128 v[2:5], v14
	ds_read_b128 v[6:9], v14 offset:1024
	ds_read_b128 v[10:13], v14 offset:2048
	ds_read_b128 v[14:17], v14 offset:3072
	ds_read_b128 v[18:21], v30
	ds_read_b128 v[22:25], v30 offset:1024
	ds_read_b128 v[26:29], v30 offset:2048
	ds_read_b128 v[30:33], v30 offset:3072
	s_mov_b32 m0, s50
	v_lshl_add_u64 v[230:231], s[30:31], 0, v[178:179]
	ds_read_b128 v[198:201], v194 offset:32768
	ds_read_b128 v[202:205], v194 offset:33792
	ds_read_b128 v[206:209], v194 offset:34816
	ds_read_b128 v[210:213], v194 offset:35840
	ds_read_b128 v[214:217], v194 offset:36864
	ds_read_b128 v[218:221], v194 offset:37888
	ds_read_b128 v[222:225], v194 offset:38912
	ds_read_b128 v[226:229], v194 offset:39936
	global_load_lds_dwordx4 v[230:231], off
	v_lshl_add_u64 v[230:231], s[30:31], 0, v[180:181]
	s_mov_b32 m0, s51
	s_nop 0
	global_load_lds_dwordx4 v[230:231], off
	s_waitcnt vmcnt(8)
	s_waitcnt lgkmcnt(0)
	s_setprio 1
	v_mfma_scale_f32_16x16x128_f8f6f4 v[158:161], v[2:9], v[198:205], v[158:161], v195, v195 op_sel_hi:[0,0,0]
	v_mfma_scale_f32_16x16x128_f8f6f4 v[154:157], v[10:17], v[198:205], v[154:157], v195, v195 op_sel_hi:[0,0,0]
	v_mfma_scale_f32_16x16x128_f8f6f4 v[142:145], v[2:9], v[206:213], v[142:145], v195, v195 op_sel_hi:[0,0,0]
	v_mfma_scale_f32_16x16x128_f8f6f4 v[138:141], v[10:17], v[206:213], v[138:141], v195, v195 op_sel_hi:[0,0,0]
	v_mfma_scale_f32_16x16x128_f8f6f4 v[126:129], v[2:9], v[214:221], v[126:129], v195, v195 op_sel_hi:[0,0,0]
	v_mfma_scale_f32_16x16x128_f8f6f4 v[122:125], v[10:17], v[214:221], v[122:125], v195, v195 op_sel_hi:[0,0,0]
	v_mfma_scale_f32_16x16x128_f8f6f4 v[110:113], v[2:9], v[222:229], v[110:113], v195, v195 op_sel_hi:[0,0,0]
	v_mfma_scale_f32_16x16x128_f8f6f4 v[106:109], v[10:17], v[222:229], v[106:109], v195, v195 op_sel_hi:[0,0,0]
	s_nop 3
	s_setprio 0
	s_setprio 1
	v_mfma_scale_f32_16x16x128_f8f6f4 v[150:153], v[18:25], v[198:205], v[150:153], v195, v195 op_sel_hi:[0,0,0]
	v_mfma_scale_f32_16x16x128_f8f6f4 v[146:149], v[26:33], v[198:205], v[146:149], v195, v195 op_sel_hi:[0,0,0]
	v_mfma_scale_f32_16x16x128_f8f6f4 v[134:137], v[18:25], v[206:213], v[134:137], v195, v195 op_sel_hi:[0,0,0]
	v_mfma_scale_f32_16x16x128_f8f6f4 v[130:133], v[26:33], v[206:213], v[130:133], v195, v195 op_sel_hi:[0,0,0]
	v_mfma_scale_f32_16x16x128_f8f6f4 v[118:121], v[18:25], v[214:221], v[118:121], v195, v195 op_sel_hi:[0,0,0]
	v_mfma_scale_f32_16x16x128_f8f6f4 v[114:117], v[26:33], v[214:221], v[114:117], v195, v195 op_sel_hi:[0,0,0]
	v_mfma_scale_f32_16x16x128_f8f6f4 v[102:105], v[18:25], v[222:229], v[102:105], v195, v195 op_sel_hi:[0,0,0]
	v_mfma_scale_f32_16x16x128_f8f6f4 v[98:101], v[26:33], v[222:229], v[98:101], v195, v195 op_sel_hi:[0,0,0]
	s_setprio 0
	s_barrier
	s_add_u32 s28, s28, 0x8000
	s_addc_u32 s29, s29, 0
	s_add_i32 s30, s75, s47
	v_lshl_add_u64 v[230:231], s[28:29], 0, v[164:165]
	s_mov_b32 m0, s30
	ds_read_b128 v[198:201], v194 offset:49152
	ds_read_b128 v[202:205], v194 offset:50176
	ds_read_b128 v[206:209], v194 offset:51200
	ds_read_b128 v[210:213], v194 offset:52224
	ds_read_b128 v[214:217], v194 offset:53248
	ds_read_b128 v[218:221], v194 offset:54272
	ds_read_b128 v[222:225], v194 offset:55296
	ds_read_b128 v[226:229], v194 offset:56320
	global_load_lds_dwordx4 v[230:231], off
	v_lshl_add_u64 v[230:231], s[28:29], 0, v[166:167]
	s_add_i32 m0, s30, 0x2000
	s_add_i32 s30, s76, s47
	global_load_lds_dwordx4 v[230:231], off
	v_lshl_add_u64 v[230:231], s[28:29], 0, v[168:169]
	s_mov_b32 m0, s30
	s_nop 0
	global_load_lds_dwordx4 v[230:231], off
	v_lshl_add_u64 v[230:231], s[28:29], 0, v[172:173]
	s_add_i32 m0, s30, 0x2000
	s_nop 0
	global_load_lds_dwordx4 v[230:231], off
	v_lshl_add_u64 v[230:231], s[26:27], 0, v[174:175]
	s_mov_b32 m0, s60
	s_nop 0
	global_load_lds_dwordx4 v[230:231], off
	v_lshl_add_u64 v[230:231], s[26:27], 0, v[176:177]
	s_mov_b32 m0, s61
	s_nop 0
	global_load_lds_dwordx4 v[230:231], off
	s_waitcnt vmcnt(8)
	s_waitcnt lgkmcnt(0)
	s_setprio 1
	v_mfma_scale_f32_16x16x128_f8f6f4 v[94:97], v[2:9], v[198:205], v[94:97], v195, v195 op_sel_hi:[0,0,0]
	v_mfma_scale_f32_16x16x128_f8f6f4 v[90:93], v[10:17], v[198:205], v[90:93], v195, v195 op_sel_hi:[0,0,0]
	v_mfma_scale_f32_16x16x128_f8f6f4 v[78:81], v[2:9], v[206:213], v[78:81], v195, v195 op_sel_hi:[0,0,0]
	v_mfma_scale_f32_16x16x128_f8f6f4 v[74:77], v[10:17], v[206:213], v[74:77], v195, v195 op_sel_hi:[0,0,0]
	v_mfma_scale_f32_16x16x128_f8f6f4 v[62:65], v[2:9], v[214:221], v[62:65], v195, v195 op_sel_hi:[0,0,0]
	v_mfma_scale_f32_16x16x128_f8f6f4 v[58:61], v[10:17], v[214:221], v[58:61], v195, v195 op_sel_hi:[0,0,0]
	v_mfma_scale_f32_16x16x128_f8f6f4 v[46:49], v[2:9], v[222:229], v[46:49], v195, v195 op_sel_hi:[0,0,0]
	v_mfma_scale_f32_16x16x128_f8f6f4 v[42:45], v[10:17], v[222:229], v[42:45], v195, v195 op_sel_hi:[0,0,0]
	s_nop 3
	s_setprio 0
	s_setprio 1
	v_mfma_scale_f32_16x16x128_f8f6f4 v[86:89], v[18:25], v[198:205], v[86:89], v195, v195 op_sel_hi:[0,0,0]
	v_mfma_scale_f32_16x16x128_f8f6f4 v[82:85], v[26:33], v[198:205], v[82:85], v195, v195 op_sel_hi:[0,0,0]
	v_mfma_scale_f32_16x16x128_f8f6f4 v[70:73], v[18:25], v[206:213], v[70:73], v195, v195 op_sel_hi:[0,0,0]
	v_mfma_scale_f32_16x16x128_f8f6f4 v[66:69], v[26:33], v[206:213], v[66:69], v195, v195 op_sel_hi:[0,0,0]
	v_mfma_scale_f32_16x16x128_f8f6f4 v[54:57], v[18:25], v[214:221], v[54:57], v195, v195 op_sel_hi:[0,0,0]
	v_mfma_scale_f32_16x16x128_f8f6f4 v[50:53], v[26:33], v[214:221], v[50:53], v195, v195 op_sel_hi:[0,0,0]
	v_mfma_scale_f32_16x16x128_f8f6f4 v[38:41], v[18:25], v[222:229], v[38:41], v195, v195 op_sel_hi:[0,0,0]
	v_mfma_scale_f32_16x16x128_f8f6f4 v[34:37], v[26:33], v[222:229], v[34:37], v195, v195 op_sel_hi:[0,0,0]
	s_setprio 0
	s_barrier
	s_add_i32 s74, s74, 2
	s_add_u32 s17, s17, 0x10000
	s_addc_u32 s19, s19, 0
	s_add_u32 s24, s24, 0x10000
	s_addc_u32 s25, s25, 0
	s_cmp_gt_u32 s74, 13
	s_cbranch_scc0 .LBB0_428
	s_branch .Lfx_11141
; #define PG8_STAGE(bufoff, gbase, voff) do { _Pragma("unroll") for (int _i = 0; _i < 2; ++_i) \
;         __builtin_amdgcn_global_load_lds((const unsigned*)((const char*)(gbase) + (voff)[_i]), (PG8_LAS unsigned*)(lds + (bufoff) + ldsw + _i * 8192), 16, 0, 0); } while (0)
; #define PG8_WAIT_V(n) asm volatile("s_waitcnt vmcnt(" #n ")" ::: "memory")
; #define PG8_WAIT_L(n) asm volatile("s_waitcnt lgkmcnt(" #n ")" ::: "memory")
; #define PG8_BAR __builtin_amdgcn_s_barrier()
; #define PG8_SCHED __builtin_amdgcn_sched_barrier(0)
; template <class Epi, class Sched, bool ALIGN_EPI = true, bool F8 = false>
; __device__ __forceinline__ void gemm_phase(PG8_LAS unsigned char* lds, const Sched& S, const Epi& E) {
;     ...
;             PG8_LDB(B0, 0, 0); PG8_LDB(B1, 0, 1); PG8_SCHED; PG8_LDA(At, 0, 0); PG8_STAGE(PG8_SA(1, 1), a1, voffA[1]);
;             PG8_WAIT_V(8); PG8_WAIT_L(0); PG8_BAR; PG8_MMA(0, 0, At, B0); PG8_MMA(0, 1, At, B1); PG8_BAR; PG8_SCHED;
;             PG8_LDA(At, 0, 1); PG8_STAGE(PG8_SB(0, 0), b2, voffB[0]); PG8_STAGE(PG8_SB(0, 1), b2, voffB[1]); PG8_STAGE(PG8_SA(0, 0), a2, vA2[0]);
;             PG8_WAIT_V(8); PG8_WAIT_L(0); PG8_BAR; PG8_MMA(1, 0, At, B0); PG8_MMA(1, 1, At, B1); PG8_BAR; PG8_SCHED;
;             PG8_LDB(B0, 1, 0); PG8_LDB(B1, 1, 1); PG8_SCHED; PG8_LDA(At, 1, 0); PG8_STAGE(PG8_SA(0, 1), a2, vA2[1]);
;             PG8_WAIT_V(8); PG8_WAIT_L(0); PG8_BAR; PG8_MMA(0, 0, At, B0); PG8_MMA(0, 1, At, B1); PG8_BAR; PG8_SCHED;
;             PG8_LDA(At, 1, 1); PG8_STAGE(PG8_SB(1, 0), b3, voffB[0]); PG8_STAGE(PG8_SB(1, 1), b3, voffB[1]); PG8_STAGE(PG8_SA(1, 0), a3, vA2[0]);
;             PG8_WAIT_V(8); PG8_WAIT_L(0); PG8_BAR; PG8_MMA(1, 0, At, B0); PG8_MMA(1, 1, At, B1); PG8_BAR; PG8_SCHED;
.Lh1e_11141:
.Lh1_428:
	ds_read_b128 v[18:21], v192
	ds_read_b128 v[22:25], v192 offset:1024
	ds_read_b128 v[26:29], v192 offset:2048
	ds_read_b128 v[30:33], v192 offset:3072
	ds_read_b128 v[2:5], v193
	ds_read_b128 v[6:9], v193 offset:1024
	ds_read_b128 v[10:13], v193 offset:2048
	ds_read_b128 v[14:17], v193 offset:3072
	s_add_u32 s26, s24, 0x8000
	s_addc_u32 s27, s25, 0
	s_cmp_eq_u32 s74, 12
	s_cselect_b32 s30, s20, s26
	s_cselect_b32 s31, s21, s27
	s_cselect_b32 s28, s22, s17
	s_cselect_b32 s29, s23, s19
	s_add_u32 s26, s30, 0x8000
	s_addc_u32 s27, s31, 0
	v_lshl_add_u64 v[230:231], s[24:25], 0, v[184:185]
	s_add_i32 m0, s48, 0xc000
	ds_read_b128 v[198:201], v194
	ds_read_b128 v[202:205], v194 offset:1024
	ds_read_b128 v[206:209], v194 offset:2048
	ds_read_b128 v[210:213], v194 offset:3072
	ds_read_b128 v[214:217], v194 offset:4096
	ds_read_b128 v[218:221], v194 offset:5120
	ds_read_b128 v[222:225], v194 offset:6144
	ds_read_b128 v[226:229], v194 offset:7168
	global_load_lds_dwordx4 v[230:231], off
	v_lshl_add_u64 v[230:231], s[24:25], 0, v[182:183]
	s_add_i32 m0, s48, 0xe000
	s_nop 0
	global_load_lds_dwordx4 v[230:231], off
	s_waitcnt vmcnt(8)
	s_waitcnt lgkmcnt(0)
	s_barrier
	s_setprio 2
	v_mfma_scale_f32_16x16x128_f8f6f4 v[158:161], v[18:25], v[198:205], v[158:161], v195, v195 op_sel_hi:[0,0,0]
	v_mfma_scale_f32_16x16x128_f8f6f4 v[154:157], v[26:33], v[198:205], v[154:157], v195, v195 op_sel_hi:[0,0,0]
	v_mfma_scale_f32_16x16x128_f8f6f4 v[142:145], v[18:25], v[206:213], v[142:145], v195, v195 op_sel_hi:[0,0,0]
	v_mfma_scale_f32_16x16x128_f8f6f4 v[138:141], v[26:33], v[206:213], v[138:141], v195, v195 op_sel_hi:[0,0,0]
	v_mfma_scale_f32_16x16x128_f8f6f4 v[126:129], v[18:25], v[214:221], v[126:129], v195, v195 op_sel_hi:[0,0,0]
	v_mfma_scale_f32_16x16x128_f8f6f4 v[122:125], v[26:33], v[214:221], v[122:125], v195, v195 op_sel_hi:[0,0,0]
	v_mfma_scale_f32_16x16x128_f8f6f4 v[110:113], v[18:25], v[222:229], v[110:113], v195, v195 op_sel_hi:[0,0,0]
	v_mfma_scale_f32_16x16x128_f8f6f4 v[106:109], v[26:33], v[222:229], v[106:109], v195, v195 op_sel_hi:[0,0,0]
	s_nop 3
	s_setprio 0
	s_setprio 2
	v_mfma_scale_f32_16x16x128_f8f6f4 v[150:153], v[2:9], v[198:205], v[150:153], v195, v195 op_sel_hi:[0,0,0]
	v_mfma_scale_f32_16x16x128_f8f6f4 v[146:149], v[10:17], v[198:205], v[146:149], v195, v195 op_sel_hi:[0,0,0]
	v_mfma_scale_f32_16x16x128_f8f6f4 v[134:137], v[2:9], v[206:213], v[134:137], v195, v195 op_sel_hi:[0,0,0]
	v_mfma_scale_f32_16x16x128_f8f6f4 v[130:133], v[10:17], v[206:213], v[130:133], v195, v195 op_sel_hi:[0,0,0]
	v_mfma_scale_f32_16x16x128_f8f6f4 v[118:121], v[2:9], v[214:221], v[118:121], v195, v195 op_sel_hi:[0,0,0]
	v_mfma_scale_f32_16x16x128_f8f6f4 v[114:117], v[10:17], v[214:221], v[114:117], v195, v195 op_sel_hi:[0,0,0]
	v_mfma_scale_f32_16x16x128_f8f6f4 v[102:105], v[2:9], v[222:229], v[102:105], v195, v195 op_sel_hi:[0,0,0]
	v_mfma_scale_f32_16x16x128_f8f6f4 v[98:101], v[10:17], v[222:229], v[98:101], v195, v195 op_sel_hi:[0,0,0]
	s_setprio 0
	s_add_i32 s75, s65, s47
	v_lshl_add_u64 v[230:231], s[28:29], 0, v[164:165]
	s_mov_b32 m0, s75
	ds_read_b128 v[198:201], v194 offset:16384
	ds_read_b128 v[202:205], v194 offset:17408
	ds_read_b128 v[206:209], v194 offset:18432
	ds_read_b128 v[210:213], v194 offset:19456
	ds_read_b128 v[214:217], v194 offset:20480
	ds_read_b128 v[218:221], v194 offset:21504
	ds_read_b128 v[222:225], v194 offset:22528
	ds_read_b128 v[226:229], v194 offset:23552
	global_load_lds_dwordx4 v[230:231], off
	v_lshl_add_u64 v[232:233], s[28:29], 0, v[166:167]
	s_add_i32 m0, s75, 0x2000
	s_add_i32 s75, s66, s47
	global_load_lds_dwordx4 v[232:233], off
	v_lshl_add_u64 v[230:231], v[230:231], 0, s[4:5]
	s_mov_b32 m0, s75
	s_nop 0
	global_load_lds_dwordx4 v[230:231], off
	v_lshl_add_u64 v[230:231], v[232:233], 0, s[4:5]
	s_add_i32 m0, s75, 0x2000
	s_nop 0
	global_load_lds_dwordx4 v[230:231], off
	v_lshl_add_u64 v[230:231], s[30:31], 0, v[174:175]
	s_mov_b32 m0, s48
	s_nop 0
	global_load_lds_dwordx4 v[230:231], off
	v_lshl_add_u64 v[230:231], s[30:31], 0, v[176:177]
	s_mov_b32 m0, s49
	s_nop 0
	global_load_lds_dwordx4 v[230:231], off
	s_waitcnt vmcnt(8)
	s_waitcnt lgkmcnt(0)
	s_barrier
	s_setprio 2
	v_mfma_scale_f32_16x16x128_f8f6f4 v[94:97], v[18:25], v[198:205], v[94:97], v195, v195 op_sel_hi:[0,0,0]
	v_mfma_scale_f32_16x16x128_f8f6f4 v[90:93], v[26:33], v[198:205], v[90:93], v195, v195 op_sel_hi:[0,0,0]
	v_mfma_scale_f32_16x16x128_f8f6f4 v[78:81], v[18:25], v[206:213], v[78:81], v195, v195 op_sel_hi:[0,0,0]
	v_mfma_scale_f32_16x16x128_f8f6f4 v[74:77], v[26:33], v[206:213], v[74:77], v195, v195 op_sel_hi:[0,0,0]
	v_mfma_scale_f32_16x16x128_f8f6f4 v[62:65], v[18:25], v[214:221], v[62:65], v195, v195 op_sel_hi:[0,0,0]
	v_mfma_scale_f32_16x16x128_f8f6f4 v[58:61], v[26:33], v[214:221], v[58:61], v195, v195 op_sel_hi:[0,0,0]
	v_mfma_scale_f32_16x16x128_f8f6f4 v[46:49], v[18:25], v[222:229], v[46:49], v195, v195 op_sel_hi:[0,0,0]
	v_mfma_scale_f32_16x16x128_f8f6f4 v[42:45], v[26:33], v[222:229], v[42:45], v195, v195 op_sel_hi:[0,0,0]
	s_nop 3
	s_setprio 0
	s_setprio 2
	v_mfma_scale_f32_16x16x128_f8f6f4 v[86:89], v[2:9], v[198:205], v[86:89], v195, v195 op_sel_hi:[0,0,0]
	v_mfma_scale_f32_16x16x128_f8f6f4 v[82:85], v[10:17], v[198:205], v[82:85], v195, v195 op_sel_hi:[0,0,0]
	v_mfma_scale_f32_16x16x128_f8f6f4 v[70:73], v[2:9], v[206:213], v[70:73], v195, v195 op_sel_hi:[0,0,0]
	v_mfma_scale_f32_16x16x128_f8f6f4 v[66:69], v[10:17], v[206:213], v[66:69], v195, v195 op_sel_hi:[0,0,0]
	v_mfma_scale_f32_16x16x128_f8f6f4 v[54:57], v[2:9], v[214:221], v[54:57], v195, v195 op_sel_hi:[0,0,0]
	v_mfma_scale_f32_16x16x128_f8f6f4 v[50:53], v[10:17], v[214:221], v[50:53], v195, v195 op_sel_hi:[0,0,0]
	v_mfma_scale_f32_16x16x128_f8f6f4 v[38:41], v[2:9], v[222:229], v[38:41], v195, v195 op_sel_hi:[0,0,0]
	v_mfma_scale_f32_16x16x128_f8f6f4 v[34:37], v[10:17], v[222:229], v[34:37], v195, v195 op_sel_hi:[0,0,0]
	s_setprio 0
	s_add_i32 s75, 0, 0x18000
	s_add_i32 s76, 0, 0x1c000
	v_add_u32_e32 v14, s75, v191
	v_add_u32_e32 v30, s76, v191
	ds_read_b128 v[2:5], v14
	ds_read_b128 v[6:9], v14 offset:1024
	ds_read_b128 v[10:13], v14 offset:2048
	ds_read_b128 v[14:17], v14 offset:3072
	ds_read_b128 v[18:21], v30
	ds_read_b128 v[22:25], v30 offset:1024
	ds_read_b128 v[26:29], v30 offset:2048
	ds_read_b128 v[30:33], v30 offset:3072
	s_mov_b32 m0, s50
	v_lshl_add_u64 v[230:231], s[30:31], 0, v[178:179]
	ds_read_b128 v[198:201], v194 offset:32768
	ds_read_b128 v[202:205], v194 offset:33792
	ds_read_b128 v[206:209], v194 offset:34816
	ds_read_b128 v[210:213], v194 offset:35840
	ds_read_b128 v[214:217], v194 offset:36864
	ds_read_b128 v[218:221], v194 offset:37888
	ds_read_b128 v[222:225], v194 offset:38912
	ds_read_b128 v[226:229], v194 offset:39936
	global_load_lds_dwordx4 v[230:231], off
	v_lshl_add_u64 v[230:231], s[30:31], 0, v[180:181]
	s_mov_b32 m0, s51
	s_nop 0
	global_load_lds_dwordx4 v[230:231], off
	s_waitcnt vmcnt(8)
	s_waitcnt lgkmcnt(0)
	s_barrier
; #define PG8_STAGE(bufoff, gbase, voff) do { _Pragma("unroll") for (int _i = 0; _i < 2; ++_i) \
;         __builtin_amdgcn_global_load_lds((const unsigned*)((const char*)(gbase) + (voff)[_i]), (PG8_LAS unsigned*)(lds + (bufoff) + ldsw + _i * 8192), 16, 0, 0); } while (0)
; #define PG8_WAIT_V(n) asm volatile("s_waitcnt vmcnt(" #n ")" ::: "memory")
; #define PG8_WAIT_L(n) asm volatile("s_waitcnt lgkmcnt(" #n ")" ::: "memory")
; #define PG8_BAR __builtin_amdgcn_s_barrier()
; #define PG8_SCHED __builtin_amdgcn_sched_barrier(0)
; template <class Epi, class Sched, bool ALIGN_EPI = true, bool F8 = false>
; __device__ __forceinline__ void gemm_phase(PG8_LAS unsigned char* lds, const Sched& S, const Epi& E) {
;     ...
;         for (int t = 0; t < nt; t += 2) {
;             const bool last = (t == nt - 2);
;             if constexpr (Sched::GATHER) { if (last && has_next) S.a_off(nxt, Rs, Cs, voffAn); }
;             const char* a1 = cA + (size_t)(t + 1) * kstep;
;             const char* a2 = last ? nA : cA + (size_t)(t + 2) * kstep; const char* b2 = last ? nB : cB + (size_t)(t + 2) * kstepB;
;             const char* a3 = a2 + kstep; const char* b3 = b2 + kstepB;
;     ...
;             PG8_LDB(B0, 0, 0); PG8_LDB(B1, 0, 1); PG8_SCHED; PG8_LDA(At, 0, 0); PG8_STAGE(PG8_SA(1, 1), a1, voffA[1]);
;             PG8_WAIT_V(8); PG8_WAIT_L(0); PG8_BAR; PG8_MMA(0, 0, At, B0); PG8_MMA(0, 1, At, B1); PG8_BAR; PG8_SCHED;
;             PG8_LDA(At, 0, 1); PG8_STAGE(PG8_SB(0, 0), b2, voffB[0]); PG8_STAGE(PG8_SB(0, 1), b2, voffB[1]); PG8_STAGE(PG8_SA(0, 0), a2, vA2[0]);
;             PG8_WAIT_V(8); PG8_WAIT_L(0); PG8_BAR; PG8_MMA(1, 0, At, B0); PG8_MMA(1, 1, At, B1); PG8_BAR; PG8_SCHED;
;             PG8_LDB(B0, 1, 0); PG8_LDB(B1, 1, 1); PG8_SCHED; PG8_LDA(At, 1, 0); PG8_STAGE(PG8_SA(0, 1), a2, vA2[1]);
;             PG8_WAIT_V(8); PG8_WAIT_L(0); PG8_BAR; PG8_MMA(0, 0, At, B0); PG8_MMA(0, 1, At, B1); PG8_BAR; PG8_SCHED;
;             PG8_LDA(At, 1, 1); PG8_STAGE(PG8_SB(1, 0), b3, voffB[0]); PG8_STAGE(PG8_SB(1, 1), b3, voffB[1]); PG8_STAGE(PG8_SA(1, 0), a3, vA2[0]);
;             PG8_WAIT_V(8); PG8_WAIT_L(0); PG8_BAR; PG8_MMA(1, 0, At, B0); PG8_MMA(1, 1, At, B1); PG8_BAR; PG8_SCHED;
	s_setprio 2
	v_mfma_scale_f32_16x16x128_f8f6f4 v[158:161], v[2:9], v[198:205], v[158:161], v195, v195 op_sel_hi:[0,0,0]
	v_mfma_scale_f32_16x16x128_f8f6f4 v[154:157], v[10:17], v[198:205], v[154:157], v195, v195 op_sel_hi:[0,0,0]
	v_mfma_scale_f32_16x16x128_f8f6f4 v[142:145], v[2:9], v[206:213], v[142:145], v195, v195 op_sel_hi:[0,0,0]
	v_mfma_scale_f32_16x16x128_f8f6f4 v[138:141], v[10:17], v[206:213], v[138:141], v195, v195 op_sel_hi:[0,0,0]
	v_mfma_scale_f32_16x16x128_f8f6f4 v[126:129], v[2:9], v[214:221], v[126:129], v195, v195 op_sel_hi:[0,0,0]
	v_mfma_scale_f32_16x16x128_f8f6f4 v[122:125], v[10:17], v[214:221], v[122:125], v195, v195 op_sel_hi:[0,0,0]
	v_mfma_scale_f32_16x16x128_f8f6f4 v[110:113], v[2:9], v[222:229], v[110:113], v195, v195 op_sel_hi:[0,0,0]
	v_mfma_scale_f32_16x16x128_f8f6f4 v[106:109], v[10:17], v[222:229], v[106:109], v195, v195 op_sel_hi:[0,0,0]
	s_nop 3
	s_setprio 0
	s_setprio 2
	v_mfma_scale_f32_16x16x128_f8f6f4 v[150:153], v[18:25], v[198:205], v[150:153], v195, v195 op_sel_hi:[0,0,0]
	v_mfma_scale_f32_16x16x128_f8f6f4 v[146:149], v[26:33], v[198:205], v[146:149], v195, v195 op_sel_hi:[0,0,0]
	v_mfma_scale_f32_16x16x128_f8f6f4 v[134:137], v[18:25], v[206:213], v[134:137], v195, v195 op_sel_hi:[0,0,0]
	v_mfma_scale_f32_16x16x128_f8f6f4 v[130:133], v[26:33], v[206:213], v[130:133], v195, v195 op_sel_hi:[0,0,0]
	v_mfma_scale_f32_16x16x128_f8f6f4 v[118:121], v[18:25], v[214:221], v[118:121], v195, v195 op_sel_hi:[0,0,0]
	v_mfma_scale_f32_16x16x128_f8f6f4 v[114:117], v[26:33], v[214:221], v[114:117], v195, v195 op_sel_hi:[0,0,0]
	v_mfma_scale_f32_16x16x128_f8f6f4 v[102:105], v[18:25], v[222:229], v[102:105], v195, v195 op_sel_hi:[0,0,0]
	v_mfma_scale_f32_16x16x128_f8f6f4 v[98:101], v[26:33], v[222:229], v[98:101], v195, v195 op_sel_hi:[0,0,0]
	s_setprio 0
	s_add_u32 s28, s28, 0x8000
	s_addc_u32 s29, s29, 0
	s_add_i32 s30, s75, s47
	v_lshl_add_u64 v[230:231], s[28:29], 0, v[164:165]
	s_mov_b32 m0, s30
	ds_read_b128 v[198:201], v194 offset:49152
	ds_read_b128 v[202:205], v194 offset:50176
	ds_read_b128 v[206:209], v194 offset:51200
	ds_read_b128 v[210:213], v194 offset:52224
	ds_read_b128 v[214:217], v194 offset:53248
	ds_read_b128 v[218:221], v194 offset:54272
	ds_read_b128 v[222:225], v194 offset:55296
	ds_read_b128 v[226:229], v194 offset:56320
	global_load_lds_dwordx4 v[230:231], off
	v_lshl_add_u64 v[230:231], s[28:29], 0, v[166:167]
	s_add_i32 m0, s30, 0x2000
	s_add_i32 s30, s76, s47
	global_load_lds_dwordx4 v[230:231], off
	v_lshl_add_u64 v[230:231], s[28:29], 0, v[168:169]
	s_mov_b32 m0, s30
	s_nop 0
	global_load_lds_dwordx4 v[230:231], off
	v_lshl_add_u64 v[230:231], s[28:29], 0, v[172:173]
	s_add_i32 m0, s30, 0x2000
	s_nop 0
	global_load_lds_dwordx4 v[230:231], off
	v_lshl_add_u64 v[230:231], s[26:27], 0, v[174:175]
	s_mov_b32 m0, s60
	s_nop 0
	global_load_lds_dwordx4 v[230:231], off
	v_lshl_add_u64 v[230:231], s[26:27], 0, v[176:177]
	s_mov_b32 m0, s61
	s_nop 0
	global_load_lds_dwordx4 v[230:231], off
	s_waitcnt vmcnt(8)
	s_waitcnt lgkmcnt(0)
	s_barrier
	s_setprio 2
	v_mfma_scale_f32_16x16x128_f8f6f4 v[94:97], v[2:9], v[198:205], v[94:97], v195, v195 op_sel_hi:[0,0,0]
	v_mfma_scale_f32_16x16x128_f8f6f4 v[90:93], v[10:17], v[198:205], v[90:93], v195, v195 op_sel_hi:[0,0,0]
	v_mfma_scale_f32_16x16x128_f8f6f4 v[78:81], v[2:9], v[206:213], v[78:81], v195, v195 op_sel_hi:[0,0,0]
	v_mfma_scale_f32_16x16x128_f8f6f4 v[74:77], v[10:17], v[206:213], v[74:77], v195, v195 op_sel_hi:[0,0,0]
	v_mfma_scale_f32_16x16x128_f8f6f4 v[62:65], v[2:9], v[214:221], v[62:65], v195, v195 op_sel_hi:[0,0,0]
	v_mfma_scale_f32_16x16x128_f8f6f4 v[58:61], v[10:17], v[214:221], v[58:61], v195, v195 op_sel_hi:[0,0,0]
	v_mfma_scale_f32_16x16x128_f8f6f4 v[46:49], v[2:9], v[222:229], v[46:49], v195, v195 op_sel_hi:[0,0,0]
	v_mfma_scale_f32_16x16x128_f8f6f4 v[42:45], v[10:17], v[222:229], v[42:45], v195, v195 op_sel_hi:[0,0,0]
	s_nop 3
	s_setprio 0
	s_setprio 2
	v_mfma_scale_f32_16x16x128_f8f6f4 v[86:89], v[18:25], v[198:205], v[86:89], v195, v195 op_sel_hi:[0,0,0]
	v_mfma_scale_f32_16x16x128_f8f6f4 v[82:85], v[26:33], v[198:205], v[82:85], v195, v195 op_sel_hi:[0,0,0]
	v_mfma_scale_f32_16x16x128_f8f6f4 v[70:73], v[18:25], v[206:213], v[70:73], v195, v195 op_sel_hi:[0,0,0]
	v_mfma_scale_f32_16x16x128_f8f6f4 v[66:69], v[26:33], v[206:213], v[66:69], v195, v195 op_sel_hi:[0,0,0]
	v_mfma_scale_f32_16x16x128_f8f6f4 v[54:57], v[18:25], v[214:221], v[54:57], v195, v195 op_sel_hi:[0,0,0]
	v_mfma_scale_f32_16x16x128_f8f6f4 v[50:53], v[26:33], v[214:221], v[50:53], v195, v195 op_sel_hi:[0,0,0]
	v_mfma_scale_f32_16x16x128_f8f6f4 v[38:41], v[18:25], v[222:229], v[38:41], v195, v195 op_sel_hi:[0,0,0]
	v_mfma_scale_f32_16x16x128_f8f6f4 v[34:37], v[26:33], v[222:229], v[34:37], v195, v195 op_sel_hi:[0,0,0]
	s_setprio 0
	s_add_i32 s74, s74, 2
	s_add_u32 s17, s17, 0x10000
	s_addc_u32 s19, s19, 0
	s_add_u32 s24, s24, 0x10000
	s_addc_u32 s25, s25, 0
	s_cmp_gt_u32 s74, 13
	s_cbranch_scc0 .Lh1_428

; #define PG8_STAGE(bufoff, gbase, voff) do { _Pragma("unroll") for (int _i = 0; _i < 2; ++_i) \
;         __builtin_amdgcn_global_load_lds((const unsigned*)((const char*)(gbase) + (voff)[_i]), (PG8_LAS unsigned*)(lds + (bufoff) + ldsw + _i * 8192), 16, 0, 0); } while (0)
; #define PG8_WAIT_V(n) asm volatile("s_waitcnt vmcnt(" #n ")" ::: "memory")
; #define PG8_WAIT_L(n) asm volatile("s_waitcnt lgkmcnt(" #n ")" ::: "memory")
; #define PG8_BAR __builtin_amdgcn_s_barrier()
; #define PG8_SCHED __builtin_amdgcn_sched_barrier(0)
; template <class Epi, class Sched, bool ALIGN_EPI = true, bool F8 = false>
; __device__ __forceinline__ void gemm_phase(PG8_LAS unsigned char* lds, const Sched& S, const Epi& E) {
;     ...
;             PG8_LDB(B0, 0, 0); PG8_LDB(B1, 0, 1); PG8_SCHED; PG8_LDA(At, 0, 0); PG8_STAGE(PG8_SA(1, 1), a1, voffA[1]);
;             PG8_WAIT_V(8); PG8_WAIT_L(0); PG8_BAR; PG8_MMA(0, 0, At, B0); PG8_MMA(0, 1, At, B1); PG8_BAR; PG8_SCHED;
;             PG8_LDA(At, 0, 1); PG8_STAGE(PG8_SB(0, 0), b2, voffB[0]); PG8_STAGE(PG8_SB(0, 1), b2, voffB[1]); PG8_STAGE(PG8_SA(0, 0), a2, vA2[0]);
;             PG8_WAIT_V(8); PG8_WAIT_L(0); PG8_BAR; PG8_MMA(1, 0, At, B0); PG8_MMA(1, 1, At, B1); PG8_BAR; PG8_SCHED;
;             PG8_LDB(B0, 1, 0); PG8_LDB(B1, 1, 1); PG8_SCHED; PG8_LDA(At, 1, 0); PG8_STAGE(PG8_SA(0, 1), a2, vA2[1]);
;             PG8_WAIT_V(8); PG8_WAIT_L(0); PG8_BAR; PG8_MMA(0, 0, At, B0); PG8_MMA(0, 1, At, B1); PG8_BAR; PG8_SCHED;
;             PG8_LDA(At, 1, 1); PG8_STAGE(PG8_SB(1, 0), b3, voffB[0]); PG8_STAGE(PG8_SB(1, 1), b3, voffB[1]); PG8_STAGE(PG8_SA(1, 0), a3, vA2[0]);
;             PG8_WAIT_V(8); PG8_WAIT_L(0); PG8_BAR; PG8_MMA(1, 0, At, B0); PG8_MMA(1, 1, At, B1); PG8_BAR; PG8_SCHED;
.LBB0_834:
	v_add_u32_e32 v10, s58, v190
	ds_read_b128 v[2:5], v10
	ds_read_b128 v[6:9], v10 offset:1024
	ds_read_b128 v[142:145], v10 offset:2048
	ds_read_b128 v[146:149], v10 offset:3072
	v_add_u32_e32 v10, s59, v190
	ds_read_b128 v[150:153], v10
	ds_read_b128 v[154:157], v10 offset:1024
	ds_read_b128 v[202:205], v10 offset:2048
	ds_read_b128 v[206:209], v10 offset:3072
	s_add_i32 s77, s26, 2
	s_add_u32 s27, s24, 0x8000
	s_addc_u32 s28, s25, 0
	s_cmp_eq_u32 s74, s26
	s_cselect_b32 s30, s20, s27
	s_cselect_b32 s31, s21, s28
	s_cselect_b32 s28, s22, s75
	s_cselect_b32 s29, s23, s76
	s_add_u32 s26, s30, 0x8000
	s_addc_u32 s27, s31, 0
	v_lshl_add_u64 v[12:13], s[24:25], 0, v[182:183]
	s_add_i32 m0, s45, 0xc000
	ds_read_b128 v[210:213], v198
	ds_read_b128 v[214:217], v198 offset:1024
	ds_read_b128 v[218:221], v198 offset:2048
	ds_read_b128 v[222:225], v198 offset:3072
	ds_read_b128 v[226:229], v198 offset:4096
	ds_read_b128 v[230:233], v198 offset:5120
	ds_read_b128 v[234:237], v198 offset:6144
	ds_read_b128 v[238:241], v198 offset:7168
	global_load_lds_dwordx4 v[12:13], off
	v_lshl_add_u64 v[12:13], s[24:25], 0, v[180:181]
	s_add_i32 m0, s45, 0xe000
	s_nop 0
	global_load_lds_dwordx4 v[12:13], off
	s_waitcnt vmcnt(8)
	s_waitcnt lgkmcnt(0)
	s_setprio 1
	v_mfma_scale_f32_16x16x128_f8f6f4 v[138:141], v[2:9], v[210:217], v[138:141], v199, v199 op_sel_hi:[0,0,0]
	v_mfma_scale_f32_16x16x128_f8f6f4 v[134:137], v[142:149], v[210:217], v[134:137], v199, v199 op_sel_hi:[0,0,0]
	v_mfma_scale_f32_16x16x128_f8f6f4 v[130:133], v[2:9], v[218:225], v[130:133], v199, v199 op_sel_hi:[0,0,0]
	v_mfma_scale_f32_16x16x128_f8f6f4 v[126:129], v[142:149], v[218:225], v[126:129], v199, v199 op_sel_hi:[0,0,0]
	v_mfma_scale_f32_16x16x128_f8f6f4 v[122:125], v[2:9], v[226:233], v[122:125], v199, v199 op_sel_hi:[0,0,0]
	v_mfma_scale_f32_16x16x128_f8f6f4 v[118:121], v[142:149], v[226:233], v[118:121], v199, v199 op_sel_hi:[0,0,0]
	v_mfma_scale_f32_16x16x128_f8f6f4 v[114:117], v[2:9], v[234:241], v[114:117], v199, v199 op_sel_hi:[0,0,0]
	v_mfma_scale_f32_16x16x128_f8f6f4 v[110:113], v[142:149], v[234:241], v[110:113], v199, v199 op_sel_hi:[0,0,0]
	s_nop 3
	s_setprio 0
	s_setprio 1
	v_mfma_scale_f32_16x16x128_f8f6f4 v[106:109], v[150:157], v[210:217], v[106:109], v199, v199 op_sel_hi:[0,0,0]
	v_mfma_scale_f32_16x16x128_f8f6f4 v[102:105], v[202:209], v[210:217], v[102:105], v199, v199 op_sel_hi:[0,0,0]
	v_mfma_scale_f32_16x16x128_f8f6f4 v[98:101], v[150:157], v[218:225], v[98:101], v199, v199 op_sel_hi:[0,0,0]
	v_mfma_scale_f32_16x16x128_f8f6f4 v[94:97], v[202:209], v[218:225], v[94:97], v199, v199 op_sel_hi:[0,0,0]
	v_mfma_scale_f32_16x16x128_f8f6f4 v[90:93], v[150:157], v[226:233], v[90:93], v199, v199 op_sel_hi:[0,0,0]
	v_mfma_scale_f32_16x16x128_f8f6f4 v[86:89], v[202:209], v[226:233], v[86:89], v199, v199 op_sel_hi:[0,0,0]
	v_mfma_scale_f32_16x16x128_f8f6f4 v[82:85], v[150:157], v[234:241], v[82:85], v199, v199 op_sel_hi:[0,0,0]
	v_mfma_scale_f32_16x16x128_f8f6f4 v[78:81], v[202:209], v[234:241], v[78:81], v199, v199 op_sel_hi:[0,0,0]
	s_setprio 0
	s_barrier
	s_add_i32 s78, s58, s44
	v_lshl_add_u64 v[12:13], s[28:29], 0, v[158:159]
	s_mov_b32 m0, s78
	ds_read_b128 v[210:213], v198 offset:16384
	ds_read_b128 v[214:217], v198 offset:17408
	ds_read_b128 v[218:221], v198 offset:18432
	ds_read_b128 v[222:225], v198 offset:19456
	ds_read_b128 v[226:229], v198 offset:20480
	ds_read_b128 v[230:233], v198 offset:21504
	ds_read_b128 v[234:237], v198 offset:22528
	ds_read_b128 v[238:241], v198 offset:23552
	global_load_lds_dwordx4 v[12:13], off
	v_lshl_add_u64 v[188:189], s[28:29], 0, v[160:161]
	s_add_i32 m0, s78, 0x2000
	s_add_i32 s78, s59, s44
	global_load_lds_dwordx4 v[188:189], off
	v_lshl_add_u64 v[12:13], v[12:13], 0, s[8:9]
	s_mov_b32 m0, s78
	s_nop 0
	global_load_lds_dwordx4 v[12:13], off
	v_lshl_add_u64 v[12:13], v[188:189], 0, s[8:9]
	s_add_i32 m0, s78, 0x2000
	s_nop 0
	global_load_lds_dwordx4 v[12:13], off
	v_lshl_add_u64 v[12:13], s[30:31], 0, v[162:163]
	s_mov_b32 m0, s45
	s_nop 0
	global_load_lds_dwordx4 v[12:13], off
	v_lshl_add_u64 v[12:13], s[30:31], 0, v[164:165]
	s_mov_b32 m0, s46
	s_nop 0
	global_load_lds_dwordx4 v[12:13], off
	s_waitcnt vmcnt(8)
	s_waitcnt lgkmcnt(0)
	s_setprio 1
	v_mfma_scale_f32_16x16x128_f8f6f4 v[74:77], v[2:9], v[210:217], v[74:77], v199, v199 op_sel_hi:[0,0,0]
	v_mfma_scale_f32_16x16x128_f8f6f4 v[70:73], v[142:149], v[210:217], v[70:73], v199, v199 op_sel_hi:[0,0,0]
	v_mfma_scale_f32_16x16x128_f8f6f4 v[66:69], v[2:9], v[218:225], v[66:69], v199, v199 op_sel_hi:[0,0,0]
	v_mfma_scale_f32_16x16x128_f8f6f4 v[62:65], v[142:149], v[218:225], v[62:65], v199, v199 op_sel_hi:[0,0,0]
	v_mfma_scale_f32_16x16x128_f8f6f4 v[58:61], v[2:9], v[226:233], v[58:61], v199, v199 op_sel_hi:[0,0,0]
	v_mfma_scale_f32_16x16x128_f8f6f4 v[54:57], v[142:149], v[226:233], v[54:57], v199, v199 op_sel_hi:[0,0,0]
	v_mfma_scale_f32_16x16x128_f8f6f4 v[50:53], v[2:9], v[234:241], v[50:53], v199, v199 op_sel_hi:[0,0,0]
	v_mfma_scale_f32_16x16x128_f8f6f4 v[46:49], v[142:149], v[234:241], v[46:49], v199, v199 op_sel_hi:[0,0,0]
	s_nop 3
	s_setprio 0
	s_setprio 1
	v_mfma_scale_f32_16x16x128_f8f6f4 v[42:45], v[150:157], v[210:217], v[42:45], v199, v199 op_sel_hi:[0,0,0]
	v_mfma_scale_f32_16x16x128_f8f6f4 v[38:41], v[202:209], v[210:217], v[38:41], v199, v199 op_sel_hi:[0,0,0]
	v_mfma_scale_f32_16x16x128_f8f6f4 v[34:37], v[150:157], v[218:225], v[34:37], v199, v199 op_sel_hi:[0,0,0]
	v_mfma_scale_f32_16x16x128_f8f6f4 v[30:33], v[202:209], v[218:225], v[30:33], v199, v199 op_sel_hi:[0,0,0]
	v_mfma_scale_f32_16x16x128_f8f6f4 v[26:29], v[150:157], v[226:233], v[26:29], v199, v199 op_sel_hi:[0,0,0]
	v_mfma_scale_f32_16x16x128_f8f6f4 v[22:25], v[202:209], v[226:233], v[22:25], v199, v199 op_sel_hi:[0,0,0]
	v_mfma_scale_f32_16x16x128_f8f6f4 v[18:21], v[150:157], v[234:241], v[18:21], v199, v199 op_sel_hi:[0,0,0]
	v_mfma_scale_f32_16x16x128_f8f6f4 v[14:17], v[202:209], v[234:241], v[14:17], v199, v199 op_sel_hi:[0,0,0]
	s_setprio 0
	s_barrier
; #define PG8_STAGE(bufoff, gbase, voff) do { _Pragma("unroll") for (int _i = 0; _i < 2; ++_i) \
;         __builtin_amdgcn_global_load_lds((const unsigned*)((const char*)(gbase) + (voff)[_i]), (PG8_LAS unsigned*)(lds + (bufoff) + ldsw + _i * 8192), 16, 0, 0); } while (0)
; #define PG8_WAIT_V(n) asm volatile("s_waitcnt vmcnt(" #n ")" ::: "memory")
; #define PG8_WAIT_L(n) asm volatile("s_waitcnt lgkmcnt(" #n ")" ::: "memory")
; #define PG8_BAR __builtin_amdgcn_s_barrier()
; #define PG8_SCHED __builtin_amdgcn_sched_barrier(0)
; template <class Epi, class Sched, bool ALIGN_EPI = true, bool F8 = false>
; __device__ __forceinline__ void gemm_phase(PG8_LAS unsigned char* lds, const Sched& S, const Epi& E) {
;     ...
;         for (int t = 0; t < nt; t += 2) {
;             const bool last = (t == nt - 2);
;             if constexpr (Sched::GATHER) { if (last && has_next) S.a_off(nxt, Rs, Cs, voffAn); }
;             const char* a1 = cA + (size_t)(t + 1) * kstep;
;             const char* a2 = last ? nA : cA + (size_t)(t + 2) * kstep; const char* b2 = last ? nB : cB + (size_t)(t + 2) * kstepB;
;             const char* a3 = a2 + kstep; const char* b3 = b2 + kstepB;
;     ...
;             PG8_LDB(B0, 0, 0); PG8_LDB(B1, 0, 1); PG8_SCHED; PG8_LDA(At, 0, 0); PG8_STAGE(PG8_SA(1, 1), a1, voffA[1]);
;             PG8_WAIT_V(8); PG8_WAIT_L(0); PG8_BAR; PG8_MMA(0, 0, At, B0); PG8_MMA(0, 1, At, B1); PG8_BAR; PG8_SCHED;
;             PG8_LDA(At, 0, 1); PG8_STAGE(PG8_SB(0, 0), b2, voffB[0]); PG8_STAGE(PG8_SB(0, 1), b2, voffB[1]); PG8_STAGE(PG8_SA(0, 0), a2, vA2[0]);
;             PG8_WAIT_V(8); PG8_WAIT_L(0); PG8_BAR; PG8_MMA(1, 0, At, B0); PG8_MMA(1, 1, At, B1); PG8_BAR; PG8_SCHED;
;             PG8_LDB(B0, 1, 0); PG8_LDB(B1, 1, 1); PG8_SCHED; PG8_LDA(At, 1, 0); PG8_STAGE(PG8_SA(0, 1), a2, vA2[1]);
;             PG8_WAIT_V(8); PG8_WAIT_L(0); PG8_BAR; PG8_MMA(0, 0, At, B0); PG8_MMA(0, 1, At, B1); PG8_BAR; PG8_SCHED;
;             PG8_LDA(At, 1, 1); PG8_STAGE(PG8_SB(1, 0), b3, voffB[0]); PG8_STAGE(PG8_SB(1, 1), b3, voffB[1]); PG8_STAGE(PG8_SA(1, 0), a3, vA2[0]);
;             PG8_WAIT_V(8); PG8_WAIT_L(0); PG8_BAR; PG8_MMA(1, 0, At, B0); PG8_MMA(1, 1, At, B1); PG8_BAR; PG8_SCHED;
	s_add_i32 s78, 0, 0x18000
	s_add_i32 s79, 0, 0x1c000
	v_add_u32_e32 v2, s78, v190
	v_add_u32_e32 v10, s79, v190
	ds_read_b128 v[142:145], v2
	ds_read_b128 v[146:149], v2 offset:1024
	ds_read_b128 v[150:153], v2 offset:2048
	ds_read_b128 v[154:157], v2 offset:3072
	ds_read_b128 v[2:5], v10
	ds_read_b128 v[6:9], v10 offset:1024
	ds_read_b128 v[202:205], v10 offset:2048
	ds_read_b128 v[206:209], v10 offset:3072
	s_mov_b32 m0, s47
	v_lshl_add_u64 v[12:13], s[30:31], 0, v[166:167]
	ds_read_b128 v[210:213], v198 offset:32768
	ds_read_b128 v[214:217], v198 offset:33792
	ds_read_b128 v[218:221], v198 offset:34816
	ds_read_b128 v[222:225], v198 offset:35840
	ds_read_b128 v[226:229], v198 offset:36864
	ds_read_b128 v[230:233], v198 offset:37888
	ds_read_b128 v[234:237], v198 offset:38912
	ds_read_b128 v[238:241], v198 offset:39936
	global_load_lds_dwordx4 v[12:13], off
	v_lshl_add_u64 v[12:13], s[30:31], 0, v[168:169]
	s_mov_b32 m0, s48
	s_nop 0
	global_load_lds_dwordx4 v[12:13], off
	s_waitcnt vmcnt(8)
	s_waitcnt lgkmcnt(0)
	s_setprio 1
	v_mfma_scale_f32_16x16x128_f8f6f4 v[138:141], v[142:149], v[210:217], v[138:141], v199, v199 op_sel_hi:[0,0,0]
	v_mfma_scale_f32_16x16x128_f8f6f4 v[134:137], v[150:157], v[210:217], v[134:137], v199, v199 op_sel_hi:[0,0,0]
	v_mfma_scale_f32_16x16x128_f8f6f4 v[130:133], v[142:149], v[218:225], v[130:133], v199, v199 op_sel_hi:[0,0,0]
	v_mfma_scale_f32_16x16x128_f8f6f4 v[126:129], v[150:157], v[218:225], v[126:129], v199, v199 op_sel_hi:[0,0,0]
	v_mfma_scale_f32_16x16x128_f8f6f4 v[122:125], v[142:149], v[226:233], v[122:125], v199, v199 op_sel_hi:[0,0,0]
	v_mfma_scale_f32_16x16x128_f8f6f4 v[118:121], v[150:157], v[226:233], v[118:121], v199, v199 op_sel_hi:[0,0,0]
	v_mfma_scale_f32_16x16x128_f8f6f4 v[114:117], v[142:149], v[234:241], v[114:117], v199, v199 op_sel_hi:[0,0,0]
	v_mfma_scale_f32_16x16x128_f8f6f4 v[110:113], v[150:157], v[234:241], v[110:113], v199, v199 op_sel_hi:[0,0,0]
	s_nop 3
	s_setprio 0
	s_setprio 1
	v_mfma_scale_f32_16x16x128_f8f6f4 v[106:109], v[2:9], v[210:217], v[106:109], v199, v199 op_sel_hi:[0,0,0]
	v_mfma_scale_f32_16x16x128_f8f6f4 v[102:105], v[202:209], v[210:217], v[102:105], v199, v199 op_sel_hi:[0,0,0]
	v_mfma_scale_f32_16x16x128_f8f6f4 v[98:101], v[2:9], v[218:225], v[98:101], v199, v199 op_sel_hi:[0,0,0]
	v_mfma_scale_f32_16x16x128_f8f6f4 v[94:97], v[202:209], v[218:225], v[94:97], v199, v199 op_sel_hi:[0,0,0]
	v_mfma_scale_f32_16x16x128_f8f6f4 v[90:93], v[2:9], v[226:233], v[90:93], v199, v199 op_sel_hi:[0,0,0]
	v_mfma_scale_f32_16x16x128_f8f6f4 v[86:89], v[202:209], v[226:233], v[86:89], v199, v199 op_sel_hi:[0,0,0]
	v_mfma_scale_f32_16x16x128_f8f6f4 v[82:85], v[2:9], v[234:241], v[82:85], v199, v199 op_sel_hi:[0,0,0]
	v_mfma_scale_f32_16x16x128_f8f6f4 v[78:81], v[202:209], v[234:241], v[78:81], v199, v199 op_sel_hi:[0,0,0]
	s_setprio 0
	s_barrier
	s_add_u32 s28, s28, 0x8000
	s_addc_u32 s29, s29, 0
	s_add_i32 s30, s78, s44
	v_lshl_add_u64 v[12:13], s[28:29], 0, v[158:159]
	s_mov_b32 m0, s30
	ds_read_b128 v[210:213], v198 offset:49152
	ds_read_b128 v[214:217], v198 offset:50176
	ds_read_b128 v[218:221], v198 offset:51200
	ds_read_b128 v[222:225], v198 offset:52224
	ds_read_b128 v[226:229], v198 offset:53248
	ds_read_b128 v[230:233], v198 offset:54272
	ds_read_b128 v[234:237], v198 offset:55296
	ds_read_b128 v[238:241], v198 offset:56320
	global_load_lds_dwordx4 v[12:13], off
	v_lshl_add_u64 v[12:13], s[28:29], 0, v[160:161]
	s_add_i32 m0, s30, 0x2000
	s_add_i32 s30, s79, s44
	global_load_lds_dwordx4 v[12:13], off
	v_lshl_add_u64 v[12:13], s[28:29], 0, v[172:173]
	s_mov_b32 m0, s30
	s_nop 0
	global_load_lds_dwordx4 v[12:13], off
	v_lshl_add_u64 v[12:13], s[28:29], 0, v[174:175]
	s_add_i32 m0, s30, 0x2000
	s_nop 0
	global_load_lds_dwordx4 v[12:13], off
	v_lshl_add_u64 v[12:13], s[26:27], 0, v[162:163]
	s_mov_b32 m0, s50
	s_nop 0
	global_load_lds_dwordx4 v[12:13], off
	v_lshl_add_u64 v[12:13], s[26:27], 0, v[164:165]
	s_mov_b32 m0, s51
	s_nop 0
	global_load_lds_dwordx4 v[12:13], off
	s_waitcnt vmcnt(8)
	s_waitcnt lgkmcnt(0)
	s_setprio 1
	v_mfma_scale_f32_16x16x128_f8f6f4 v[74:77], v[142:149], v[210:217], v[74:77], v199, v199 op_sel_hi:[0,0,0]
	v_mfma_scale_f32_16x16x128_f8f6f4 v[70:73], v[150:157], v[210:217], v[70:73], v199, v199 op_sel_hi:[0,0,0]
	v_mfma_scale_f32_16x16x128_f8f6f4 v[66:69], v[142:149], v[218:225], v[66:69], v199, v199 op_sel_hi:[0,0,0]
	v_mfma_scale_f32_16x16x128_f8f6f4 v[62:65], v[150:157], v[218:225], v[62:65], v199, v199 op_sel_hi:[0,0,0]
	v_mfma_scale_f32_16x16x128_f8f6f4 v[58:61], v[142:149], v[226:233], v[58:61], v199, v199 op_sel_hi:[0,0,0]
	v_mfma_scale_f32_16x16x128_f8f6f4 v[54:57], v[150:157], v[226:233], v[54:57], v199, v199 op_sel_hi:[0,0,0]
	v_mfma_scale_f32_16x16x128_f8f6f4 v[50:53], v[142:149], v[234:241], v[50:53], v199, v199 op_sel_hi:[0,0,0]
	v_mfma_scale_f32_16x16x128_f8f6f4 v[46:49], v[150:157], v[234:241], v[46:49], v199, v199 op_sel_hi:[0,0,0]
	s_nop 3
	s_setprio 0
	s_setprio 1
	v_mfma_scale_f32_16x16x128_f8f6f4 v[42:45], v[2:9], v[210:217], v[42:45], v199, v199 op_sel_hi:[0,0,0]
	v_mfma_scale_f32_16x16x128_f8f6f4 v[38:41], v[202:209], v[210:217], v[38:41], v199, v199 op_sel_hi:[0,0,0]
	v_mfma_scale_f32_16x16x128_f8f6f4 v[34:37], v[2:9], v[218:225], v[34:37], v199, v199 op_sel_hi:[0,0,0]
	v_mfma_scale_f32_16x16x128_f8f6f4 v[30:33], v[202:209], v[218:225], v[30:33], v199, v199 op_sel_hi:[0,0,0]
	v_mfma_scale_f32_16x16x128_f8f6f4 v[26:29], v[2:9], v[226:233], v[26:29], v199, v199 op_sel_hi:[0,0,0]
	v_mfma_scale_f32_16x16x128_f8f6f4 v[22:25], v[202:209], v[226:233], v[22:25], v199, v199 op_sel_hi:[0,0,0]
	v_mfma_scale_f32_16x16x128_f8f6f4 v[18:21], v[2:9], v[234:241], v[18:21], v199, v199 op_sel_hi:[0,0,0]
	v_mfma_scale_f32_16x16x128_f8f6f4 v[14:17], v[202:209], v[234:241], v[14:17], v199, v199 op_sel_hi:[0,0,0]
	s_setprio 0
	s_barrier
	s_add_u32 s75, s75, 0x10000
	s_addc_u32 s76, s76, 0
	s_add_u32 s24, s24, 0x10000
	s_addc_u32 s25, s25, 0
	s_cmp_ge_i32 s77, s72
	s_mov_b32 s26, s77
	s_cbranch_scc0 .LBB0_834
	s_branch .Lfx_23459
; #define PG8_STAGE(bufoff, gbase, voff) do { _Pragma("unroll") for (int _i = 0; _i < 2; ++_i) \
;         __builtin_amdgcn_global_load_lds((const unsigned*)((const char*)(gbase) + (voff)[_i]), (PG8_LAS unsigned*)(lds + (bufoff) + ldsw + _i * 8192), 16, 0, 0); } while (0)
; #define PG8_WAIT_V(n) asm volatile("s_waitcnt vmcnt(" #n ")" ::: "memory")
; #define PG8_WAIT_L(n) asm volatile("s_waitcnt lgkmcnt(" #n ")" ::: "memory")
; #define PG8_BAR __builtin_amdgcn_s_barrier()
; #define PG8_SCHED __builtin_amdgcn_sched_barrier(0)
; template <class Epi, class Sched, bool ALIGN_EPI = true, bool F8 = false>
; __device__ __forceinline__ void gemm_phase(PG8_LAS unsigned char* lds, const Sched& S, const Epi& E) {
;     ...
;             PG8_LDB(B0, 0, 0); PG8_LDB(B1, 0, 1); PG8_SCHED; PG8_LDA(At, 0, 0); PG8_STAGE(PG8_SA(1, 1), a1, voffA[1]);
;             PG8_WAIT_V(8); PG8_WAIT_L(0); PG8_BAR; PG8_MMA(0, 0, At, B0); PG8_MMA(0, 1, At, B1); PG8_BAR; PG8_SCHED;
;             PG8_LDA(At, 0, 1); PG8_STAGE(PG8_SB(0, 0), b2, voffB[0]); PG8_STAGE(PG8_SB(0, 1), b2, voffB[1]); PG8_STAGE(PG8_SA(0, 0), a2, vA2[0]);
;             PG8_WAIT_V(8); PG8_WAIT_L(0); PG8_BAR; PG8_MMA(1, 0, At, B0); PG8_MMA(1, 1, At, B1); PG8_BAR; PG8_SCHED;
;             PG8_LDB(B0, 1, 0); PG8_LDB(B1, 1, 1); PG8_SCHED; PG8_LDA(At, 1, 0); PG8_STAGE(PG8_SA(0, 1), a2, vA2[1]);
;             PG8_WAIT_V(8); PG8_WAIT_L(0); PG8_BAR; PG8_MMA(0, 0, At, B0); PG8_MMA(0, 1, At, B1); PG8_BAR; PG8_SCHED;
;             PG8_LDA(At, 1, 1); PG8_STAGE(PG8_SB(1, 0), b3, voffB[0]); PG8_STAGE(PG8_SB(1, 1), b3, voffB[1]); PG8_STAGE(PG8_SA(1, 0), a3, vA2[0]);
;             PG8_WAIT_V(8); PG8_WAIT_L(0); PG8_BAR; PG8_MMA(1, 0, At, B0); PG8_MMA(1, 1, At, B1); PG8_BAR; PG8_SCHED;
.Lh1e_23459:
.Lh1_834:
	v_add_u32_e32 v10, s58, v190
	ds_read_b128 v[2:5], v10
	ds_read_b128 v[6:9], v10 offset:1024
	ds_read_b128 v[142:145], v10 offset:2048
	ds_read_b128 v[146:149], v10 offset:3072
	v_add_u32_e32 v10, s59, v190
	ds_read_b128 v[150:153], v10
	ds_read_b128 v[154:157], v10 offset:1024
	ds_read_b128 v[202:205], v10 offset:2048
	ds_read_b128 v[206:209], v10 offset:3072
	s_add_i32 s77, s26, 2
	s_add_u32 s27, s24, 0x8000
	s_addc_u32 s28, s25, 0
	s_cmp_eq_u32 s74, s26
	s_cselect_b32 s30, s20, s27
	s_cselect_b32 s31, s21, s28
	s_cselect_b32 s28, s22, s75
	s_cselect_b32 s29, s23, s76
	s_add_u32 s26, s30, 0x8000
	s_addc_u32 s27, s31, 0
	v_lshl_add_u64 v[12:13], s[24:25], 0, v[182:183]
	s_add_i32 m0, s45, 0xc000
	ds_read_b128 v[210:213], v198
	ds_read_b128 v[214:217], v198 offset:1024
	ds_read_b128 v[218:221], v198 offset:2048
	ds_read_b128 v[222:225], v198 offset:3072
	ds_read_b128 v[226:229], v198 offset:4096
	ds_read_b128 v[230:233], v198 offset:5120
	ds_read_b128 v[234:237], v198 offset:6144
	ds_read_b128 v[238:241], v198 offset:7168
	global_load_lds_dwordx4 v[12:13], off
	v_lshl_add_u64 v[12:13], s[24:25], 0, v[180:181]
	s_add_i32 m0, s45, 0xe000
	s_nop 0
	global_load_lds_dwordx4 v[12:13], off
	s_waitcnt vmcnt(8)
	s_waitcnt lgkmcnt(0)
	s_barrier
	s_setprio 2
	v_mfma_scale_f32_16x16x128_f8f6f4 v[138:141], v[2:9], v[210:217], v[138:141], v199, v199 op_sel_hi:[0,0,0]
	v_mfma_scale_f32_16x16x128_f8f6f4 v[134:137], v[142:149], v[210:217], v[134:137], v199, v199 op_sel_hi:[0,0,0]
	v_mfma_scale_f32_16x16x128_f8f6f4 v[130:133], v[2:9], v[218:225], v[130:133], v199, v199 op_sel_hi:[0,0,0]
	v_mfma_scale_f32_16x16x128_f8f6f4 v[126:129], v[142:149], v[218:225], v[126:129], v199, v199 op_sel_hi:[0,0,0]
	v_mfma_scale_f32_16x16x128_f8f6f4 v[122:125], v[2:9], v[226:233], v[122:125], v199, v199 op_sel_hi:[0,0,0]
	v_mfma_scale_f32_16x16x128_f8f6f4 v[118:121], v[142:149], v[226:233], v[118:121], v199, v199 op_sel_hi:[0,0,0]
	v_mfma_scale_f32_16x16x128_f8f6f4 v[114:117], v[2:9], v[234:241], v[114:117], v199, v199 op_sel_hi:[0,0,0]
	v_mfma_scale_f32_16x16x128_f8f6f4 v[110:113], v[142:149], v[234:241], v[110:113], v199, v199 op_sel_hi:[0,0,0]
	s_nop 3
	s_setprio 0
	s_setprio 2
	v_mfma_scale_f32_16x16x128_f8f6f4 v[106:109], v[150:157], v[210:217], v[106:109], v199, v199 op_sel_hi:[0,0,0]
	v_mfma_scale_f32_16x16x128_f8f6f4 v[102:105], v[202:209], v[210:217], v[102:105], v199, v199 op_sel_hi:[0,0,0]
	v_mfma_scale_f32_16x16x128_f8f6f4 v[98:101], v[150:157], v[218:225], v[98:101], v199, v199 op_sel_hi:[0,0,0]
	v_mfma_scale_f32_16x16x128_f8f6f4 v[94:97], v[202:209], v[218:225], v[94:97], v199, v199 op_sel_hi:[0,0,0]
	v_mfma_scale_f32_16x16x128_f8f6f4 v[90:93], v[150:157], v[226:233], v[90:93], v199, v199 op_sel_hi:[0,0,0]
	v_mfma_scale_f32_16x16x128_f8f6f4 v[86:89], v[202:209], v[226:233], v[86:89], v199, v199 op_sel_hi:[0,0,0]
	v_mfma_scale_f32_16x16x128_f8f6f4 v[82:85], v[150:157], v[234:241], v[82:85], v199, v199 op_sel_hi:[0,0,0]
	v_mfma_scale_f32_16x16x128_f8f6f4 v[78:81], v[202:209], v[234:241], v[78:81], v199, v199 op_sel_hi:[0,0,0]
	s_setprio 0
	s_add_i32 s78, s58, s44
	v_lshl_add_u64 v[12:13], s[28:29], 0, v[158:159]
	s_mov_b32 m0, s78
	ds_read_b128 v[210:213], v198 offset:16384
	ds_read_b128 v[214:217], v198 offset:17408
	ds_read_b128 v[218:221], v198 offset:18432
	ds_read_b128 v[222:225], v198 offset:19456
	ds_read_b128 v[226:229], v198 offset:20480
	ds_read_b128 v[230:233], v198 offset:21504
	ds_read_b128 v[234:237], v198 offset:22528
	ds_read_b128 v[238:241], v198 offset:23552
	global_load_lds_dwordx4 v[12:13], off
	v_lshl_add_u64 v[188:189], s[28:29], 0, v[160:161]
	s_add_i32 m0, s78, 0x2000
	s_add_i32 s78, s59, s44
	global_load_lds_dwordx4 v[188:189], off
	v_lshl_add_u64 v[12:13], v[12:13], 0, s[8:9]
	s_mov_b32 m0, s78
	s_nop 0
	global_load_lds_dwordx4 v[12:13], off
	v_lshl_add_u64 v[12:13], v[188:189], 0, s[8:9]
	s_add_i32 m0, s78, 0x2000
	s_nop 0
	global_load_lds_dwordx4 v[12:13], off
	v_lshl_add_u64 v[12:13], s[30:31], 0, v[162:163]
	s_mov_b32 m0, s45
	s_nop 0
	global_load_lds_dwordx4 v[12:13], off
	v_lshl_add_u64 v[12:13], s[30:31], 0, v[164:165]
	s_mov_b32 m0, s46
	s_nop 0
	global_load_lds_dwordx4 v[12:13], off
	s_waitcnt vmcnt(8)
	s_waitcnt lgkmcnt(0)
	s_barrier
; #define PG8_STAGE(bufoff, gbase, voff) do { _Pragma("unroll") for (int _i = 0; _i < 2; ++_i) \
;         __builtin_amdgcn_global_load_lds((const unsigned*)((const char*)(gbase) + (voff)[_i]), (PG8_LAS unsigned*)(lds + (bufoff) + ldsw + _i * 8192), 16, 0, 0); } while (0)
; #define PG8_WAIT_V(n) asm volatile("s_waitcnt vmcnt(" #n ")" ::: "memory")
; #define PG8_WAIT_L(n) asm volatile("s_waitcnt lgkmcnt(" #n ")" ::: "memory")
; #define PG8_BAR __builtin_amdgcn_s_barrier()
; #define PG8_SCHED __builtin_amdgcn_sched_barrier(0)
; template <class Epi, class Sched, bool ALIGN_EPI = true, bool F8 = false>
; __device__ __forceinline__ void gemm_phase(PG8_LAS unsigned char* lds, const Sched& S, const Epi& E) {
;     ...
;             PG8_LDB(B0, 0, 0); PG8_LDB(B1, 0, 1); PG8_SCHED; PG8_LDA(At, 0, 0); PG8_STAGE(PG8_SA(1, 1), a1, voffA[1]);
;             PG8_WAIT_V(8); PG8_WAIT_L(0); PG8_BAR; PG8_MMA(0, 0, At, B0); PG8_MMA(0, 1, At, B1); PG8_BAR; PG8_SCHED;
;             PG8_LDA(At, 0, 1); PG8_STAGE(PG8_SB(0, 0), b2, voffB[0]); PG8_STAGE(PG8_SB(0, 1), b2, voffB[1]); PG8_STAGE(PG8_SA(0, 0), a2, vA2[0]);
;             PG8_WAIT_V(8); PG8_WAIT_L(0); PG8_BAR; PG8_MMA(1, 0, At, B0); PG8_MMA(1, 1, At, B1); PG8_BAR; PG8_SCHED;
;             PG8_LDB(B0, 1, 0); PG8_LDB(B1, 1, 1); PG8_SCHED; PG8_LDA(At, 1, 0); PG8_STAGE(PG8_SA(0, 1), a2, vA2[1]);
;             PG8_WAIT_V(8); PG8_WAIT_L(0); PG8_BAR; PG8_MMA(0, 0, At, B0); PG8_MMA(0, 1, At, B1); PG8_BAR; PG8_SCHED;
;             PG8_LDA(At, 1, 1); PG8_STAGE(PG8_SB(1, 0), b3, voffB[0]); PG8_STAGE(PG8_SB(1, 1), b3, voffB[1]); PG8_STAGE(PG8_SA(1, 0), a3, vA2[0]);
;             PG8_WAIT_V(8); PG8_WAIT_L(0); PG8_BAR; PG8_MMA(1, 0, At, B0); PG8_MMA(1, 1, At, B1); PG8_BAR; PG8_SCHED;
	s_setprio 2
	v_mfma_scale_f32_16x16x128_f8f6f4 v[74:77], v[2:9], v[210:217], v[74:77], v199, v199 op_sel_hi:[0,0,0]
	v_mfma_scale_f32_16x16x128_f8f6f4 v[70:73], v[142:149], v[210:217], v[70:73], v199, v199 op_sel_hi:[0,0,0]
	v_mfma_scale_f32_16x16x128_f8f6f4 v[66:69], v[2:9], v[218:225], v[66:69], v199, v199 op_sel_hi:[0,0,0]
	v_mfma_scale_f32_16x16x128_f8f6f4 v[62:65], v[142:149], v[218:225], v[62:65], v199, v199 op_sel_hi:[0,0,0]
	v_mfma_scale_f32_16x16x128_f8f6f4 v[58:61], v[2:9], v[226:233], v[58:61], v199, v199 op_sel_hi:[0,0,0]
	v_mfma_scale_f32_16x16x128_f8f6f4 v[54:57], v[142:149], v[226:233], v[54:57], v199, v199 op_sel_hi:[0,0,0]
	v_mfma_scale_f32_16x16x128_f8f6f4 v[50:53], v[2:9], v[234:241], v[50:53], v199, v199 op_sel_hi:[0,0,0]
	v_mfma_scale_f32_16x16x128_f8f6f4 v[46:49], v[142:149], v[234:241], v[46:49], v199, v199 op_sel_hi:[0,0,0]
	s_nop 3
	s_setprio 0
	s_setprio 2
	v_mfma_scale_f32_16x16x128_f8f6f4 v[42:45], v[150:157], v[210:217], v[42:45], v199, v199 op_sel_hi:[0,0,0]
	v_mfma_scale_f32_16x16x128_f8f6f4 v[38:41], v[202:209], v[210:217], v[38:41], v199, v199 op_sel_hi:[0,0,0]
	v_mfma_scale_f32_16x16x128_f8f6f4 v[34:37], v[150:157], v[218:225], v[34:37], v199, v199 op_sel_hi:[0,0,0]
	v_mfma_scale_f32_16x16x128_f8f6f4 v[30:33], v[202:209], v[218:225], v[30:33], v199, v199 op_sel_hi:[0,0,0]
	v_mfma_scale_f32_16x16x128_f8f6f4 v[26:29], v[150:157], v[226:233], v[26:29], v199, v199 op_sel_hi:[0,0,0]
	v_mfma_scale_f32_16x16x128_f8f6f4 v[22:25], v[202:209], v[226:233], v[22:25], v199, v199 op_sel_hi:[0,0,0]
	v_mfma_scale_f32_16x16x128_f8f6f4 v[18:21], v[150:157], v[234:241], v[18:21], v199, v199 op_sel_hi:[0,0,0]
	v_mfma_scale_f32_16x16x128_f8f6f4 v[14:17], v[202:209], v[234:241], v[14:17], v199, v199 op_sel_hi:[0,0,0]
	s_setprio 0
	s_add_i32 s78, 0, 0x18000
	s_add_i32 s79, 0, 0x1c000
	v_add_u32_e32 v2, s78, v190
	v_add_u32_e32 v10, s79, v190
	ds_read_b128 v[142:145], v2
	ds_read_b128 v[146:149], v2 offset:1024
	ds_read_b128 v[150:153], v2 offset:2048
	ds_read_b128 v[154:157], v2 offset:3072
	ds_read_b128 v[2:5], v10
	ds_read_b128 v[6:9], v10 offset:1024
	ds_read_b128 v[202:205], v10 offset:2048
	ds_read_b128 v[206:209], v10 offset:3072
	s_mov_b32 m0, s47
	v_lshl_add_u64 v[12:13], s[30:31], 0, v[166:167]
	ds_read_b128 v[210:213], v198 offset:32768
	ds_read_b128 v[214:217], v198 offset:33792
	ds_read_b128 v[218:221], v198 offset:34816
	ds_read_b128 v[222:225], v198 offset:35840
	ds_read_b128 v[226:229], v198 offset:36864
	ds_read_b128 v[230:233], v198 offset:37888
	ds_read_b128 v[234:237], v198 offset:38912
	ds_read_b128 v[238:241], v198 offset:39936
	global_load_lds_dwordx4 v[12:13], off
	v_lshl_add_u64 v[12:13], s[30:31], 0, v[168:169]
	s_mov_b32 m0, s48
	s_nop 0
	global_load_lds_dwordx4 v[12:13], off
	s_waitcnt vmcnt(8)
	s_waitcnt lgkmcnt(0)
	s_barrier
; #define PG8_STAGE(bufoff, gbase, voff) do { _Pragma("unroll") for (int _i = 0; _i < 2; ++_i) \
;         __builtin_amdgcn_global_load_lds((const unsigned*)((const char*)(gbase) + (voff)[_i]), (PG8_LAS unsigned*)(lds + (bufoff) + ldsw + _i * 8192), 16, 0, 0); } while (0)
; #define PG8_WAIT_V(n) asm volatile("s_waitcnt vmcnt(" #n ")" ::: "memory")
; #define PG8_WAIT_L(n) asm volatile("s_waitcnt lgkmcnt(" #n ")" ::: "memory")
; #define PG8_BAR __builtin_amdgcn_s_barrier()
; #define PG8_SCHED __builtin_amdgcn_sched_barrier(0)
; template <class Epi, class Sched, bool ALIGN_EPI = true, bool F8 = false>
; __device__ __forceinline__ void gemm_phase(PG8_LAS unsigned char* lds, const Sched& S, const Epi& E) {
;     ...
;             PG8_LDB(B0, 0, 0); PG8_LDB(B1, 0, 1); PG8_SCHED; PG8_LDA(At, 0, 0); PG8_STAGE(PG8_SA(1, 1), a1, voffA[1]);
;             PG8_WAIT_V(8); PG8_WAIT_L(0); PG8_BAR; PG8_MMA(0, 0, At, B0); PG8_MMA(0, 1, At, B1); PG8_BAR; PG8_SCHED;
;             PG8_LDA(At, 0, 1); PG8_STAGE(PG8_SB(0, 0), b2, voffB[0]); PG8_STAGE(PG8_SB(0, 1), b2, voffB[1]); PG8_STAGE(PG8_SA(0, 0), a2, vA2[0]);
;             PG8_WAIT_V(8); PG8_WAIT_L(0); PG8_BAR; PG8_MMA(1, 0, At, B0); PG8_MMA(1, 1, At, B1); PG8_BAR; PG8_SCHED;
;             PG8_LDB(B0, 1, 0); PG8_LDB(B1, 1, 1); PG8_SCHED; PG8_LDA(At, 1, 0); PG8_STAGE(PG8_SA(0, 1), a2, vA2[1]);
;             PG8_WAIT_V(8); PG8_WAIT_L(0); PG8_BAR; PG8_MMA(0, 0, At, B0); PG8_MMA(0, 1, At, B1); PG8_BAR; PG8_SCHED;
;             PG8_LDA(At, 1, 1); PG8_STAGE(PG8_SB(1, 0), b3, voffB[0]); PG8_STAGE(PG8_SB(1, 1), b3, voffB[1]); PG8_STAGE(PG8_SA(1, 0), a3, vA2[0]);
;             PG8_WAIT_V(8); PG8_WAIT_L(0); PG8_BAR; PG8_MMA(1, 0, At, B0); PG8_MMA(1, 1, At, B1); PG8_BAR; PG8_SCHED;
	s_setprio 2
	v_mfma_scale_f32_16x16x128_f8f6f4 v[138:141], v[142:149], v[210:217], v[138:141], v199, v199 op_sel_hi:[0,0,0]
	v_mfma_scale_f32_16x16x128_f8f6f4 v[134:137], v[150:157], v[210:217], v[134:137], v199, v199 op_sel_hi:[0,0,0]
	v_mfma_scale_f32_16x16x128_f8f6f4 v[130:133], v[142:149], v[218:225], v[130:133], v199, v199 op_sel_hi:[0,0,0]
	v_mfma_scale_f32_16x16x128_f8f6f4 v[126:129], v[150:157], v[218:225], v[126:129], v199, v199 op_sel_hi:[0,0,0]
	v_mfma_scale_f32_16x16x128_f8f6f4 v[122:125], v[142:149], v[226:233], v[122:125], v199, v199 op_sel_hi:[0,0,0]
	v_mfma_scale_f32_16x16x128_f8f6f4 v[118:121], v[150:157], v[226:233], v[118:121], v199, v199 op_sel_hi:[0,0,0]
	v_mfma_scale_f32_16x16x128_f8f6f4 v[114:117], v[142:149], v[234:241], v[114:117], v199, v199 op_sel_hi:[0,0,0]
	v_mfma_scale_f32_16x16x128_f8f6f4 v[110:113], v[150:157], v[234:241], v[110:113], v199, v199 op_sel_hi:[0,0,0]
	s_nop 3
	s_setprio 0
	s_setprio 2
	v_mfma_scale_f32_16x16x128_f8f6f4 v[106:109], v[2:9], v[210:217], v[106:109], v199, v199 op_sel_hi:[0,0,0]
	v_mfma_scale_f32_16x16x128_f8f6f4 v[102:105], v[202:209], v[210:217], v[102:105], v199, v199 op_sel_hi:[0,0,0]
	v_mfma_scale_f32_16x16x128_f8f6f4 v[98:101], v[2:9], v[218:225], v[98:101], v199, v199 op_sel_hi:[0,0,0]
	v_mfma_scale_f32_16x16x128_f8f6f4 v[94:97], v[202:209], v[218:225], v[94:97], v199, v199 op_sel_hi:[0,0,0]
	v_mfma_scale_f32_16x16x128_f8f6f4 v[90:93], v[2:9], v[226:233], v[90:93], v199, v199 op_sel_hi:[0,0,0]
	v_mfma_scale_f32_16x16x128_f8f6f4 v[86:89], v[202:209], v[226:233], v[86:89], v199, v199 op_sel_hi:[0,0,0]
	v_mfma_scale_f32_16x16x128_f8f6f4 v[82:85], v[2:9], v[234:241], v[82:85], v199, v199 op_sel_hi:[0,0,0]
	v_mfma_scale_f32_16x16x128_f8f6f4 v[78:81], v[202:209], v[234:241], v[78:81], v199, v199 op_sel_hi:[0,0,0]
	s_setprio 0
	s_add_u32 s28, s28, 0x8000
	s_addc_u32 s29, s29, 0
	s_add_i32 s30, s78, s44
	v_lshl_add_u64 v[12:13], s[28:29], 0, v[158:159]
	s_mov_b32 m0, s30
	ds_read_b128 v[210:213], v198 offset:49152
	ds_read_b128 v[214:217], v198 offset:50176
	ds_read_b128 v[218:221], v198 offset:51200
	ds_read_b128 v[222:225], v198 offset:52224
	ds_read_b128 v[226:229], v198 offset:53248
	ds_read_b128 v[230:233], v198 offset:54272
	ds_read_b128 v[234:237], v198 offset:55296
	ds_read_b128 v[238:241], v198 offset:56320
	global_load_lds_dwordx4 v[12:13], off
	v_lshl_add_u64 v[12:13], s[28:29], 0, v[160:161]
	s_add_i32 m0, s30, 0x2000
	s_add_i32 s30, s79, s44
	global_load_lds_dwordx4 v[12:13], off
	v_lshl_add_u64 v[12:13], s[28:29], 0, v[172:173]
	s_mov_b32 m0, s30
	s_nop 0
	global_load_lds_dwordx4 v[12:13], off
	v_lshl_add_u64 v[12:13], s[28:29], 0, v[174:175]
	s_add_i32 m0, s30, 0x2000
	s_nop 0
	global_load_lds_dwordx4 v[12:13], off
	v_lshl_add_u64 v[12:13], s[26:27], 0, v[162:163]
	s_mov_b32 m0, s50
	s_nop 0
	global_load_lds_dwordx4 v[12:13], off
	v_lshl_add_u64 v[12:13], s[26:27], 0, v[164:165]
	s_mov_b32 m0, s51
	s_nop 0
	global_load_lds_dwordx4 v[12:13], off
	s_waitcnt vmcnt(8)
	s_waitcnt lgkmcnt(0)
	s_barrier
	s_setprio 2
	v_mfma_scale_f32_16x16x128_f8f6f4 v[74:77], v[142:149], v[210:217], v[74:77], v199, v199 op_sel_hi:[0,0,0]
	v_mfma_scale_f32_16x16x128_f8f6f4 v[70:73], v[150:157], v[210:217], v[70:73], v199, v199 op_sel_hi:[0,0,0]
	v_mfma_scale_f32_16x16x128_f8f6f4 v[66:69], v[142:149], v[218:225], v[66:69], v199, v199 op_sel_hi:[0,0,0]
	v_mfma_scale_f32_16x16x128_f8f6f4 v[62:65], v[150:157], v[218:225], v[62:65], v199, v199 op_sel_hi:[0,0,0]
	v_mfma_scale_f32_16x16x128_f8f6f4 v[58:61], v[142:149], v[226:233], v[58:61], v199, v199 op_sel_hi:[0,0,0]
	v_mfma_scale_f32_16x16x128_f8f6f4 v[54:57], v[150:157], v[226:233], v[54:57], v199, v199 op_sel_hi:[0,0,0]
	v_mfma_scale_f32_16x16x128_f8f6f4 v[50:53], v[142:149], v[234:241], v[50:53], v199, v199 op_sel_hi:[0,0,0]
	v_mfma_scale_f32_16x16x128_f8f6f4 v[46:49], v[150:157], v[234:241], v[46:49], v199, v199 op_sel_hi:[0,0,0]
	s_nop 3
	s_setprio 0
	s_setprio 2
	v_mfma_scale_f32_16x16x128_f8f6f4 v[42:45], v[2:9], v[210:217], v[42:45], v199, v199 op_sel_hi:[0,0,0]
	v_mfma_scale_f32_16x16x128_f8f6f4 v[38:41], v[202:209], v[210:217], v[38:41], v199, v199 op_sel_hi:[0,0,0]
	v_mfma_scale_f32_16x16x128_f8f6f4 v[34:37], v[2:9], v[218:225], v[34:37], v199, v199 op_sel_hi:[0,0,0]
	v_mfma_scale_f32_16x16x128_f8f6f4 v[30:33], v[202:209], v[218:225], v[30:33], v199, v199 op_sel_hi:[0,0,0]
	v_mfma_scale_f32_16x16x128_f8f6f4 v[26:29], v[2:9], v[226:233], v[26:29], v199, v199 op_sel_hi:[0,0,0]
	v_mfma_scale_f32_16x16x128_f8f6f4 v[22:25], v[202:209], v[226:233], v[22:25], v199, v199 op_sel_hi:[0,0,0]
	v_mfma_scale_f32_16x16x128_f8f6f4 v[18:21], v[2:9], v[234:241], v[18:21], v199, v199 op_sel_hi:[0,0,0]
	v_mfma_scale_f32_16x16x128_f8f6f4 v[14:17], v[202:209], v[234:241], v[14:17], v199, v199 op_sel_hi:[0,0,0]
	s_setprio 0
	s_add_u32 s75, s75, 0x10000
	s_addc_u32 s76, s76, 0
	s_add_u32 s24, s24, 0x10000
	s_addc_u32 s25, s25, 0
	s_cmp_ge_i32 s77, s72
	s_mov_b32 s26, s77
	s_cbranch_scc0 .Lh1_834

; #define PG8_STAGE(bufoff, gbase, voff) do { _Pragma("unroll") for (int _i = 0; _i < 2; ++_i) \
;         __builtin_amdgcn_global_load_lds((const unsigned*)((const char*)(gbase) + (voff)[_i]), (PG8_LAS unsigned*)(lds + (bufoff) + ldsw + _i * 8192), 16, 0, 0); } while (0)
; #define PG8_WAIT_V(n) asm volatile("s_waitcnt vmcnt(" #n ")" ::: "memory")
; #define PG8_WAIT_L(n) asm volatile("s_waitcnt lgkmcnt(" #n ")" ::: "memory")
; #define PG8_BAR __builtin_amdgcn_s_barrier()
; #define PG8_SCHED __builtin_amdgcn_sched_barrier(0)
; template <class Epi, class Sched, bool ALIGN_EPI = true, bool F8 = false>
; __device__ __forceinline__ void gemm_phase(PG8_LAS unsigned char* lds, const Sched& S, const Epi& E) {
;     ...
;             PG8_LDB(B0, 0, 0); PG8_LDB(B1, 0, 1); PG8_SCHED; PG8_LDA(At, 0, 0); PG8_STAGE(PG8_SA(1, 1), a1, voffA[1]);
;             PG8_WAIT_V(8); PG8_WAIT_L(0); PG8_BAR; PG8_MMA(0, 0, At, B0); PG8_MMA(0, 1, At, B1); PG8_BAR; PG8_SCHED;
;             PG8_LDA(At, 0, 1); PG8_STAGE(PG8_SB(0, 0), b2, voffB[0]); PG8_STAGE(PG8_SB(0, 1), b2, voffB[1]); PG8_STAGE(PG8_SA(0, 0), a2, vA2[0]);
;             PG8_WAIT_V(8); PG8_WAIT_L(0); PG8_BAR; PG8_MMA(1, 0, At, B0); PG8_MMA(1, 1, At, B1); PG8_BAR; PG8_SCHED;
;             PG8_LDB(B0, 1, 0); PG8_LDB(B1, 1, 1); PG8_SCHED; PG8_LDA(At, 1, 0); PG8_STAGE(PG8_SA(0, 1), a2, vA2[1]);
;             PG8_WAIT_V(8); PG8_WAIT_L(0); PG8_BAR; PG8_MMA(0, 0, At, B0); PG8_MMA(0, 1, At, B1); PG8_BAR; PG8_SCHED;
.LBB0_911:
	ds_read_b128 v[18:21], v191
	ds_read_b128 v[22:25], v191 offset:1024
	ds_read_b128 v[26:29], v191 offset:2048
	ds_read_b128 v[30:33], v191 offset:3072
	ds_read_b128 v[2:5], v192
	ds_read_b128 v[6:9], v192 offset:1024
	ds_read_b128 v[10:13], v192 offset:2048
	ds_read_b128 v[14:17], v192 offset:3072
	s_add_u32 s30, s28, 0x8000
	s_addc_u32 s31, s29, 0
	s_cmp_eq_u32 s65, 12
	s_cselect_b32 s42, s22, s30
	s_cselect_b32 s43, s23, s31
	s_cselect_b32 s40, s24, s19
	s_cselect_b32 s41, s25, s21
	s_add_u32 s30, s42, 0x8000
	s_addc_u32 s31, s43, 0
	v_lshl_add_u64 v[228:229], s[28:29], 0, v[182:183]
	s_add_i32 m0, s27, 0xc000
	ds_read_b128 v[196:199], v193
	ds_read_b128 v[200:203], v193 offset:1024
	ds_read_b128 v[204:207], v193 offset:2048
	ds_read_b128 v[208:211], v193 offset:3072
	ds_read_b128 v[212:215], v193 offset:4096
	ds_read_b128 v[216:219], v193 offset:5120
	ds_read_b128 v[220:223], v193 offset:6144
	ds_read_b128 v[224:227], v193 offset:7168
	global_load_lds_dwordx4 v[228:229], off
	v_lshl_add_u64 v[228:229], s[28:29], 0, v[180:181]
	s_add_i32 m0, s27, 0xe000
	s_nop 0
	global_load_lds_dwordx4 v[228:229], off
	s_waitcnt vmcnt(8)
	s_waitcnt lgkmcnt(0)
	s_setprio 1
	v_mfma_scale_f32_16x16x128_f8f6f4 v[158:161], v[18:25], v[196:203], v[158:161], v194, v194 op_sel_hi:[0,0,0]
	v_mfma_scale_f32_16x16x128_f8f6f4 v[154:157], v[26:33], v[196:203], v[154:157], v194, v194 op_sel_hi:[0,0,0]
	v_mfma_scale_f32_16x16x128_f8f6f4 v[150:153], v[18:25], v[204:211], v[150:153], v194, v194 op_sel_hi:[0,0,0]
	v_mfma_scale_f32_16x16x128_f8f6f4 v[146:149], v[26:33], v[204:211], v[146:149], v194, v194 op_sel_hi:[0,0,0]
	v_mfma_scale_f32_16x16x128_f8f6f4 v[130:133], v[18:25], v[212:219], v[130:133], v194, v194 op_sel_hi:[0,0,0]
	v_mfma_scale_f32_16x16x128_f8f6f4 v[122:125], v[26:33], v[212:219], v[122:125], v194, v194 op_sel_hi:[0,0,0]
	v_mfma_scale_f32_16x16x128_f8f6f4 v[114:117], v[18:25], v[220:227], v[114:117], v194, v194 op_sel_hi:[0,0,0]
	v_mfma_scale_f32_16x16x128_f8f6f4 v[106:109], v[26:33], v[220:227], v[106:109], v194, v194 op_sel_hi:[0,0,0]
	s_nop 3
	s_setprio 0
	s_setprio 1
	v_mfma_scale_f32_16x16x128_f8f6f4 v[142:145], v[2:9], v[196:203], v[142:145], v194, v194 op_sel_hi:[0,0,0]
	v_mfma_scale_f32_16x16x128_f8f6f4 v[138:141], v[10:17], v[196:203], v[138:141], v194, v194 op_sel_hi:[0,0,0]
	v_mfma_scale_f32_16x16x128_f8f6f4 v[134:137], v[2:9], v[204:211], v[134:137], v194, v194 op_sel_hi:[0,0,0]
	v_mfma_scale_f32_16x16x128_f8f6f4 v[126:129], v[10:17], v[204:211], v[126:129], v194, v194 op_sel_hi:[0,0,0]
	v_mfma_scale_f32_16x16x128_f8f6f4 v[118:121], v[2:9], v[212:219], v[118:121], v194, v194 op_sel_hi:[0,0,0]
	v_mfma_scale_f32_16x16x128_f8f6f4 v[110:113], v[10:17], v[212:219], v[110:113], v194, v194 op_sel_hi:[0,0,0]
	v_mfma_scale_f32_16x16x128_f8f6f4 v[102:105], v[2:9], v[220:227], v[102:105], v194, v194 op_sel_hi:[0,0,0]
	v_mfma_scale_f32_16x16x128_f8f6f4 v[98:101], v[10:17], v[220:227], v[98:101], v194, v194 op_sel_hi:[0,0,0]
	s_setprio 0
	s_barrier
	s_add_i32 s66, s60, s48
	v_lshl_add_u64 v[228:229], s[40:41], 0, v[162:163]
	s_mov_b32 m0, s66
	ds_read_b128 v[196:199], v193 offset:16384
	ds_read_b128 v[200:203], v193 offset:17408
	ds_read_b128 v[204:207], v193 offset:18432
	ds_read_b128 v[208:211], v193 offset:19456
	ds_read_b128 v[212:215], v193 offset:20480
	ds_read_b128 v[216:219], v193 offset:21504
	ds_read_b128 v[220:223], v193 offset:22528
	ds_read_b128 v[224:227], v193 offset:23552
	global_load_lds_dwordx4 v[228:229], off
	v_lshl_add_u64 v[230:231], s[40:41], 0, v[164:165]
	s_add_i32 m0, s66, 0x2000
	s_add_i32 s66, s61, s48
	global_load_lds_dwordx4 v[230:231], off
	v_lshl_add_u64 v[228:229], v[228:229], 0, s[6:7]
	s_mov_b32 m0, s66
	s_nop 0
	global_load_lds_dwordx4 v[228:229], off
	v_lshl_add_u64 v[228:229], v[230:231], 0, s[6:7]
	s_add_i32 m0, s66, 0x2000
	s_nop 0
	global_load_lds_dwordx4 v[228:229], off
	v_lshl_add_u64 v[228:229], s[42:43], 0, v[166:167]
	s_mov_b32 m0, s27
	s_nop 0
	global_load_lds_dwordx4 v[228:229], off
	v_lshl_add_u64 v[228:229], s[42:43], 0, v[168:169]
	s_mov_b32 m0, s49
	s_nop 0
	global_load_lds_dwordx4 v[228:229], off
	s_waitcnt vmcnt(8)
	s_waitcnt lgkmcnt(0)
	s_setprio 1
	v_mfma_scale_f32_16x16x128_f8f6f4 v[94:97], v[18:25], v[196:203], v[94:97], v194, v194 op_sel_hi:[0,0,0]
	v_mfma_scale_f32_16x16x128_f8f6f4 v[90:93], v[26:33], v[196:203], v[90:93], v194, v194 op_sel_hi:[0,0,0]
	v_mfma_scale_f32_16x16x128_f8f6f4 v[82:85], v[18:25], v[204:211], v[82:85], v194, v194 op_sel_hi:[0,0,0]
	v_mfma_scale_f32_16x16x128_f8f6f4 v[74:77], v[26:33], v[204:211], v[74:77], v194, v194 op_sel_hi:[0,0,0]
	v_mfma_scale_f32_16x16x128_f8f6f4 v[66:69], v[18:25], v[212:219], v[66:69], v194, v194 op_sel_hi:[0,0,0]
	v_mfma_scale_f32_16x16x128_f8f6f4 v[58:61], v[26:33], v[212:219], v[58:61], v194, v194 op_sel_hi:[0,0,0]
	v_mfma_scale_f32_16x16x128_f8f6f4 v[50:53], v[18:25], v[220:227], v[50:53], v194, v194 op_sel_hi:[0,0,0]
	v_mfma_scale_f32_16x16x128_f8f6f4 v[42:45], v[26:33], v[220:227], v[42:45], v194, v194 op_sel_hi:[0,0,0]
	s_nop 3
	s_setprio 0
	s_setprio 1
	v_mfma_scale_f32_16x16x128_f8f6f4 v[86:89], v[2:9], v[196:203], v[86:89], v194, v194 op_sel_hi:[0,0,0]
	v_mfma_scale_f32_16x16x128_f8f6f4 v[78:81], v[10:17], v[196:203], v[78:81], v194, v194 op_sel_hi:[0,0,0]
	v_mfma_scale_f32_16x16x128_f8f6f4 v[70:73], v[2:9], v[204:211], v[70:73], v194, v194 op_sel_hi:[0,0,0]
	v_mfma_scale_f32_16x16x128_f8f6f4 v[62:65], v[10:17], v[204:211], v[62:65], v194, v194 op_sel_hi:[0,0,0]
	v_mfma_scale_f32_16x16x128_f8f6f4 v[54:57], v[2:9], v[212:219], v[54:57], v194, v194 op_sel_hi:[0,0,0]
	v_mfma_scale_f32_16x16x128_f8f6f4 v[46:49], v[10:17], v[212:219], v[46:49], v194, v194 op_sel_hi:[0,0,0]
	v_mfma_scale_f32_16x16x128_f8f6f4 v[38:41], v[2:9], v[220:227], v[38:41], v194, v194 op_sel_hi:[0,0,0]
	v_mfma_scale_f32_16x16x128_f8f6f4 v[34:37], v[10:17], v[220:227], v[34:37], v194, v194 op_sel_hi:[0,0,0]
	s_setprio 0
	s_barrier
; #define PG8_STAGE(bufoff, gbase, voff) do { _Pragma("unroll") for (int _i = 0; _i < 2; ++_i) \
;         __builtin_amdgcn_global_load_lds((const unsigned*)((const char*)(gbase) + (voff)[_i]), (PG8_LAS unsigned*)(lds + (bufoff) + ldsw + _i * 8192), 16, 0, 0); } while (0)
; #define PG8_WAIT_V(n) asm volatile("s_waitcnt vmcnt(" #n ")" ::: "memory")
; #define PG8_WAIT_L(n) asm volatile("s_waitcnt lgkmcnt(" #n ")" ::: "memory")
; #define PG8_BAR __builtin_amdgcn_s_barrier()
; #define PG8_SCHED __builtin_amdgcn_sched_barrier(0)
; template <class Epi, class Sched, bool ALIGN_EPI = true, bool F8 = false>
; __device__ __forceinline__ void gemm_phase(PG8_LAS unsigned char* lds, const Sched& S, const Epi& E) {
;     ...
;         for (int t = 0; t < nt; t += 2) {
;             const bool last = (t == nt - 2);
;             if constexpr (Sched::GATHER) { if (last && has_next) S.a_off(nxt, Rs, Cs, voffAn); }
;             const char* a1 = cA + (size_t)(t + 1) * kstep;
;             const char* a2 = last ? nA : cA + (size_t)(t + 2) * kstep; const char* b2 = last ? nB : cB + (size_t)(t + 2) * kstepB;
;     ...
;             PG8_LDB(B0, 1, 0); PG8_LDB(B1, 1, 1); PG8_SCHED; PG8_LDA(At, 1, 0); PG8_STAGE(PG8_SA(0, 1), a2, vA2[1]);
;             PG8_WAIT_V(8); PG8_WAIT_L(0); PG8_BAR; PG8_MMA(0, 0, At, B0); PG8_MMA(0, 1, At, B1); PG8_BAR; PG8_SCHED;
;             PG8_LDA(At, 1, 1); PG8_STAGE(PG8_SB(1, 0), b3, voffB[0]); PG8_STAGE(PG8_SB(1, 1), b3, voffB[1]); PG8_STAGE(PG8_SA(1, 0), a3, vA2[0]);
;             PG8_WAIT_V(8); PG8_WAIT_L(0); PG8_BAR; PG8_MMA(1, 0, At, B0); PG8_MMA(1, 1, At, B1); PG8_BAR; PG8_SCHED;
	s_add_i32 s66, 0, 0x18000
	s_add_i32 s67, 0, 0x1c000
	v_add_u32_e32 v14, s66, v189
	v_add_u32_e32 v30, s67, v189
	ds_read_b128 v[2:5], v14
	ds_read_b128 v[6:9], v14 offset:1024
	ds_read_b128 v[10:13], v14 offset:2048
	ds_read_b128 v[14:17], v14 offset:3072
	ds_read_b128 v[18:21], v30
	ds_read_b128 v[22:25], v30 offset:1024
	ds_read_b128 v[26:29], v30 offset:2048
	ds_read_b128 v[30:33], v30 offset:3072
	s_mov_b32 m0, s50
	v_lshl_add_u64 v[228:229], s[42:43], 0, v[172:173]
	ds_read_b128 v[196:199], v193 offset:32768
	ds_read_b128 v[200:203], v193 offset:33792
	ds_read_b128 v[204:207], v193 offset:34816
	ds_read_b128 v[208:211], v193 offset:35840
	ds_read_b128 v[212:215], v193 offset:36864
	ds_read_b128 v[216:219], v193 offset:37888
	ds_read_b128 v[220:223], v193 offset:38912
	ds_read_b128 v[224:227], v193 offset:39936
	global_load_lds_dwordx4 v[228:229], off
	v_lshl_add_u64 v[228:229], s[42:43], 0, v[174:175]
	s_mov_b32 m0, s51
	s_nop 0
	global_load_lds_dwordx4 v[228:229], off
	s_waitcnt vmcnt(8)
	s_waitcnt lgkmcnt(0)
	s_setprio 1
	v_mfma_scale_f32_16x16x128_f8f6f4 v[158:161], v[2:9], v[196:203], v[158:161], v194, v194 op_sel_hi:[0,0,0]
	v_mfma_scale_f32_16x16x128_f8f6f4 v[154:157], v[10:17], v[196:203], v[154:157], v194, v194 op_sel_hi:[0,0,0]
	v_mfma_scale_f32_16x16x128_f8f6f4 v[150:153], v[2:9], v[204:211], v[150:153], v194, v194 op_sel_hi:[0,0,0]
	v_mfma_scale_f32_16x16x128_f8f6f4 v[146:149], v[10:17], v[204:211], v[146:149], v194, v194 op_sel_hi:[0,0,0]
	v_mfma_scale_f32_16x16x128_f8f6f4 v[130:133], v[2:9], v[212:219], v[130:133], v194, v194 op_sel_hi:[0,0,0]
	v_mfma_scale_f32_16x16x128_f8f6f4 v[122:125], v[10:17], v[212:219], v[122:125], v194, v194 op_sel_hi:[0,0,0]
	v_mfma_scale_f32_16x16x128_f8f6f4 v[114:117], v[2:9], v[220:227], v[114:117], v194, v194 op_sel_hi:[0,0,0]
	v_mfma_scale_f32_16x16x128_f8f6f4 v[106:109], v[10:17], v[220:227], v[106:109], v194, v194 op_sel_hi:[0,0,0]
	s_nop 3
	s_setprio 0
	s_setprio 1
	v_mfma_scale_f32_16x16x128_f8f6f4 v[142:145], v[18:25], v[196:203], v[142:145], v194, v194 op_sel_hi:[0,0,0]
	v_mfma_scale_f32_16x16x128_f8f6f4 v[138:141], v[26:33], v[196:203], v[138:141], v194, v194 op_sel_hi:[0,0,0]
	v_mfma_scale_f32_16x16x128_f8f6f4 v[134:137], v[18:25], v[204:211], v[134:137], v194, v194 op_sel_hi:[0,0,0]
	v_mfma_scale_f32_16x16x128_f8f6f4 v[126:129], v[26:33], v[204:211], v[126:129], v194, v194 op_sel_hi:[0,0,0]
	v_mfma_scale_f32_16x16x128_f8f6f4 v[118:121], v[18:25], v[212:219], v[118:121], v194, v194 op_sel_hi:[0,0,0]
	v_mfma_scale_f32_16x16x128_f8f6f4 v[110:113], v[26:33], v[212:219], v[110:113], v194, v194 op_sel_hi:[0,0,0]
	v_mfma_scale_f32_16x16x128_f8f6f4 v[102:105], v[18:25], v[220:227], v[102:105], v194, v194 op_sel_hi:[0,0,0]
	v_mfma_scale_f32_16x16x128_f8f6f4 v[98:101], v[26:33], v[220:227], v[98:101], v194, v194 op_sel_hi:[0,0,0]
	s_setprio 0
	s_barrier
	s_add_u32 s40, s40, 0x8000
	s_addc_u32 s41, s41, 0
	s_add_i32 s42, s66, s48
	v_lshl_add_u64 v[228:229], s[40:41], 0, v[162:163]
	s_mov_b32 m0, s42
	ds_read_b128 v[196:199], v193 offset:49152
	ds_read_b128 v[200:203], v193 offset:50176
	ds_read_b128 v[204:207], v193 offset:51200
	ds_read_b128 v[208:211], v193 offset:52224
	ds_read_b128 v[212:215], v193 offset:53248
	ds_read_b128 v[216:219], v193 offset:54272
	ds_read_b128 v[220:223], v193 offset:55296
	ds_read_b128 v[224:227], v193 offset:56320
	global_load_lds_dwordx4 v[228:229], off
	v_lshl_add_u64 v[228:229], s[40:41], 0, v[164:165]
	s_add_i32 m0, s42, 0x2000
	s_add_i32 s42, s67, s48
	global_load_lds_dwordx4 v[228:229], off
	v_lshl_add_u64 v[228:229], s[40:41], 0, v[176:177]
	s_mov_b32 m0, s42
	s_nop 0
	global_load_lds_dwordx4 v[228:229], off
	v_lshl_add_u64 v[228:229], s[40:41], 0, v[178:179]
	s_add_i32 m0, s42, 0x2000
	s_nop 0
	global_load_lds_dwordx4 v[228:229], off
	v_lshl_add_u64 v[228:229], s[30:31], 0, v[166:167]
	s_mov_b32 m0, s53
	s_nop 0
	global_load_lds_dwordx4 v[228:229], off
	v_lshl_add_u64 v[228:229], s[30:31], 0, v[168:169]
	s_mov_b32 m0, s58
	s_nop 0
	global_load_lds_dwordx4 v[228:229], off
	s_waitcnt vmcnt(8)
	s_waitcnt lgkmcnt(0)
	s_setprio 1
	v_mfma_scale_f32_16x16x128_f8f6f4 v[94:97], v[2:9], v[196:203], v[94:97], v194, v194 op_sel_hi:[0,0,0]
	v_mfma_scale_f32_16x16x128_f8f6f4 v[90:93], v[10:17], v[196:203], v[90:93], v194, v194 op_sel_hi:[0,0,0]
	v_mfma_scale_f32_16x16x128_f8f6f4 v[82:85], v[2:9], v[204:211], v[82:85], v194, v194 op_sel_hi:[0,0,0]
	v_mfma_scale_f32_16x16x128_f8f6f4 v[74:77], v[10:17], v[204:211], v[74:77], v194, v194 op_sel_hi:[0,0,0]
	v_mfma_scale_f32_16x16x128_f8f6f4 v[66:69], v[2:9], v[212:219], v[66:69], v194, v194 op_sel_hi:[0,0,0]
	v_mfma_scale_f32_16x16x128_f8f6f4 v[58:61], v[10:17], v[212:219], v[58:61], v194, v194 op_sel_hi:[0,0,0]
	v_mfma_scale_f32_16x16x128_f8f6f4 v[50:53], v[2:9], v[220:227], v[50:53], v194, v194 op_sel_hi:[0,0,0]
	v_mfma_scale_f32_16x16x128_f8f6f4 v[42:45], v[10:17], v[220:227], v[42:45], v194, v194 op_sel_hi:[0,0,0]
	s_nop 3
	s_setprio 0
	s_setprio 1
	v_mfma_scale_f32_16x16x128_f8f6f4 v[86:89], v[18:25], v[196:203], v[86:89], v194, v194 op_sel_hi:[0,0,0]
	v_mfma_scale_f32_16x16x128_f8f6f4 v[78:81], v[26:33], v[196:203], v[78:81], v194, v194 op_sel_hi:[0,0,0]
	v_mfma_scale_f32_16x16x128_f8f6f4 v[70:73], v[18:25], v[204:211], v[70:73], v194, v194 op_sel_hi:[0,0,0]
	v_mfma_scale_f32_16x16x128_f8f6f4 v[62:65], v[26:33], v[204:211], v[62:65], v194, v194 op_sel_hi:[0,0,0]
	v_mfma_scale_f32_16x16x128_f8f6f4 v[54:57], v[18:25], v[212:219], v[54:57], v194, v194 op_sel_hi:[0,0,0]
	v_mfma_scale_f32_16x16x128_f8f6f4 v[46:49], v[26:33], v[212:219], v[46:49], v194, v194 op_sel_hi:[0,0,0]
	v_mfma_scale_f32_16x16x128_f8f6f4 v[38:41], v[18:25], v[220:227], v[38:41], v194, v194 op_sel_hi:[0,0,0]
	v_mfma_scale_f32_16x16x128_f8f6f4 v[34:37], v[26:33], v[220:227], v[34:37], v194, v194 op_sel_hi:[0,0,0]
	s_setprio 0
	s_barrier
	s_add_i32 s65, s65, 2
	s_add_u32 s19, s19, 0x10000
	s_addc_u32 s21, s21, 0
	s_add_u32 s28, s28, 0x10000
	s_addc_u32 s29, s29, 0
	s_cmp_gt_u32 s65, 13
	s_cbranch_scc0 .LBB0_911
	s_branch .Lfx_26630
; #define PG8_STAGE(bufoff, gbase, voff) do { _Pragma("unroll") for (int _i = 0; _i < 2; ++_i) \
;         __builtin_amdgcn_global_load_lds((const unsigned*)((const char*)(gbase) + (voff)[_i]), (PG8_LAS unsigned*)(lds + (bufoff) + ldsw + _i * 8192), 16, 0, 0); } while (0)
; #define PG8_WAIT_V(n) asm volatile("s_waitcnt vmcnt(" #n ")" ::: "memory")
; #define PG8_WAIT_L(n) asm volatile("s_waitcnt lgkmcnt(" #n ")" ::: "memory")
; #define PG8_BAR __builtin_amdgcn_s_barrier()
; #define PG8_SCHED __builtin_amdgcn_sched_barrier(0)
; template <class Epi, class Sched, bool ALIGN_EPI = true, bool F8 = false>
; __device__ __forceinline__ void gemm_phase(PG8_LAS unsigned char* lds, const Sched& S, const Epi& E) {
;     ...
;             PG8_LDB(B0, 0, 0); PG8_LDB(B1, 0, 1); PG8_SCHED; PG8_LDA(At, 0, 0); PG8_STAGE(PG8_SA(1, 1), a1, voffA[1]);
;             PG8_WAIT_V(8); PG8_WAIT_L(0); PG8_BAR; PG8_MMA(0, 0, At, B0); PG8_MMA(0, 1, At, B1); PG8_BAR; PG8_SCHED;
;             PG8_LDA(At, 0, 1); PG8_STAGE(PG8_SB(0, 0), b2, voffB[0]); PG8_STAGE(PG8_SB(0, 1), b2, voffB[1]); PG8_STAGE(PG8_SA(0, 0), a2, vA2[0]);
;             PG8_WAIT_V(8); PG8_WAIT_L(0); PG8_BAR; PG8_MMA(1, 0, At, B0); PG8_MMA(1, 1, At, B1); PG8_BAR; PG8_SCHED;
;             PG8_LDB(B0, 1, 0); PG8_LDB(B1, 1, 1); PG8_SCHED; PG8_LDA(At, 1, 0); PG8_STAGE(PG8_SA(0, 1), a2, vA2[1]);
;             PG8_WAIT_V(8); PG8_WAIT_L(0); PG8_BAR; PG8_MMA(0, 0, At, B0); PG8_MMA(0, 1, At, B1); PG8_BAR; PG8_SCHED;
;             PG8_LDA(At, 1, 1); PG8_STAGE(PG8_SB(1, 0), b3, voffB[0]); PG8_STAGE(PG8_SB(1, 1), b3, voffB[1]); PG8_STAGE(PG8_SA(1, 0), a3, vA2[0]);
;             PG8_WAIT_V(8); PG8_WAIT_L(0); PG8_BAR; PG8_MMA(1, 0, At, B0); PG8_MMA(1, 1, At, B1); PG8_BAR; PG8_SCHED;
.Lh1e_26630:
.Lh1_911:
	ds_read_b128 v[18:21], v191
	ds_read_b128 v[22:25], v191 offset:1024
	ds_read_b128 v[26:29], v191 offset:2048
	ds_read_b128 v[30:33], v191 offset:3072
	ds_read_b128 v[2:5], v192
	ds_read_b128 v[6:9], v192 offset:1024
	ds_read_b128 v[10:13], v192 offset:2048
	ds_read_b128 v[14:17], v192 offset:3072
	s_add_u32 s30, s28, 0x8000
	s_addc_u32 s31, s29, 0
	s_cmp_eq_u32 s65, 12
	s_cselect_b32 s42, s22, s30
	s_cselect_b32 s43, s23, s31
	s_cselect_b32 s40, s24, s19
	s_cselect_b32 s41, s25, s21
	s_add_u32 s30, s42, 0x8000
	s_addc_u32 s31, s43, 0
	v_lshl_add_u64 v[228:229], s[28:29], 0, v[182:183]
	s_add_i32 m0, s27, 0xc000
	ds_read_b128 v[196:199], v193
	ds_read_b128 v[200:203], v193 offset:1024
	ds_read_b128 v[204:207], v193 offset:2048
	ds_read_b128 v[208:211], v193 offset:3072
	ds_read_b128 v[212:215], v193 offset:4096
	ds_read_b128 v[216:219], v193 offset:5120
	ds_read_b128 v[220:223], v193 offset:6144
	ds_read_b128 v[224:227], v193 offset:7168
	global_load_lds_dwordx4 v[228:229], off
	v_lshl_add_u64 v[228:229], s[28:29], 0, v[180:181]
	s_add_i32 m0, s27, 0xe000
	s_nop 0
	global_load_lds_dwordx4 v[228:229], off
	s_waitcnt vmcnt(8)
	s_waitcnt lgkmcnt(0)
	s_barrier
	s_setprio 2
	v_mfma_scale_f32_16x16x128_f8f6f4 v[158:161], v[18:25], v[196:203], v[158:161], v194, v194 op_sel_hi:[0,0,0]
	v_mfma_scale_f32_16x16x128_f8f6f4 v[154:157], v[26:33], v[196:203], v[154:157], v194, v194 op_sel_hi:[0,0,0]
	v_mfma_scale_f32_16x16x128_f8f6f4 v[150:153], v[18:25], v[204:211], v[150:153], v194, v194 op_sel_hi:[0,0,0]
	v_mfma_scale_f32_16x16x128_f8f6f4 v[146:149], v[26:33], v[204:211], v[146:149], v194, v194 op_sel_hi:[0,0,0]
	v_mfma_scale_f32_16x16x128_f8f6f4 v[130:133], v[18:25], v[212:219], v[130:133], v194, v194 op_sel_hi:[0,0,0]
	v_mfma_scale_f32_16x16x128_f8f6f4 v[122:125], v[26:33], v[212:219], v[122:125], v194, v194 op_sel_hi:[0,0,0]
	v_mfma_scale_f32_16x16x128_f8f6f4 v[114:117], v[18:25], v[220:227], v[114:117], v194, v194 op_sel_hi:[0,0,0]
	v_mfma_scale_f32_16x16x128_f8f6f4 v[106:109], v[26:33], v[220:227], v[106:109], v194, v194 op_sel_hi:[0,0,0]
	s_nop 3
	s_setprio 0
	s_setprio 2
	v_mfma_scale_f32_16x16x128_f8f6f4 v[142:145], v[2:9], v[196:203], v[142:145], v194, v194 op_sel_hi:[0,0,0]
	v_mfma_scale_f32_16x16x128_f8f6f4 v[138:141], v[10:17], v[196:203], v[138:141], v194, v194 op_sel_hi:[0,0,0]
	v_mfma_scale_f32_16x16x128_f8f6f4 v[134:137], v[2:9], v[204:211], v[134:137], v194, v194 op_sel_hi:[0,0,0]
	v_mfma_scale_f32_16x16x128_f8f6f4 v[126:129], v[10:17], v[204:211], v[126:129], v194, v194 op_sel_hi:[0,0,0]
	v_mfma_scale_f32_16x16x128_f8f6f4 v[118:121], v[2:9], v[212:219], v[118:121], v194, v194 op_sel_hi:[0,0,0]
	v_mfma_scale_f32_16x16x128_f8f6f4 v[110:113], v[10:17], v[212:219], v[110:113], v194, v194 op_sel_hi:[0,0,0]
	v_mfma_scale_f32_16x16x128_f8f6f4 v[102:105], v[2:9], v[220:227], v[102:105], v194, v194 op_sel_hi:[0,0,0]
	v_mfma_scale_f32_16x16x128_f8f6f4 v[98:101], v[10:17], v[220:227], v[98:101], v194, v194 op_sel_hi:[0,0,0]
	s_setprio 0
	s_add_i32 s66, s60, s48
	v_lshl_add_u64 v[228:229], s[40:41], 0, v[162:163]
	s_mov_b32 m0, s66
	ds_read_b128 v[196:199], v193 offset:16384
	ds_read_b128 v[200:203], v193 offset:17408
	ds_read_b128 v[204:207], v193 offset:18432
	ds_read_b128 v[208:211], v193 offset:19456
	ds_read_b128 v[212:215], v193 offset:20480
	ds_read_b128 v[216:219], v193 offset:21504
	ds_read_b128 v[220:223], v193 offset:22528
	ds_read_b128 v[224:227], v193 offset:23552
	global_load_lds_dwordx4 v[228:229], off
	v_lshl_add_u64 v[230:231], s[40:41], 0, v[164:165]
	s_add_i32 m0, s66, 0x2000
	s_add_i32 s66, s61, s48
	global_load_lds_dwordx4 v[230:231], off
	v_lshl_add_u64 v[228:229], v[228:229], 0, s[6:7]
	s_mov_b32 m0, s66
	s_nop 0
	global_load_lds_dwordx4 v[228:229], off
	v_lshl_add_u64 v[228:229], v[230:231], 0, s[6:7]
	s_add_i32 m0, s66, 0x2000
	s_nop 0
	global_load_lds_dwordx4 v[228:229], off
	v_lshl_add_u64 v[228:229], s[42:43], 0, v[166:167]
	s_mov_b32 m0, s27
	s_nop 0
	global_load_lds_dwordx4 v[228:229], off
	v_lshl_add_u64 v[228:229], s[42:43], 0, v[168:169]
	s_mov_b32 m0, s49
	s_nop 0
	global_load_lds_dwordx4 v[228:229], off
	s_waitcnt vmcnt(8)
	s_waitcnt lgkmcnt(0)
	s_barrier
	s_setprio 2
	v_mfma_scale_f32_16x16x128_f8f6f4 v[94:97], v[18:25], v[196:203], v[94:97], v194, v194 op_sel_hi:[0,0,0]
	v_mfma_scale_f32_16x16x128_f8f6f4 v[90:93], v[26:33], v[196:203], v[90:93], v194, v194 op_sel_hi:[0,0,0]
	v_mfma_scale_f32_16x16x128_f8f6f4 v[82:85], v[18:25], v[204:211], v[82:85], v194, v194 op_sel_hi:[0,0,0]
	v_mfma_scale_f32_16x16x128_f8f6f4 v[74:77], v[26:33], v[204:211], v[74:77], v194, v194 op_sel_hi:[0,0,0]
	v_mfma_scale_f32_16x16x128_f8f6f4 v[66:69], v[18:25], v[212:219], v[66:69], v194, v194 op_sel_hi:[0,0,0]
	v_mfma_scale_f32_16x16x128_f8f6f4 v[58:61], v[26:33], v[212:219], v[58:61], v194, v194 op_sel_hi:[0,0,0]
	v_mfma_scale_f32_16x16x128_f8f6f4 v[50:53], v[18:25], v[220:227], v[50:53], v194, v194 op_sel_hi:[0,0,0]
	v_mfma_scale_f32_16x16x128_f8f6f4 v[42:45], v[26:33], v[220:227], v[42:45], v194, v194 op_sel_hi:[0,0,0]
	s_nop 3
	s_setprio 0
	s_setprio 2
	v_mfma_scale_f32_16x16x128_f8f6f4 v[86:89], v[2:9], v[196:203], v[86:89], v194, v194 op_sel_hi:[0,0,0]
	v_mfma_scale_f32_16x16x128_f8f6f4 v[78:81], v[10:17], v[196:203], v[78:81], v194, v194 op_sel_hi:[0,0,0]
	v_mfma_scale_f32_16x16x128_f8f6f4 v[70:73], v[2:9], v[204:211], v[70:73], v194, v194 op_sel_hi:[0,0,0]
	v_mfma_scale_f32_16x16x128_f8f6f4 v[62:65], v[10:17], v[204:211], v[62:65], v194, v194 op_sel_hi:[0,0,0]
	v_mfma_scale_f32_16x16x128_f8f6f4 v[54:57], v[2:9], v[212:219], v[54:57], v194, v194 op_sel_hi:[0,0,0]
	v_mfma_scale_f32_16x16x128_f8f6f4 v[46:49], v[10:17], v[212:219], v[46:49], v194, v194 op_sel_hi:[0,0,0]
	v_mfma_scale_f32_16x16x128_f8f6f4 v[38:41], v[2:9], v[220:227], v[38:41], v194, v194 op_sel_hi:[0,0,0]
	v_mfma_scale_f32_16x16x128_f8f6f4 v[34:37], v[10:17], v[220:227], v[34:37], v194, v194 op_sel_hi:[0,0,0]
	s_setprio 0
	s_add_i32 s66, 0, 0x18000
	s_add_i32 s67, 0, 0x1c000
	v_add_u32_e32 v14, s66, v189
	v_add_u32_e32 v30, s67, v189
	ds_read_b128 v[2:5], v14
	ds_read_b128 v[6:9], v14 offset:1024
	ds_read_b128 v[10:13], v14 offset:2048
	ds_read_b128 v[14:17], v14 offset:3072
	ds_read_b128 v[18:21], v30
	ds_read_b128 v[22:25], v30 offset:1024
	ds_read_b128 v[26:29], v30 offset:2048
	ds_read_b128 v[30:33], v30 offset:3072
	s_mov_b32 m0, s50
	v_lshl_add_u64 v[228:229], s[42:43], 0, v[172:173]
	ds_read_b128 v[196:199], v193 offset:32768
	ds_read_b128 v[200:203], v193 offset:33792
	ds_read_b128 v[204:207], v193 offset:34816
	ds_read_b128 v[208:211], v193 offset:35840
	ds_read_b128 v[212:215], v193 offset:36864
	ds_read_b128 v[216:219], v193 offset:37888
	ds_read_b128 v[220:223], v193 offset:38912
	ds_read_b128 v[224:227], v193 offset:39936
	global_load_lds_dwordx4 v[228:229], off
	v_lshl_add_u64 v[228:229], s[42:43], 0, v[174:175]
	s_mov_b32 m0, s51
	s_nop 0
	global_load_lds_dwordx4 v[228:229], off
	s_waitcnt vmcnt(8)
	s_waitcnt lgkmcnt(0)
	s_barrier
; #define PG8_STAGE(bufoff, gbase, voff) do { _Pragma("unroll") for (int _i = 0; _i < 2; ++_i) \
;         __builtin_amdgcn_global_load_lds((const unsigned*)((const char*)(gbase) + (voff)[_i]), (PG8_LAS unsigned*)(lds + (bufoff) + ldsw + _i * 8192), 16, 0, 0); } while (0)
; #define PG8_WAIT_V(n) asm volatile("s_waitcnt vmcnt(" #n ")" ::: "memory")
; #define PG8_WAIT_L(n) asm volatile("s_waitcnt lgkmcnt(" #n ")" ::: "memory")
; #define PG8_BAR __builtin_amdgcn_s_barrier()
; #define PG8_SCHED __builtin_amdgcn_sched_barrier(0)
; template <class Epi, class Sched, bool ALIGN_EPI = true, bool F8 = false>
; __device__ __forceinline__ void gemm_phase(PG8_LAS unsigned char* lds, const Sched& S, const Epi& E) {
;     ...
;         for (int t = 0; t < nt; t += 2) {
;             const bool last = (t == nt - 2);
;             if constexpr (Sched::GATHER) { if (last && has_next) S.a_off(nxt, Rs, Cs, voffAn); }
;             const char* a1 = cA + (size_t)(t + 1) * kstep;
;             const char* a2 = last ? nA : cA + (size_t)(t + 2) * kstep; const char* b2 = last ? nB : cB + (size_t)(t + 2) * kstepB;
;     ...
;             PG8_WAIT_V(8); PG8_WAIT_L(0); PG8_BAR; PG8_MMA(0, 0, At, B0); PG8_MMA(0, 1, At, B1); PG8_BAR; PG8_SCHED;
;             PG8_LDA(At, 1, 1); PG8_STAGE(PG8_SB(1, 0), b3, voffB[0]); PG8_STAGE(PG8_SB(1, 1), b3, voffB[1]); PG8_STAGE(PG8_SA(1, 0), a3, vA2[0]);
;             PG8_WAIT_V(8); PG8_WAIT_L(0); PG8_BAR; PG8_MMA(1, 0, At, B0); PG8_MMA(1, 1, At, B1); PG8_BAR; PG8_SCHED;
	s_setprio 2
	v_mfma_scale_f32_16x16x128_f8f6f4 v[158:161], v[2:9], v[196:203], v[158:161], v194, v194 op_sel_hi:[0,0,0]
	v_mfma_scale_f32_16x16x128_f8f6f4 v[154:157], v[10:17], v[196:203], v[154:157], v194, v194 op_sel_hi:[0,0,0]
	v_mfma_scale_f32_16x16x128_f8f6f4 v[150:153], v[2:9], v[204:211], v[150:153], v194, v194 op_sel_hi:[0,0,0]
	v_mfma_scale_f32_16x16x128_f8f6f4 v[146:149], v[10:17], v[204:211], v[146:149], v194, v194 op_sel_hi:[0,0,0]
	v_mfma_scale_f32_16x16x128_f8f6f4 v[130:133], v[2:9], v[212:219], v[130:133], v194, v194 op_sel_hi:[0,0,0]
	v_mfma_scale_f32_16x16x128_f8f6f4 v[122:125], v[10:17], v[212:219], v[122:125], v194, v194 op_sel_hi:[0,0,0]
	v_mfma_scale_f32_16x16x128_f8f6f4 v[114:117], v[2:9], v[220:227], v[114:117], v194, v194 op_sel_hi:[0,0,0]
	v_mfma_scale_f32_16x16x128_f8f6f4 v[106:109], v[10:17], v[220:227], v[106:109], v194, v194 op_sel_hi:[0,0,0]
	s_nop 3
	s_setprio 0
	s_setprio 2
	v_mfma_scale_f32_16x16x128_f8f6f4 v[142:145], v[18:25], v[196:203], v[142:145], v194, v194 op_sel_hi:[0,0,0]
	v_mfma_scale_f32_16x16x128_f8f6f4 v[138:141], v[26:33], v[196:203], v[138:141], v194, v194 op_sel_hi:[0,0,0]
	v_mfma_scale_f32_16x16x128_f8f6f4 v[134:137], v[18:25], v[204:211], v[134:137], v194, v194 op_sel_hi:[0,0,0]
	v_mfma_scale_f32_16x16x128_f8f6f4 v[126:129], v[26:33], v[204:211], v[126:129], v194, v194 op_sel_hi:[0,0,0]
	v_mfma_scale_f32_16x16x128_f8f6f4 v[118:121], v[18:25], v[212:219], v[118:121], v194, v194 op_sel_hi:[0,0,0]
	v_mfma_scale_f32_16x16x128_f8f6f4 v[110:113], v[26:33], v[212:219], v[110:113], v194, v194 op_sel_hi:[0,0,0]
	v_mfma_scale_f32_16x16x128_f8f6f4 v[102:105], v[18:25], v[220:227], v[102:105], v194, v194 op_sel_hi:[0,0,0]
	v_mfma_scale_f32_16x16x128_f8f6f4 v[98:101], v[26:33], v[220:227], v[98:101], v194, v194 op_sel_hi:[0,0,0]
	s_setprio 0
	s_add_u32 s40, s40, 0x8000
	s_addc_u32 s41, s41, 0
	s_add_i32 s42, s66, s48
	v_lshl_add_u64 v[228:229], s[40:41], 0, v[162:163]
	s_mov_b32 m0, s42
	ds_read_b128 v[196:199], v193 offset:49152
	ds_read_b128 v[200:203], v193 offset:50176
	ds_read_b128 v[204:207], v193 offset:51200
	ds_read_b128 v[208:211], v193 offset:52224
	ds_read_b128 v[212:215], v193 offset:53248
	ds_read_b128 v[216:219], v193 offset:54272
	ds_read_b128 v[220:223], v193 offset:55296
	ds_read_b128 v[224:227], v193 offset:56320
	global_load_lds_dwordx4 v[228:229], off
	v_lshl_add_u64 v[228:229], s[40:41], 0, v[164:165]
	s_add_i32 m0, s42, 0x2000
	s_add_i32 s42, s67, s48
	global_load_lds_dwordx4 v[228:229], off
	v_lshl_add_u64 v[228:229], s[40:41], 0, v[176:177]
	s_mov_b32 m0, s42
	s_nop 0
	global_load_lds_dwordx4 v[228:229], off
	v_lshl_add_u64 v[228:229], s[40:41], 0, v[178:179]
	s_add_i32 m0, s42, 0x2000
	s_nop 0
	global_load_lds_dwordx4 v[228:229], off
	v_lshl_add_u64 v[228:229], s[30:31], 0, v[166:167]
	s_mov_b32 m0, s53
	s_nop 0
	global_load_lds_dwordx4 v[228:229], off
	v_lshl_add_u64 v[228:229], s[30:31], 0, v[168:169]
	s_mov_b32 m0, s58
	s_nop 0
	global_load_lds_dwordx4 v[228:229], off
	s_waitcnt vmcnt(8)
	s_waitcnt lgkmcnt(0)
	s_barrier
	s_setprio 2
	v_mfma_scale_f32_16x16x128_f8f6f4 v[94:97], v[2:9], v[196:203], v[94:97], v194, v194 op_sel_hi:[0,0,0]
	v_mfma_scale_f32_16x16x128_f8f6f4 v[90:93], v[10:17], v[196:203], v[90:93], v194, v194 op_sel_hi:[0,0,0]
	v_mfma_scale_f32_16x16x128_f8f6f4 v[82:85], v[2:9], v[204:211], v[82:85], v194, v194 op_sel_hi:[0,0,0]
	v_mfma_scale_f32_16x16x128_f8f6f4 v[74:77], v[10:17], v[204:211], v[74:77], v194, v194 op_sel_hi:[0,0,0]
	v_mfma_scale_f32_16x16x128_f8f6f4 v[66:69], v[2:9], v[212:219], v[66:69], v194, v194 op_sel_hi:[0,0,0]
	v_mfma_scale_f32_16x16x128_f8f6f4 v[58:61], v[10:17], v[212:219], v[58:61], v194, v194 op_sel_hi:[0,0,0]
	v_mfma_scale_f32_16x16x128_f8f6f4 v[50:53], v[2:9], v[220:227], v[50:53], v194, v194 op_sel_hi:[0,0,0]
	v_mfma_scale_f32_16x16x128_f8f6f4 v[42:45], v[10:17], v[220:227], v[42:45], v194, v194 op_sel_hi:[0,0,0]
	s_nop 3
	s_setprio 0
	s_setprio 2
	v_mfma_scale_f32_16x16x128_f8f6f4 v[86:89], v[18:25], v[196:203], v[86:89], v194, v194 op_sel_hi:[0,0,0]
	v_mfma_scale_f32_16x16x128_f8f6f4 v[78:81], v[26:33], v[196:203], v[78:81], v194, v194 op_sel_hi:[0,0,0]
	v_mfma_scale_f32_16x16x128_f8f6f4 v[70:73], v[18:25], v[204:211], v[70:73], v194, v194 op_sel_hi:[0,0,0]
	v_mfma_scale_f32_16x16x128_f8f6f4 v[62:65], v[26:33], v[204:211], v[62:65], v194, v194 op_sel_hi:[0,0,0]
	v_mfma_scale_f32_16x16x128_f8f6f4 v[54:57], v[18:25], v[212:219], v[54:57], v194, v194 op_sel_hi:[0,0,0]
	v_mfma_scale_f32_16x16x128_f8f6f4 v[46:49], v[26:33], v[212:219], v[46:49], v194, v194 op_sel_hi:[0,0,0]
	v_mfma_scale_f32_16x16x128_f8f6f4 v[38:41], v[18:25], v[220:227], v[38:41], v194, v194 op_sel_hi:[0,0,0]
	v_mfma_scale_f32_16x16x128_f8f6f4 v[34:37], v[26:33], v[220:227], v[34:37], v194, v194 op_sel_hi:[0,0,0]
	s_setprio 0
	s_add_i32 s65, s65, 2
	s_add_u32 s19, s19, 0x10000
	s_addc_u32 s21, s21, 0
	s_add_u32 s28, s28, 0x10000
	s_addc_u32 s29, s29, 0
	s_cmp_gt_u32 s65, 13
	s_cbranch_scc0 .Lh1_911

; #define PG8_STAGE(bufoff, gbase, voff) do { _Pragma("unroll") for (int _i = 0; _i < 2; ++_i) \
;         __builtin_amdgcn_global_load_lds((const unsigned*)((const char*)(gbase) + (voff)[_i]), (PG8_LAS unsigned*)(lds + (bufoff) + ldsw + _i * 8192), 16, 0, 0); } while (0)
; #define PG8_WAIT_V(n) asm volatile("s_waitcnt vmcnt(" #n ")" ::: "memory")
; #define PG8_WAIT_L(n) asm volatile("s_waitcnt lgkmcnt(" #n ")" ::: "memory")
; #define PG8_BAR __builtin_amdgcn_s_barrier()
; #define PG8_SCHED __builtin_amdgcn_sched_barrier(0)
; template <class Epi, class Sched, bool ALIGN_EPI = true, bool F8 = false>
; __device__ __forceinline__ void gemm_phase(PG8_LAS unsigned char* lds, const Sched& S, const Epi& E) {
;     ...
;             if constexpr (Sched::GATHER) { if (last && has_next) S.a_off(nxt, Rs, Cs, voffAn); }
;             const char* a1 = cA + (size_t)(t + 1) * kstep;
;             const char* a2 = last ? nA : cA + (size_t)(t + 2) * kstep; const char* b2 = last ? nB : cB + (size_t)(t + 2) * kstepB;
;             const char* a3 = a2 + kstep; const char* b3 = b2 + kstepB;
;             unsigned vA2[2][2];
; #pragma unroll
;             for (int h = 0; h < 2; ++h)
; #pragma unroll
;                 for (int i = 0; i < 2; ++i) { if constexpr (Sched::GATHER) vA2[h][i] = (last && has_next) ? voffAn[h][i] : voffA[h][i]; else vA2[h][i] = voffA[h][i]; }
;             PG8_LDB(B0, 0, 0); PG8_LDB(B1, 0, 1); PG8_SCHED; PG8_LDA(At, 0, 0); PG8_STAGE(PG8_SA(1, 1), a1, voffA[1]);
;             PG8_WAIT_V(8); PG8_WAIT_L(0); PG8_BAR; PG8_MMA(0, 0, At, B0); PG8_MMA(0, 1, At, B1); PG8_BAR; PG8_SCHED;
;             PG8_LDA(At, 0, 1); PG8_STAGE(PG8_SB(0, 0), b2, voffB[0]); PG8_STAGE(PG8_SB(0, 1), b2, voffB[1]); PG8_STAGE(PG8_SA(0, 0), a2, vA2[0]);
;             PG8_WAIT_V(8); PG8_WAIT_L(0); PG8_BAR; PG8_MMA(1, 0, At, B0); PG8_MMA(1, 1, At, B1); PG8_BAR; PG8_SCHED;
;             PG8_LDB(B0, 1, 0); PG8_LDB(B1, 1, 1); PG8_SCHED; PG8_LDA(At, 1, 0); PG8_STAGE(PG8_SA(0, 1), a2, vA2[1]);
;             PG8_WAIT_V(8); PG8_WAIT_L(0); PG8_BAR; PG8_MMA(0, 0, At, B0); PG8_MMA(0, 1, At, B1); PG8_BAR; PG8_SCHED;
.LBB0_1060:
	v_add_u32_e32 v2, s12, v210
	v_add_u32_e32 v14, s62, v210
	s_add_u32 s28, s30, 0x100
	ds_read_b128 v[18:21], v2
	ds_read_b128 v[22:25], v2 offset:1024
	ds_read_b128 v[26:29], v2 offset:2048
	ds_read_b128 v[30:33], v2 offset:3072
	ds_read_b128 v[2:5], v14
	ds_read_b128 v[6:9], v14 offset:1024
	ds_read_b128 v[10:13], v14 offset:2048
	ds_read_b128 v[14:17], v14 offset:3072
	s_addc_u32 s29, s31, 0
	s_and_b64 s[42:43], s[40:41], exec
	s_cselect_b32 s42, 0, s28
	s_cselect_b32 s43, 0, s29
	s_add_u32 s42, s6, s42
	s_addc_u32 s43, s7, s43
	s_and_b64 s[40:41], s[40:41], exec
	s_cselect_b32 s41, s25, s68
	s_cselect_b32 s40, s24, s21
	v_lshl_add_u64 v[204:205], v[196:197], 0, s[30:31]
	s_add_i32 m0, s52, 0xc000
	ds_read_b128 v[222:225], v213
	ds_read_b128 v[226:229], v213 offset:1024
	ds_read_b128 v[230:233], v213 offset:2048
	ds_read_b128 v[234:237], v213 offset:3072
	ds_read_b128 v[238:241], v213 offset:4096
	ds_read_b128 v[242:245], v213 offset:5120
	ds_read_b128 v[246:249], v213 offset:6144
	ds_read_b128 v[250:253], v213 offset:7168
	global_load_lds_dwordx4 v[204:205], off
	v_lshl_add_u64 v[204:205], v[194:195], 0, s[30:31]
	s_add_i32 m0, s52, 0xe000
	s_nop 0
	global_load_lds_dwordx4 v[204:205], off
	s_waitcnt vmcnt(8)
	s_waitcnt lgkmcnt(0)
	s_setprio 1
	v_mfma_scale_f32_16x16x128_f8f6f4 v[142:145], v[18:25], v[222:229], v[142:145], v214, v214 op_sel_hi:[0,0,0]
	v_mfma_scale_f32_16x16x128_f8f6f4 v[138:141], v[26:33], v[222:229], v[138:141], v214, v214 op_sel_hi:[0,0,0]
	v_mfma_scale_f32_16x16x128_f8f6f4 v[134:137], v[18:25], v[230:237], v[134:137], v214, v214 op_sel_hi:[0,0,0]
	v_mfma_scale_f32_16x16x128_f8f6f4 v[130:133], v[26:33], v[230:237], v[130:133], v214, v214 op_sel_hi:[0,0,0]
	v_mfma_scale_f32_16x16x128_f8f6f4 v[126:129], v[18:25], v[238:245], v[126:129], v214, v214 op_sel_hi:[0,0,0]
	v_mfma_scale_f32_16x16x128_f8f6f4 v[122:125], v[26:33], v[238:245], v[122:125], v214, v214 op_sel_hi:[0,0,0]
	v_mfma_scale_f32_16x16x128_f8f6f4 v[118:121], v[18:25], v[246:253], v[118:121], v214, v214 op_sel_hi:[0,0,0]
	v_mfma_scale_f32_16x16x128_f8f6f4 v[114:117], v[26:33], v[246:253], v[114:117], v214, v214 op_sel_hi:[0,0,0]
	s_nop 3
	s_setprio 0
	s_setprio 1
	v_mfma_scale_f32_16x16x128_f8f6f4 v[110:113], v[2:9], v[222:229], v[110:113], v214, v214 op_sel_hi:[0,0,0]
	v_mfma_scale_f32_16x16x128_f8f6f4 v[106:109], v[10:17], v[222:229], v[106:109], v214, v214 op_sel_hi:[0,0,0]
	v_mfma_scale_f32_16x16x128_f8f6f4 v[102:105], v[2:9], v[230:237], v[102:105], v214, v214 op_sel_hi:[0,0,0]
	v_mfma_scale_f32_16x16x128_f8f6f4 v[98:101], v[10:17], v[230:237], v[98:101], v214, v214 op_sel_hi:[0,0,0]
	v_mfma_scale_f32_16x16x128_f8f6f4 v[94:97], v[2:9], v[238:245], v[94:97], v214, v214 op_sel_hi:[0,0,0]
	v_mfma_scale_f32_16x16x128_f8f6f4 v[90:93], v[10:17], v[238:245], v[90:93], v214, v214 op_sel_hi:[0,0,0]
	v_mfma_scale_f32_16x16x128_f8f6f4 v[86:89], v[2:9], v[246:253], v[86:89], v214, v214 op_sel_hi:[0,0,0]
	v_mfma_scale_f32_16x16x128_f8f6f4 v[82:85], v[10:17], v[246:253], v[82:85], v214, v214 op_sel_hi:[0,0,0]
	s_setprio 0
	s_barrier
	s_add_i32 s30, s12, s48
	v_lshl_add_u64 v[204:205], s[40:41], 0, v[162:163]
	s_mov_b32 m0, s30
	ds_read_b128 v[222:225], v213 offset:16384
	ds_read_b128 v[226:229], v213 offset:17408
	ds_read_b128 v[230:233], v213 offset:18432
	ds_read_b128 v[234:237], v213 offset:19456
	ds_read_b128 v[238:241], v213 offset:20480
	ds_read_b128 v[242:245], v213 offset:21504
	ds_read_b128 v[246:249], v213 offset:22528
	ds_read_b128 v[250:253], v213 offset:23552
	global_load_lds_dwordx4 v[204:205], off
	v_lshl_add_u64 v[204:205], s[40:41], 0, v[164:165]
	s_add_i32 m0, s30, 0x2000
	s_add_i32 s30, s62, s48
	global_load_lds_dwordx4 v[204:205], off
	v_lshl_add_u64 v[204:205], s[40:41], 0, v[166:167]
	s_mov_b32 m0, s30
	v_mov_b32_e32 v203, v171
	global_load_lds_dwordx4 v[204:205], off
	v_lshl_add_u64 v[204:205], s[40:41], 0, v[168:169]
	s_add_i32 m0, s30, 0x2000
	s_nop 0
	global_load_lds_dwordx4 v[204:205], off
	s_mov_b32 m0, s52
	v_lshl_add_u64 v[204:205], s[42:43], 0, v[170:171]
	global_load_lds_dwordx4 v170, s[42:43]
	s_mov_b32 m0, s53
	s_nop 0
	global_load_lds_dwordx4 v202, s[42:43]
	s_waitcnt vmcnt(8)
	s_waitcnt lgkmcnt(0)
	v_lshl_add_u64 v[202:203], s[42:43], 0, v[202:203]
	s_setprio 1
	v_mfma_scale_f32_16x16x128_f8f6f4 v[78:81], v[18:25], v[222:229], v[78:81], v214, v214 op_sel_hi:[0,0,0]
	v_mfma_scale_f32_16x16x128_f8f6f4 v[74:77], v[26:33], v[222:229], v[74:77], v214, v214 op_sel_hi:[0,0,0]
	v_mfma_scale_f32_16x16x128_f8f6f4 v[70:73], v[18:25], v[230:237], v[70:73], v214, v214 op_sel_hi:[0,0,0]
	v_mfma_scale_f32_16x16x128_f8f6f4 v[66:69], v[26:33], v[230:237], v[66:69], v214, v214 op_sel_hi:[0,0,0]
	v_mfma_scale_f32_16x16x128_f8f6f4 v[62:65], v[18:25], v[238:245], v[62:65], v214, v214 op_sel_hi:[0,0,0]
	v_mfma_scale_f32_16x16x128_f8f6f4 v[58:61], v[26:33], v[238:245], v[58:61], v214, v214 op_sel_hi:[0,0,0]
	v_mfma_scale_f32_16x16x128_f8f6f4 v[54:57], v[18:25], v[246:253], v[54:57], v214, v214 op_sel_hi:[0,0,0]
	v_mfma_scale_f32_16x16x128_f8f6f4 v[50:53], v[26:33], v[246:253], v[50:53], v214, v214 op_sel_hi:[0,0,0]
	s_nop 3
	s_setprio 0
	s_setprio 1
	v_mfma_scale_f32_16x16x128_f8f6f4 v[46:49], v[2:9], v[222:229], v[46:49], v214, v214 op_sel_hi:[0,0,0]
	v_mfma_scale_f32_16x16x128_f8f6f4 v[42:45], v[10:17], v[222:229], v[42:45], v214, v214 op_sel_hi:[0,0,0]
	v_mfma_scale_f32_16x16x128_f8f6f4 v[38:41], v[2:9], v[230:237], v[38:41], v214, v214 op_sel_hi:[0,0,0]
	v_mfma_scale_f32_16x16x128_f8f6f4 v[34:37], v[10:17], v[230:237], v[34:37], v214, v214 op_sel_hi:[0,0,0]
	v_mfma_scale_f32_16x16x128_f8f6f4 v[146:149], v[2:9], v[238:245], v[146:149], v214, v214 op_sel_hi:[0,0,0]
	v_mfma_scale_f32_16x16x128_f8f6f4 v[150:153], v[10:17], v[238:245], v[150:153], v214, v214 op_sel_hi:[0,0,0]
	v_mfma_scale_f32_16x16x128_f8f6f4 v[154:157], v[2:9], v[246:253], v[154:157], v214, v214 op_sel_hi:[0,0,0]
	v_mfma_scale_f32_16x16x128_f8f6f4 v[158:161], v[10:17], v[246:253], v[158:161], v214, v214 op_sel_hi:[0,0,0]
	s_setprio 0
	s_barrier
; #define PG8_STAGE(bufoff, gbase, voff) do { _Pragma("unroll") for (int _i = 0; _i < 2; ++_i) \
;         __builtin_amdgcn_global_load_lds((const unsigned*)((const char*)(gbase) + (voff)[_i]), (PG8_LAS unsigned*)(lds + (bufoff) + ldsw + _i * 8192), 16, 0, 0); } while (0)
; #define PG8_WAIT_V(n) asm volatile("s_waitcnt vmcnt(" #n ")" ::: "memory")
; #define PG8_WAIT_L(n) asm volatile("s_waitcnt lgkmcnt(" #n ")" ::: "memory")
; #define PG8_BAR __builtin_amdgcn_s_barrier()
; #define PG8_SCHED __builtin_amdgcn_sched_barrier(0)
; template <class Epi, class Sched, bool ALIGN_EPI = true, bool F8 = false>
; __device__ __forceinline__ void gemm_phase(PG8_LAS unsigned char* lds, const Sched& S, const Epi& E) {
;     ...
;         for (int t = 0; t < nt; t += 2) {
;             const bool last = (t == nt - 2);
;             if constexpr (Sched::GATHER) { if (last && has_next) S.a_off(nxt, Rs, Cs, voffAn); }
;             const char* a1 = cA + (size_t)(t + 1) * kstep;
;             const char* a2 = last ? nA : cA + (size_t)(t + 2) * kstep; const char* b2 = last ? nB : cB + (size_t)(t + 2) * kstepB;
;     ...
;             PG8_LDB(B0, 1, 0); PG8_LDB(B1, 1, 1); PG8_SCHED; PG8_LDA(At, 1, 0); PG8_STAGE(PG8_SA(0, 1), a2, vA2[1]);
;             PG8_WAIT_V(8); PG8_WAIT_L(0); PG8_BAR; PG8_MMA(0, 0, At, B0); PG8_MMA(0, 1, At, B1); PG8_BAR; PG8_SCHED;
;             PG8_LDA(At, 1, 1); PG8_STAGE(PG8_SB(1, 0), b3, voffB[0]); PG8_STAGE(PG8_SB(1, 1), b3, voffB[1]); PG8_STAGE(PG8_SA(1, 0), a3, vA2[0]);
;             PG8_WAIT_V(8); PG8_WAIT_L(0); PG8_BAR; PG8_MMA(1, 0, At, B0); PG8_MMA(1, 1, At, B1); PG8_BAR; PG8_SCHED;
	s_add_i32 s70, 0, 0x18000
	s_add_i32 s71, 0, 0x1c000
	v_add_u32_e32 v14, s70, v210
	v_add_u32_e32 v30, s71, v210
	ds_read_b128 v[2:5], v14
	ds_read_b128 v[6:9], v14 offset:1024
	ds_read_b128 v[10:13], v14 offset:2048
	ds_read_b128 v[14:17], v14 offset:3072
	ds_read_b128 v[18:21], v30
	ds_read_b128 v[22:25], v30 offset:1024
	ds_read_b128 v[26:29], v30 offset:2048
	ds_read_b128 v[30:33], v30 offset:3072
	s_mov_b32 m0, s58
	v_lshl_add_u64 v[200:201], s[42:43], 0, v[200:201]
	ds_read_b128 v[222:225], v213 offset:32768
	ds_read_b128 v[226:229], v213 offset:33792
	ds_read_b128 v[230:233], v213 offset:34816
	ds_read_b128 v[234:237], v213 offset:35840
	ds_read_b128 v[238:241], v213 offset:36864
	ds_read_b128 v[242:245], v213 offset:37888
	ds_read_b128 v[246:249], v213 offset:38912
	ds_read_b128 v[250:253], v213 offset:39936
	global_load_lds_dwordx4 v[200:201], off
	v_lshl_add_u64 v[198:199], s[42:43], 0, v[198:199]
	s_mov_b32 m0, s59
	s_nop 0
	global_load_lds_dwordx4 v[198:199], off
	s_waitcnt vmcnt(8)
	s_waitcnt lgkmcnt(0)
	s_setprio 1
	v_mfma_scale_f32_16x16x128_f8f6f4 v[142:145], v[2:9], v[222:229], v[142:145], v214, v214 op_sel_hi:[0,0,0]
	v_mfma_scale_f32_16x16x128_f8f6f4 v[138:141], v[10:17], v[222:229], v[138:141], v214, v214 op_sel_hi:[0,0,0]
	v_mfma_scale_f32_16x16x128_f8f6f4 v[134:137], v[2:9], v[230:237], v[134:137], v214, v214 op_sel_hi:[0,0,0]
	v_mfma_scale_f32_16x16x128_f8f6f4 v[130:133], v[10:17], v[230:237], v[130:133], v214, v214 op_sel_hi:[0,0,0]
	v_mfma_scale_f32_16x16x128_f8f6f4 v[126:129], v[2:9], v[238:245], v[126:129], v214, v214 op_sel_hi:[0,0,0]
	v_mfma_scale_f32_16x16x128_f8f6f4 v[122:125], v[10:17], v[238:245], v[122:125], v214, v214 op_sel_hi:[0,0,0]
	v_mfma_scale_f32_16x16x128_f8f6f4 v[118:121], v[2:9], v[246:253], v[118:121], v214, v214 op_sel_hi:[0,0,0]
	v_mfma_scale_f32_16x16x128_f8f6f4 v[114:117], v[10:17], v[246:253], v[114:117], v214, v214 op_sel_hi:[0,0,0]
	s_nop 3
	s_setprio 0
	s_setprio 1
	v_mfma_scale_f32_16x16x128_f8f6f4 v[110:113], v[18:25], v[222:229], v[110:113], v214, v214 op_sel_hi:[0,0,0]
	v_mfma_scale_f32_16x16x128_f8f6f4 v[106:109], v[26:33], v[222:229], v[106:109], v214, v214 op_sel_hi:[0,0,0]
	v_mfma_scale_f32_16x16x128_f8f6f4 v[102:105], v[18:25], v[230:237], v[102:105], v214, v214 op_sel_hi:[0,0,0]
	v_mfma_scale_f32_16x16x128_f8f6f4 v[98:101], v[26:33], v[230:237], v[98:101], v214, v214 op_sel_hi:[0,0,0]
	v_mfma_scale_f32_16x16x128_f8f6f4 v[94:97], v[18:25], v[238:245], v[94:97], v214, v214 op_sel_hi:[0,0,0]
	v_mfma_scale_f32_16x16x128_f8f6f4 v[90:93], v[26:33], v[238:245], v[90:93], v214, v214 op_sel_hi:[0,0,0]
	v_mfma_scale_f32_16x16x128_f8f6f4 v[86:89], v[18:25], v[246:253], v[86:89], v214, v214 op_sel_hi:[0,0,0]
	v_mfma_scale_f32_16x16x128_f8f6f4 v[82:85], v[26:33], v[246:253], v[82:85], v214, v214 op_sel_hi:[0,0,0]
	s_setprio 0
	s_barrier
	s_add_u32 s30, s40, 0x8000
	s_addc_u32 s31, s41, 0
	s_add_i32 s40, s70, s48
	v_lshl_add_u64 v[198:199], s[30:31], 0, v[162:163]
	s_mov_b32 m0, s40
	ds_read_b128 v[222:225], v213 offset:49152
	ds_read_b128 v[226:229], v213 offset:50176
	ds_read_b128 v[230:233], v213 offset:51200
	ds_read_b128 v[234:237], v213 offset:52224
	ds_read_b128 v[238:241], v213 offset:53248
	ds_read_b128 v[242:245], v213 offset:54272
	ds_read_b128 v[246:249], v213 offset:55296
	ds_read_b128 v[250:253], v213 offset:56320
	global_load_lds_dwordx4 v[198:199], off
	v_lshl_add_u64 v[198:199], s[30:31], 0, v[164:165]
	s_add_i32 m0, s40, 0x2000
	s_add_i32 s40, s71, s48
	global_load_lds_dwordx4 v[198:199], off
	v_lshl_add_u64 v[198:199], s[30:31], 0, v[166:167]
	s_mov_b32 m0, s40
	s_nop 0
	global_load_lds_dwordx4 v[198:199], off
	v_lshl_add_u64 v[198:199], s[30:31], 0, v[168:169]
	s_add_i32 m0, s40, 0x2000
	s_nop 0
	global_load_lds_dwordx4 v[198:199], off
	v_lshl_add_u64 v[198:199], v[204:205], 0, s[18:19]
	s_mov_b32 m0, s60
	s_nop 0
	global_load_lds_dwordx4 v[198:199], off
	v_lshl_add_u64 v[198:199], v[202:203], 0, s[18:19]
	s_mov_b32 m0, s61
	s_nop 0
	global_load_lds_dwordx4 v[198:199], off
	s_waitcnt vmcnt(8)
	s_waitcnt lgkmcnt(0)
	s_setprio 1
	v_mfma_scale_f32_16x16x128_f8f6f4 v[78:81], v[2:9], v[222:229], v[78:81], v214, v214 op_sel_hi:[0,0,0]
	v_mfma_scale_f32_16x16x128_f8f6f4 v[74:77], v[10:17], v[222:229], v[74:77], v214, v214 op_sel_hi:[0,0,0]
	v_mfma_scale_f32_16x16x128_f8f6f4 v[70:73], v[2:9], v[230:237], v[70:73], v214, v214 op_sel_hi:[0,0,0]
	v_mfma_scale_f32_16x16x128_f8f6f4 v[66:69], v[10:17], v[230:237], v[66:69], v214, v214 op_sel_hi:[0,0,0]
	v_mfma_scale_f32_16x16x128_f8f6f4 v[62:65], v[2:9], v[238:245], v[62:65], v214, v214 op_sel_hi:[0,0,0]
	v_mfma_scale_f32_16x16x128_f8f6f4 v[58:61], v[10:17], v[238:245], v[58:61], v214, v214 op_sel_hi:[0,0,0]
	v_mfma_scale_f32_16x16x128_f8f6f4 v[54:57], v[2:9], v[246:253], v[54:57], v214, v214 op_sel_hi:[0,0,0]
	v_mfma_scale_f32_16x16x128_f8f6f4 v[50:53], v[10:17], v[246:253], v[50:53], v214, v214 op_sel_hi:[0,0,0]
	s_nop 3
	s_setprio 0
	s_setprio 1
	v_mfma_scale_f32_16x16x128_f8f6f4 v[46:49], v[18:25], v[222:229], v[46:49], v214, v214 op_sel_hi:[0,0,0]
	v_mfma_scale_f32_16x16x128_f8f6f4 v[42:45], v[26:33], v[222:229], v[42:45], v214, v214 op_sel_hi:[0,0,0]
	v_mfma_scale_f32_16x16x128_f8f6f4 v[38:41], v[18:25], v[230:237], v[38:41], v214, v214 op_sel_hi:[0,0,0]
	v_mfma_scale_f32_16x16x128_f8f6f4 v[34:37], v[26:33], v[230:237], v[34:37], v214, v214 op_sel_hi:[0,0,0]
	v_mfma_scale_f32_16x16x128_f8f6f4 v[146:149], v[18:25], v[238:245], v[146:149], v214, v214 op_sel_hi:[0,0,0]
	v_mfma_scale_f32_16x16x128_f8f6f4 v[150:153], v[26:33], v[238:245], v[150:153], v214, v214 op_sel_hi:[0,0,0]
	v_mfma_scale_f32_16x16x128_f8f6f4 v[154:157], v[18:25], v[246:253], v[154:157], v214, v214 op_sel_hi:[0,0,0]
	v_mfma_scale_f32_16x16x128_f8f6f4 v[158:161], v[26:33], v[246:253], v[158:161], v214, v214 op_sel_hi:[0,0,0]
	s_setprio 0
	s_barrier
	s_add_i32 s69, s69, 2
	s_add_u32 s21, s21, 0x10000
	s_addc_u32 s68, s68, 0
	s_cmp_gt_u32 s69, 13
	s_cbranch_scc1 .LBB0_1062
	s_mov_b64 s[30:31], s[28:29]
	s_branch .LBB0_1058

; #define PG8_STAGE(bufoff, gbase, voff) do { _Pragma("unroll") for (int _i = 0; _i < 2; ++_i) \
;         __builtin_amdgcn_global_load_lds((const unsigned*)((const char*)(gbase) + (voff)[_i]), (PG8_LAS unsigned*)(lds + (bufoff) + ldsw + _i * 8192), 16, 0, 0); } while (0)
; #define PG8_WAIT_V(n) asm volatile("s_waitcnt vmcnt(" #n ")" ::: "memory")
; #define PG8_WAIT_L(n) asm volatile("s_waitcnt lgkmcnt(" #n ")" ::: "memory")
; #define PG8_BAR __builtin_amdgcn_s_barrier()
; #define PG8_SCHED __builtin_amdgcn_sched_barrier(0)
; template <class Epi, class Sched, bool ALIGN_EPI = true, bool F8 = false>
; __device__ __forceinline__ void gemm_phase(PG8_LAS unsigned char* lds, const Sched& S, const Epi& E) {
;     ...
;             if constexpr (Sched::GATHER) { if (last && has_next) S.a_off(nxt, Rs, Cs, voffAn); }
;             const char* a1 = cA + (size_t)(t + 1) * kstep;
;             const char* a2 = last ? nA : cA + (size_t)(t + 2) * kstep; const char* b2 = last ? nB : cB + (size_t)(t + 2) * kstepB;
;             const char* a3 = a2 + kstep; const char* b3 = b2 + kstepB;
;             unsigned vA2[2][2];
; #pragma unroll
;             for (int h = 0; h < 2; ++h)
; #pragma unroll
;                 for (int i = 0; i < 2; ++i) { if constexpr (Sched::GATHER) vA2[h][i] = (last && has_next) ? voffAn[h][i] : voffA[h][i]; else vA2[h][i] = voffA[h][i]; }
;             PG8_LDB(B0, 0, 0); PG8_LDB(B1, 0, 1); PG8_SCHED; PG8_LDA(At, 0, 0); PG8_STAGE(PG8_SA(1, 1), a1, voffA[1]);
;             PG8_WAIT_V(8); PG8_WAIT_L(0); PG8_BAR; PG8_MMA(0, 0, At, B0); PG8_MMA(0, 1, At, B1); PG8_BAR; PG8_SCHED;
;             PG8_LDA(At, 0, 1); PG8_STAGE(PG8_SB(0, 0), b2, voffB[0]); PG8_STAGE(PG8_SB(0, 1), b2, voffB[1]); PG8_STAGE(PG8_SA(0, 0), a2, vA2[0]);
;             PG8_WAIT_V(8); PG8_WAIT_L(0); PG8_BAR; PG8_MMA(1, 0, At, B0); PG8_MMA(1, 1, At, B1); PG8_BAR; PG8_SCHED;
.Lh1_1060:
	v_add_u32_e32 v2, s12, v210
	v_add_u32_e32 v14, s62, v210
	s_add_u32 s28, s30, 0x100
	ds_read_b128 v[18:21], v2
	ds_read_b128 v[22:25], v2 offset:1024
	ds_read_b128 v[26:29], v2 offset:2048
	ds_read_b128 v[30:33], v2 offset:3072
	ds_read_b128 v[2:5], v14
	ds_read_b128 v[6:9], v14 offset:1024
	ds_read_b128 v[10:13], v14 offset:2048
	ds_read_b128 v[14:17], v14 offset:3072
	s_addc_u32 s29, s31, 0
	s_and_b64 s[42:43], s[40:41], exec
	s_cselect_b32 s42, 0, s28
	s_cselect_b32 s43, 0, s29
	s_add_u32 s42, s6, s42
	s_addc_u32 s43, s7, s43
	s_and_b64 s[40:41], s[40:41], exec
	s_cselect_b32 s41, s25, s68
	s_cselect_b32 s40, s24, s21
	v_lshl_add_u64 v[204:205], v[196:197], 0, s[30:31]
	s_add_i32 m0, s52, 0xc000
	ds_read_b128 v[222:225], v213
	ds_read_b128 v[226:229], v213 offset:1024
	ds_read_b128 v[230:233], v213 offset:2048
	ds_read_b128 v[234:237], v213 offset:3072
	ds_read_b128 v[238:241], v213 offset:4096
	ds_read_b128 v[242:245], v213 offset:5120
	ds_read_b128 v[246:249], v213 offset:6144
	ds_read_b128 v[250:253], v213 offset:7168
	global_load_lds_dwordx4 v[204:205], off
	v_lshl_add_u64 v[204:205], v[194:195], 0, s[30:31]
	s_add_i32 m0, s52, 0xe000
	s_nop 0
	global_load_lds_dwordx4 v[204:205], off
	s_waitcnt vmcnt(8)
	s_waitcnt lgkmcnt(0)
	s_barrier
	s_setprio 2
	v_mfma_scale_f32_16x16x128_f8f6f4 v[142:145], v[18:25], v[222:229], v[142:145], v214, v214 op_sel_hi:[0,0,0]
	v_mfma_scale_f32_16x16x128_f8f6f4 v[138:141], v[26:33], v[222:229], v[138:141], v214, v214 op_sel_hi:[0,0,0]
	v_mfma_scale_f32_16x16x128_f8f6f4 v[134:137], v[18:25], v[230:237], v[134:137], v214, v214 op_sel_hi:[0,0,0]
	v_mfma_scale_f32_16x16x128_f8f6f4 v[130:133], v[26:33], v[230:237], v[130:133], v214, v214 op_sel_hi:[0,0,0]
	v_mfma_scale_f32_16x16x128_f8f6f4 v[126:129], v[18:25], v[238:245], v[126:129], v214, v214 op_sel_hi:[0,0,0]
	v_mfma_scale_f32_16x16x128_f8f6f4 v[122:125], v[26:33], v[238:245], v[122:125], v214, v214 op_sel_hi:[0,0,0]
	v_mfma_scale_f32_16x16x128_f8f6f4 v[118:121], v[18:25], v[246:253], v[118:121], v214, v214 op_sel_hi:[0,0,0]
	v_mfma_scale_f32_16x16x128_f8f6f4 v[114:117], v[26:33], v[246:253], v[114:117], v214, v214 op_sel_hi:[0,0,0]
	s_nop 3
	s_setprio 0
	s_setprio 2
	v_mfma_scale_f32_16x16x128_f8f6f4 v[110:113], v[2:9], v[222:229], v[110:113], v214, v214 op_sel_hi:[0,0,0]
	v_mfma_scale_f32_16x16x128_f8f6f4 v[106:109], v[10:17], v[222:229], v[106:109], v214, v214 op_sel_hi:[0,0,0]
	v_mfma_scale_f32_16x16x128_f8f6f4 v[102:105], v[2:9], v[230:237], v[102:105], v214, v214 op_sel_hi:[0,0,0]
	v_mfma_scale_f32_16x16x128_f8f6f4 v[98:101], v[10:17], v[230:237], v[98:101], v214, v214 op_sel_hi:[0,0,0]
	v_mfma_scale_f32_16x16x128_f8f6f4 v[94:97], v[2:9], v[238:245], v[94:97], v214, v214 op_sel_hi:[0,0,0]
	v_mfma_scale_f32_16x16x128_f8f6f4 v[90:93], v[10:17], v[238:245], v[90:93], v214, v214 op_sel_hi:[0,0,0]
	v_mfma_scale_f32_16x16x128_f8f6f4 v[86:89], v[2:9], v[246:253], v[86:89], v214, v214 op_sel_hi:[0,0,0]
	v_mfma_scale_f32_16x16x128_f8f6f4 v[82:85], v[10:17], v[246:253], v[82:85], v214, v214 op_sel_hi:[0,0,0]
	s_setprio 0
	s_add_i32 s30, s12, s48
	v_lshl_add_u64 v[204:205], s[40:41], 0, v[162:163]
	s_mov_b32 m0, s30
	ds_read_b128 v[222:225], v213 offset:16384
	ds_read_b128 v[226:229], v213 offset:17408
	ds_read_b128 v[230:233], v213 offset:18432
	ds_read_b128 v[234:237], v213 offset:19456
	ds_read_b128 v[238:241], v213 offset:20480
	ds_read_b128 v[242:245], v213 offset:21504
	ds_read_b128 v[246:249], v213 offset:22528
	ds_read_b128 v[250:253], v213 offset:23552
	global_load_lds_dwordx4 v[204:205], off
	v_lshl_add_u64 v[204:205], s[40:41], 0, v[164:165]
	s_add_i32 m0, s30, 0x2000
	s_add_i32 s30, s62, s48
	global_load_lds_dwordx4 v[204:205], off
	v_lshl_add_u64 v[204:205], s[40:41], 0, v[166:167]
	s_mov_b32 m0, s30
	v_mov_b32_e32 v203, v171
	global_load_lds_dwordx4 v[204:205], off
	v_lshl_add_u64 v[204:205], s[40:41], 0, v[168:169]
	s_add_i32 m0, s30, 0x2000
	s_nop 0
	global_load_lds_dwordx4 v[204:205], off
	s_mov_b32 m0, s52
	v_lshl_add_u64 v[204:205], s[42:43], 0, v[170:171]
	global_load_lds_dwordx4 v170, s[42:43]
	s_mov_b32 m0, s53
	s_nop 0
	global_load_lds_dwordx4 v202, s[42:43]
	s_waitcnt vmcnt(8)
	s_waitcnt lgkmcnt(0)
	v_lshl_add_u64 v[202:203], s[42:43], 0, v[202:203]
	s_barrier
; #define PG8_STAGE(bufoff, gbase, voff) do { _Pragma("unroll") for (int _i = 0; _i < 2; ++_i) \
;         __builtin_amdgcn_global_load_lds((const unsigned*)((const char*)(gbase) + (voff)[_i]), (PG8_LAS unsigned*)(lds + (bufoff) + ldsw + _i * 8192), 16, 0, 0); } while (0)
; #define PG8_WAIT_V(n) asm volatile("s_waitcnt vmcnt(" #n ")" ::: "memory")
; #define PG8_WAIT_L(n) asm volatile("s_waitcnt lgkmcnt(" #n ")" ::: "memory")
; #define PG8_BAR __builtin_amdgcn_s_barrier()
; #define PG8_SCHED __builtin_amdgcn_sched_barrier(0)
; template <class Epi, class Sched, bool ALIGN_EPI = true, bool F8 = false>
; __device__ __forceinline__ void gemm_phase(PG8_LAS unsigned char* lds, const Sched& S, const Epi& E) {
;     ...
;             PG8_WAIT_V(8); PG8_WAIT_L(0); PG8_BAR; PG8_MMA(1, 0, At, B0); PG8_MMA(1, 1, At, B1); PG8_BAR; PG8_SCHED;
;             PG8_LDB(B0, 1, 0); PG8_LDB(B1, 1, 1); PG8_SCHED; PG8_LDA(At, 1, 0); PG8_STAGE(PG8_SA(0, 1), a2, vA2[1]);
;             PG8_WAIT_V(8); PG8_WAIT_L(0); PG8_BAR; PG8_MMA(0, 0, At, B0); PG8_MMA(0, 1, At, B1); PG8_BAR; PG8_SCHED;
	s_setprio 2
	v_mfma_scale_f32_16x16x128_f8f6f4 v[78:81], v[18:25], v[222:229], v[78:81], v214, v214 op_sel_hi:[0,0,0]
	v_mfma_scale_f32_16x16x128_f8f6f4 v[74:77], v[26:33], v[222:229], v[74:77], v214, v214 op_sel_hi:[0,0,0]
	v_mfma_scale_f32_16x16x128_f8f6f4 v[70:73], v[18:25], v[230:237], v[70:73], v214, v214 op_sel_hi:[0,0,0]
	v_mfma_scale_f32_16x16x128_f8f6f4 v[66:69], v[26:33], v[230:237], v[66:69], v214, v214 op_sel_hi:[0,0,0]
	v_mfma_scale_f32_16x16x128_f8f6f4 v[62:65], v[18:25], v[238:245], v[62:65], v214, v214 op_sel_hi:[0,0,0]
	v_mfma_scale_f32_16x16x128_f8f6f4 v[58:61], v[26:33], v[238:245], v[58:61], v214, v214 op_sel_hi:[0,0,0]
	v_mfma_scale_f32_16x16x128_f8f6f4 v[54:57], v[18:25], v[246:253], v[54:57], v214, v214 op_sel_hi:[0,0,0]
	v_mfma_scale_f32_16x16x128_f8f6f4 v[50:53], v[26:33], v[246:253], v[50:53], v214, v214 op_sel_hi:[0,0,0]
	s_nop 3
	s_setprio 0
	s_setprio 2
	v_mfma_scale_f32_16x16x128_f8f6f4 v[46:49], v[2:9], v[222:229], v[46:49], v214, v214 op_sel_hi:[0,0,0]
	v_mfma_scale_f32_16x16x128_f8f6f4 v[42:45], v[10:17], v[222:229], v[42:45], v214, v214 op_sel_hi:[0,0,0]
	v_mfma_scale_f32_16x16x128_f8f6f4 v[38:41], v[2:9], v[230:237], v[38:41], v214, v214 op_sel_hi:[0,0,0]
	v_mfma_scale_f32_16x16x128_f8f6f4 v[34:37], v[10:17], v[230:237], v[34:37], v214, v214 op_sel_hi:[0,0,0]
	v_mfma_scale_f32_16x16x128_f8f6f4 v[146:149], v[2:9], v[238:245], v[146:149], v214, v214 op_sel_hi:[0,0,0]
	v_mfma_scale_f32_16x16x128_f8f6f4 v[150:153], v[10:17], v[238:245], v[150:153], v214, v214 op_sel_hi:[0,0,0]
	v_mfma_scale_f32_16x16x128_f8f6f4 v[154:157], v[2:9], v[246:253], v[154:157], v214, v214 op_sel_hi:[0,0,0]
	v_mfma_scale_f32_16x16x128_f8f6f4 v[158:161], v[10:17], v[246:253], v[158:161], v214, v214 op_sel_hi:[0,0,0]
	s_setprio 0
	s_add_i32 s70, 0, 0x18000
	s_add_i32 s71, 0, 0x1c000
	v_add_u32_e32 v14, s70, v210
	v_add_u32_e32 v30, s71, v210
	ds_read_b128 v[2:5], v14
	ds_read_b128 v[6:9], v14 offset:1024
	ds_read_b128 v[10:13], v14 offset:2048
	ds_read_b128 v[14:17], v14 offset:3072
	ds_read_b128 v[18:21], v30
	ds_read_b128 v[22:25], v30 offset:1024
	ds_read_b128 v[26:29], v30 offset:2048
	ds_read_b128 v[30:33], v30 offset:3072
	s_mov_b32 m0, s58
	v_lshl_add_u64 v[200:201], s[42:43], 0, v[200:201]
	ds_read_b128 v[222:225], v213 offset:32768
	ds_read_b128 v[226:229], v213 offset:33792
	ds_read_b128 v[230:233], v213 offset:34816
	ds_read_b128 v[234:237], v213 offset:35840
	ds_read_b128 v[238:241], v213 offset:36864
	ds_read_b128 v[242:245], v213 offset:37888
	ds_read_b128 v[246:249], v213 offset:38912
	ds_read_b128 v[250:253], v213 offset:39936
	global_load_lds_dwordx4 v[200:201], off
	v_lshl_add_u64 v[198:199], s[42:43], 0, v[198:199]
	s_mov_b32 m0, s59
	s_nop 0
	global_load_lds_dwordx4 v[198:199], off
	s_waitcnt vmcnt(8)
	s_waitcnt lgkmcnt(0)
	s_barrier
; #define PG8_STAGE(bufoff, gbase, voff) do { _Pragma("unroll") for (int _i = 0; _i < 2; ++_i) \
;         __builtin_amdgcn_global_load_lds((const unsigned*)((const char*)(gbase) + (voff)[_i]), (PG8_LAS unsigned*)(lds + (bufoff) + ldsw + _i * 8192), 16, 0, 0); } while (0)
; #define PG8_WAIT_V(n) asm volatile("s_waitcnt vmcnt(" #n ")" ::: "memory")
; #define PG8_WAIT_L(n) asm volatile("s_waitcnt lgkmcnt(" #n ")" ::: "memory")
; #define PG8_BAR __builtin_amdgcn_s_barrier()
; #define PG8_SCHED __builtin_amdgcn_sched_barrier(0)
; template <class Epi, class Sched, bool ALIGN_EPI = true, bool F8 = false>
; __device__ __forceinline__ void gemm_phase(PG8_LAS unsigned char* lds, const Sched& S, const Epi& E) {
;     ...
;         for (int t = 0; t < nt; t += 2) {
;             const bool last = (t == nt - 2);
;             if constexpr (Sched::GATHER) { if (last && has_next) S.a_off(nxt, Rs, Cs, voffAn); }
;             const char* a1 = cA + (size_t)(t + 1) * kstep;
;             const char* a2 = last ? nA : cA + (size_t)(t + 2) * kstep; const char* b2 = last ? nB : cB + (size_t)(t + 2) * kstepB;
;     ...
;             PG8_WAIT_V(8); PG8_WAIT_L(0); PG8_BAR; PG8_MMA(0, 0, At, B0); PG8_MMA(0, 1, At, B1); PG8_BAR; PG8_SCHED;
;             PG8_LDA(At, 1, 1); PG8_STAGE(PG8_SB(1, 0), b3, voffB[0]); PG8_STAGE(PG8_SB(1, 1), b3, voffB[1]); PG8_STAGE(PG8_SA(1, 0), a3, vA2[0]);
;             PG8_WAIT_V(8); PG8_WAIT_L(0); PG8_BAR; PG8_MMA(1, 0, At, B0); PG8_MMA(1, 1, At, B1); PG8_BAR; PG8_SCHED;
	s_setprio 2
	v_mfma_scale_f32_16x16x128_f8f6f4 v[142:145], v[2:9], v[222:229], v[142:145], v214, v214 op_sel_hi:[0,0,0]
	v_mfma_scale_f32_16x16x128_f8f6f4 v[138:141], v[10:17], v[222:229], v[138:141], v214, v214 op_sel_hi:[0,0,0]
	v_mfma_scale_f32_16x16x128_f8f6f4 v[134:137], v[2:9], v[230:237], v[134:137], v214, v214 op_sel_hi:[0,0,0]
	v_mfma_scale_f32_16x16x128_f8f6f4 v[130:133], v[10:17], v[230:237], v[130:133], v214, v214 op_sel_hi:[0,0,0]
	v_mfma_scale_f32_16x16x128_f8f6f4 v[126:129], v[2:9], v[238:245], v[126:129], v214, v214 op_sel_hi:[0,0,0]
	v_mfma_scale_f32_16x16x128_f8f6f4 v[122:125], v[10:17], v[238:245], v[122:125], v214, v214 op_sel_hi:[0,0,0]
	v_mfma_scale_f32_16x16x128_f8f6f4 v[118:121], v[2:9], v[246:253], v[118:121], v214, v214 op_sel_hi:[0,0,0]
	v_mfma_scale_f32_16x16x128_f8f6f4 v[114:117], v[10:17], v[246:253], v[114:117], v214, v214 op_sel_hi:[0,0,0]
	s_nop 3
	s_setprio 0
	s_setprio 2
	v_mfma_scale_f32_16x16x128_f8f6f4 v[110:113], v[18:25], v[222:229], v[110:113], v214, v214 op_sel_hi:[0,0,0]
	v_mfma_scale_f32_16x16x128_f8f6f4 v[106:109], v[26:33], v[222:229], v[106:109], v214, v214 op_sel_hi:[0,0,0]
	v_mfma_scale_f32_16x16x128_f8f6f4 v[102:105], v[18:25], v[230:237], v[102:105], v214, v214 op_sel_hi:[0,0,0]
	v_mfma_scale_f32_16x16x128_f8f6f4 v[98:101], v[26:33], v[230:237], v[98:101], v214, v214 op_sel_hi:[0,0,0]
	v_mfma_scale_f32_16x16x128_f8f6f4 v[94:97], v[18:25], v[238:245], v[94:97], v214, v214 op_sel_hi:[0,0,0]
	v_mfma_scale_f32_16x16x128_f8f6f4 v[90:93], v[26:33], v[238:245], v[90:93], v214, v214 op_sel_hi:[0,0,0]
	v_mfma_scale_f32_16x16x128_f8f6f4 v[86:89], v[18:25], v[246:253], v[86:89], v214, v214 op_sel_hi:[0,0,0]
	v_mfma_scale_f32_16x16x128_f8f6f4 v[82:85], v[26:33], v[246:253], v[82:85], v214, v214 op_sel_hi:[0,0,0]
	s_setprio 0
	s_add_u32 s30, s40, 0x8000
	s_addc_u32 s31, s41, 0
	s_add_i32 s40, s70, s48
	v_lshl_add_u64 v[198:199], s[30:31], 0, v[162:163]
	s_mov_b32 m0, s40
	ds_read_b128 v[222:225], v213 offset:49152
	ds_read_b128 v[226:229], v213 offset:50176
	ds_read_b128 v[230:233], v213 offset:51200
	ds_read_b128 v[234:237], v213 offset:52224
	ds_read_b128 v[238:241], v213 offset:53248
	ds_read_b128 v[242:245], v213 offset:54272
	ds_read_b128 v[246:249], v213 offset:55296
	ds_read_b128 v[250:253], v213 offset:56320
	global_load_lds_dwordx4 v[198:199], off
	v_lshl_add_u64 v[198:199], s[30:31], 0, v[164:165]
	s_add_i32 m0, s40, 0x2000
	s_add_i32 s40, s71, s48
	global_load_lds_dwordx4 v[198:199], off
	v_lshl_add_u64 v[198:199], s[30:31], 0, v[166:167]
	s_mov_b32 m0, s40
	s_nop 0
	global_load_lds_dwordx4 v[198:199], off
	v_lshl_add_u64 v[198:199], s[30:31], 0, v[168:169]
	s_add_i32 m0, s40, 0x2000
	s_nop 0
	global_load_lds_dwordx4 v[198:199], off
	v_lshl_add_u64 v[198:199], v[204:205], 0, s[18:19]
	s_mov_b32 m0, s60
	s_nop 0
	global_load_lds_dwordx4 v[198:199], off
	v_lshl_add_u64 v[198:199], v[202:203], 0, s[18:19]
	s_mov_b32 m0, s61
	s_nop 0
	global_load_lds_dwordx4 v[198:199], off
	s_waitcnt vmcnt(8)
	s_waitcnt lgkmcnt(0)
	s_barrier
	s_setprio 2
	v_mfma_scale_f32_16x16x128_f8f6f4 v[78:81], v[2:9], v[222:229], v[78:81], v214, v214 op_sel_hi:[0,0,0]
	v_mfma_scale_f32_16x16x128_f8f6f4 v[74:77], v[10:17], v[222:229], v[74:77], v214, v214 op_sel_hi:[0,0,0]
	v_mfma_scale_f32_16x16x128_f8f6f4 v[70:73], v[2:9], v[230:237], v[70:73], v214, v214 op_sel_hi:[0,0,0]
	v_mfma_scale_f32_16x16x128_f8f6f4 v[66:69], v[10:17], v[230:237], v[66:69], v214, v214 op_sel_hi:[0,0,0]
	v_mfma_scale_f32_16x16x128_f8f6f4 v[62:65], v[2:9], v[238:245], v[62:65], v214, v214 op_sel_hi:[0,0,0]
	v_mfma_scale_f32_16x16x128_f8f6f4 v[58:61], v[10:17], v[238:245], v[58:61], v214, v214 op_sel_hi:[0,0,0]
	v_mfma_scale_f32_16x16x128_f8f6f4 v[54:57], v[2:9], v[246:253], v[54:57], v214, v214 op_sel_hi:[0,0,0]
	v_mfma_scale_f32_16x16x128_f8f6f4 v[50:53], v[10:17], v[246:253], v[50:53], v214, v214 op_sel_hi:[0,0,0]
	s_nop 3
	s_setprio 0
	s_setprio 2
	v_mfma_scale_f32_16x16x128_f8f6f4 v[46:49], v[18:25], v[222:229], v[46:49], v214, v214 op_sel_hi:[0,0,0]
	v_mfma_scale_f32_16x16x128_f8f6f4 v[42:45], v[26:33], v[222:229], v[42:45], v214, v214 op_sel_hi:[0,0,0]
	v_mfma_scale_f32_16x16x128_f8f6f4 v[38:41], v[18:25], v[230:237], v[38:41], v214, v214 op_sel_hi:[0,0,0]
	v_mfma_scale_f32_16x16x128_f8f6f4 v[34:37], v[26:33], v[230:237], v[34:37], v214, v214 op_sel_hi:[0,0,0]
	v_mfma_scale_f32_16x16x128_f8f6f4 v[146:149], v[18:25], v[238:245], v[146:149], v214, v214 op_sel_hi:[0,0,0]
	v_mfma_scale_f32_16x16x128_f8f6f4 v[150:153], v[26:33], v[238:245], v[150:153], v214, v214 op_sel_hi:[0,0,0]
	v_mfma_scale_f32_16x16x128_f8f6f4 v[154:157], v[18:25], v[246:253], v[154:157], v214, v214 op_sel_hi:[0,0,0]
	v_mfma_scale_f32_16x16x128_f8f6f4 v[158:161], v[26:33], v[246:253], v[158:161], v214, v214 op_sel_hi:[0,0,0]
	s_setprio 0
	s_add_i32 s69, s69, 2
	s_add_u32 s21, s21, 0x10000
	s_addc_u32 s68, s68, 0
	s_cmp_gt_u32 s69, 13
	s_cbranch_scc1 .LBB0_1062
	s_mov_b64 s[30:31], s[28:29]
	s_branch .Lh1_1058

; #define PG8_STAGE(bufoff, gbase, voff) do { _Pragma("unroll") for (int _i = 0; _i < 2; ++_i) \
;         __builtin_amdgcn_global_load_lds((const unsigned*)((const char*)(gbase) + (voff)[_i]), (PG8_LAS unsigned*)(lds + (bufoff) + ldsw + _i * 8192), 16, 0, 0); } while (0)
; #define PG8_WAIT_V(n) asm volatile("s_waitcnt vmcnt(" #n ")" ::: "memory")
; #define PG8_WAIT_L(n) asm volatile("s_waitcnt lgkmcnt(" #n ")" ::: "memory")
; #define PG8_BAR __builtin_amdgcn_s_barrier()
; #define PG8_SCHED __builtin_amdgcn_sched_barrier(0)
; template <class Epi, class Sched, bool ALIGN_EPI = true, bool F8 = false>
; __device__ __forceinline__ void gemm_phase(PG8_LAS unsigned char* lds, const Sched& S, const Epi& E) {
;     ...
;             PG8_LDB(B0, 0, 0); PG8_LDB(B1, 0, 1); PG8_SCHED; PG8_LDA(At, 0, 0); PG8_STAGE(PG8_SA(1, 1), a1, voffA[1]);
;             PG8_WAIT_V(8); PG8_WAIT_L(0); PG8_BAR; PG8_MMA(0, 0, At, B0); PG8_MMA(0, 1, At, B1); PG8_BAR; PG8_SCHED;
;             PG8_LDA(At, 0, 1); PG8_STAGE(PG8_SB(0, 0), b2, voffB[0]); PG8_STAGE(PG8_SB(0, 1), b2, voffB[1]); PG8_STAGE(PG8_SA(0, 0), a2, vA2[0]);
;             PG8_WAIT_V(8); PG8_WAIT_L(0); PG8_BAR; PG8_MMA(1, 0, At, B0); PG8_MMA(1, 1, At, B1); PG8_BAR; PG8_SCHED;
;             PG8_LDB(B0, 1, 0); PG8_LDB(B1, 1, 1); PG8_SCHED; PG8_LDA(At, 1, 0); PG8_STAGE(PG8_SA(0, 1), a2, vA2[1]);
;             PG8_WAIT_V(8); PG8_WAIT_L(0); PG8_BAR; PG8_MMA(0, 0, At, B0); PG8_MMA(0, 1, At, B1); PG8_BAR; PG8_SCHED;
.LBB0_1138:
	ds_read_b128 v[18:21], v189
	ds_read_b128 v[22:25], v189 offset:1024
	ds_read_b128 v[26:29], v189 offset:2048
	ds_read_b128 v[30:33], v189 offset:3072
	ds_read_b128 v[2:5], v190
	ds_read_b128 v[6:9], v190 offset:1024
	ds_read_b128 v[10:13], v190 offset:2048
	ds_read_b128 v[14:17], v190 offset:3072
	s_add_u32 s26, s24, 0x8000
	s_addc_u32 s27, s25, 0
	s_cmp_eq_u32 s68, 4
	s_cselect_b32 s30, s16, s26
	s_cselect_b32 s31, s17, s27
	s_cselect_b32 s28, s18, s23
	s_cselect_b32 s29, s19, s67
	s_add_u32 s26, s30, 0x8000
	s_addc_u32 s27, s31, 0
	v_lshl_add_u64 v[226:227], s[24:25], 0, v[184:185]
	s_add_i32 m0, s44, 0xc000
	ds_read_b128 v[194:197], v191
	ds_read_b128 v[198:201], v191 offset:1024
	ds_read_b128 v[202:205], v191 offset:2048
	ds_read_b128 v[206:209], v191 offset:3072
	ds_read_b128 v[210:213], v191 offset:4096
	ds_read_b128 v[214:217], v191 offset:5120
	ds_read_b128 v[218:221], v191 offset:6144
	ds_read_b128 v[222:225], v191 offset:7168
	global_load_lds_dwordx4 v[226:227], off
	v_lshl_add_u64 v[226:227], s[24:25], 0, v[182:183]
	s_add_i32 m0, s44, 0xe000
	s_nop 0
	global_load_lds_dwordx4 v[226:227], off
	s_waitcnt vmcnt(8)
	s_waitcnt lgkmcnt(0)
	s_setprio 1
	v_mfma_scale_f32_16x16x128_f8f6f4 v[158:161], v[18:25], v[194:201], v[158:161], v192, v192 op_sel_hi:[0,0,0]
	v_mfma_scale_f32_16x16x128_f8f6f4 v[154:157], v[26:33], v[194:201], v[154:157], v192, v192 op_sel_hi:[0,0,0]
	v_mfma_scale_f32_16x16x128_f8f6f4 v[142:145], v[18:25], v[202:209], v[142:145], v192, v192 op_sel_hi:[0,0,0]
	v_mfma_scale_f32_16x16x128_f8f6f4 v[138:141], v[26:33], v[202:209], v[138:141], v192, v192 op_sel_hi:[0,0,0]
	v_mfma_scale_f32_16x16x128_f8f6f4 v[126:129], v[18:25], v[210:217], v[126:129], v192, v192 op_sel_hi:[0,0,0]
	v_mfma_scale_f32_16x16x128_f8f6f4 v[122:125], v[26:33], v[210:217], v[122:125], v192, v192 op_sel_hi:[0,0,0]
	v_mfma_scale_f32_16x16x128_f8f6f4 v[110:113], v[18:25], v[218:225], v[110:113], v192, v192 op_sel_hi:[0,0,0]
	v_mfma_scale_f32_16x16x128_f8f6f4 v[106:109], v[26:33], v[218:225], v[106:109], v192, v192 op_sel_hi:[0,0,0]
	s_nop 3
	s_setprio 0
	s_setprio 1
	v_mfma_scale_f32_16x16x128_f8f6f4 v[150:153], v[2:9], v[194:201], v[150:153], v192, v192 op_sel_hi:[0,0,0]
	v_mfma_scale_f32_16x16x128_f8f6f4 v[146:149], v[10:17], v[194:201], v[146:149], v192, v192 op_sel_hi:[0,0,0]
	v_mfma_scale_f32_16x16x128_f8f6f4 v[134:137], v[2:9], v[202:209], v[134:137], v192, v192 op_sel_hi:[0,0,0]
	v_mfma_scale_f32_16x16x128_f8f6f4 v[130:133], v[10:17], v[202:209], v[130:133], v192, v192 op_sel_hi:[0,0,0]
	v_mfma_scale_f32_16x16x128_f8f6f4 v[118:121], v[2:9], v[210:217], v[118:121], v192, v192 op_sel_hi:[0,0,0]
	v_mfma_scale_f32_16x16x128_f8f6f4 v[114:117], v[10:17], v[210:217], v[114:117], v192, v192 op_sel_hi:[0,0,0]
	v_mfma_scale_f32_16x16x128_f8f6f4 v[102:105], v[2:9], v[218:225], v[102:105], v192, v192 op_sel_hi:[0,0,0]
	v_mfma_scale_f32_16x16x128_f8f6f4 v[98:101], v[10:17], v[218:225], v[98:101], v192, v192 op_sel_hi:[0,0,0]
	s_setprio 0
	s_barrier
	s_add_i32 s69, s53, s43
	v_lshl_add_u64 v[226:227], s[28:29], 0, v[164:165]
	s_mov_b32 m0, s69
	ds_read_b128 v[194:197], v191 offset:16384
	ds_read_b128 v[198:201], v191 offset:17408
	ds_read_b128 v[202:205], v191 offset:18432
	ds_read_b128 v[206:209], v191 offset:19456
	ds_read_b128 v[210:213], v191 offset:20480
	ds_read_b128 v[214:217], v191 offset:21504
	ds_read_b128 v[218:221], v191 offset:22528
	ds_read_b128 v[222:225], v191 offset:23552
	global_load_lds_dwordx4 v[226:227], off
	v_lshl_add_u64 v[228:229], s[28:29], 0, v[166:167]
	s_add_i32 m0, s69, 0x2000
	s_add_i32 s69, s58, s43
	global_load_lds_dwordx4 v[228:229], off
	v_lshl_add_u64 v[226:227], v[226:227], 0, s[4:5]
	s_mov_b32 m0, s69
	s_nop 0
	global_load_lds_dwordx4 v[226:227], off
	v_lshl_add_u64 v[226:227], v[228:229], 0, s[4:5]
	s_add_i32 m0, s69, 0x2000
	s_nop 0
	global_load_lds_dwordx4 v[226:227], off
	v_lshl_add_u64 v[226:227], s[30:31], 0, v[168:169]
	s_mov_b32 m0, s44
	s_nop 0
	global_load_lds_dwordx4 v[226:227], off
	v_lshl_add_u64 v[226:227], s[30:31], 0, v[170:171]
	s_mov_b32 m0, s45
	s_nop 0
	global_load_lds_dwordx4 v[226:227], off
	s_waitcnt vmcnt(8)
	s_waitcnt lgkmcnt(0)
	s_setprio 1
	v_mfma_scale_f32_16x16x128_f8f6f4 v[94:97], v[18:25], v[194:201], v[94:97], v192, v192 op_sel_hi:[0,0,0]
	v_mfma_scale_f32_16x16x128_f8f6f4 v[90:93], v[26:33], v[194:201], v[90:93], v192, v192 op_sel_hi:[0,0,0]
	v_mfma_scale_f32_16x16x128_f8f6f4 v[78:81], v[18:25], v[202:209], v[78:81], v192, v192 op_sel_hi:[0,0,0]
	v_mfma_scale_f32_16x16x128_f8f6f4 v[74:77], v[26:33], v[202:209], v[74:77], v192, v192 op_sel_hi:[0,0,0]
	v_mfma_scale_f32_16x16x128_f8f6f4 v[62:65], v[18:25], v[210:217], v[62:65], v192, v192 op_sel_hi:[0,0,0]
	v_mfma_scale_f32_16x16x128_f8f6f4 v[58:61], v[26:33], v[210:217], v[58:61], v192, v192 op_sel_hi:[0,0,0]
	v_mfma_scale_f32_16x16x128_f8f6f4 v[46:49], v[18:25], v[218:225], v[46:49], v192, v192 op_sel_hi:[0,0,0]
	v_mfma_scale_f32_16x16x128_f8f6f4 v[42:45], v[26:33], v[218:225], v[42:45], v192, v192 op_sel_hi:[0,0,0]
	s_nop 3
	s_setprio 0
	s_setprio 1
	v_mfma_scale_f32_16x16x128_f8f6f4 v[86:89], v[2:9], v[194:201], v[86:89], v192, v192 op_sel_hi:[0,0,0]
	v_mfma_scale_f32_16x16x128_f8f6f4 v[82:85], v[10:17], v[194:201], v[82:85], v192, v192 op_sel_hi:[0,0,0]
	v_mfma_scale_f32_16x16x128_f8f6f4 v[70:73], v[2:9], v[202:209], v[70:73], v192, v192 op_sel_hi:[0,0,0]
	v_mfma_scale_f32_16x16x128_f8f6f4 v[66:69], v[10:17], v[202:209], v[66:69], v192, v192 op_sel_hi:[0,0,0]
	v_mfma_scale_f32_16x16x128_f8f6f4 v[54:57], v[2:9], v[210:217], v[54:57], v192, v192 op_sel_hi:[0,0,0]
	v_mfma_scale_f32_16x16x128_f8f6f4 v[50:53], v[10:17], v[210:217], v[50:53], v192, v192 op_sel_hi:[0,0,0]
	v_mfma_scale_f32_16x16x128_f8f6f4 v[38:41], v[2:9], v[218:225], v[38:41], v192, v192 op_sel_hi:[0,0,0]
	v_mfma_scale_f32_16x16x128_f8f6f4 v[34:37], v[10:17], v[218:225], v[34:37], v192, v192 op_sel_hi:[0,0,0]
	s_setprio 0
	s_barrier
; #define PG8_STAGE(bufoff, gbase, voff) do { _Pragma("unroll") for (int _i = 0; _i < 2; ++_i) \
;         __builtin_amdgcn_global_load_lds((const unsigned*)((const char*)(gbase) + (voff)[_i]), (PG8_LAS unsigned*)(lds + (bufoff) + ldsw + _i * 8192), 16, 0, 0); } while (0)
; #define PG8_WAIT_V(n) asm volatile("s_waitcnt vmcnt(" #n ")" ::: "memory")
; #define PG8_WAIT_L(n) asm volatile("s_waitcnt lgkmcnt(" #n ")" ::: "memory")
; #define PG8_BAR __builtin_amdgcn_s_barrier()
; #define PG8_SCHED __builtin_amdgcn_sched_barrier(0)
; template <class Epi, class Sched, bool ALIGN_EPI = true, bool F8 = false>
; __device__ __forceinline__ void gemm_phase(PG8_LAS unsigned char* lds, const Sched& S, const Epi& E) {
;     ...
;         for (int t = 0; t < nt; t += 2) {
;             const bool last = (t == nt - 2);
;             if constexpr (Sched::GATHER) { if (last && has_next) S.a_off(nxt, Rs, Cs, voffAn); }
;             const char* a1 = cA + (size_t)(t + 1) * kstep;
;             const char* a2 = last ? nA : cA + (size_t)(t + 2) * kstep; const char* b2 = last ? nB : cB + (size_t)(t + 2) * kstepB;
;     ...
;             PG8_LDB(B0, 1, 0); PG8_LDB(B1, 1, 1); PG8_SCHED; PG8_LDA(At, 1, 0); PG8_STAGE(PG8_SA(0, 1), a2, vA2[1]);
;             PG8_WAIT_V(8); PG8_WAIT_L(0); PG8_BAR; PG8_MMA(0, 0, At, B0); PG8_MMA(0, 1, At, B1); PG8_BAR; PG8_SCHED;
;             PG8_LDA(At, 1, 1); PG8_STAGE(PG8_SB(1, 0), b3, voffB[0]); PG8_STAGE(PG8_SB(1, 1), b3, voffB[1]); PG8_STAGE(PG8_SA(1, 0), a3, vA2[0]);
;             PG8_WAIT_V(8); PG8_WAIT_L(0); PG8_BAR; PG8_MMA(1, 0, At, B0); PG8_MMA(1, 1, At, B1); PG8_BAR; PG8_SCHED;
	s_add_i32 s69, 0, 0x18000
	s_add_i32 s70, 0, 0x1c000
	v_add_u32_e32 v14, s69, v187
	v_add_u32_e32 v30, s70, v187
	ds_read_b128 v[2:5], v14
	ds_read_b128 v[6:9], v14 offset:1024
	ds_read_b128 v[10:13], v14 offset:2048
	ds_read_b128 v[14:17], v14 offset:3072
	ds_read_b128 v[18:21], v30
	ds_read_b128 v[22:25], v30 offset:1024
	ds_read_b128 v[26:29], v30 offset:2048
	ds_read_b128 v[30:33], v30 offset:3072
	s_mov_b32 m0, s46
	v_lshl_add_u64 v[226:227], s[30:31], 0, v[172:173]
	ds_read_b128 v[194:197], v191 offset:32768
	ds_read_b128 v[198:201], v191 offset:33792
	ds_read_b128 v[202:205], v191 offset:34816
	ds_read_b128 v[206:209], v191 offset:35840
	ds_read_b128 v[210:213], v191 offset:36864
	ds_read_b128 v[214:217], v191 offset:37888
	ds_read_b128 v[218:221], v191 offset:38912
	ds_read_b128 v[222:225], v191 offset:39936
	global_load_lds_dwordx4 v[226:227], off
	v_lshl_add_u64 v[226:227], s[30:31], 0, v[174:175]
	s_mov_b32 m0, s47
	s_nop 0
	global_load_lds_dwordx4 v[226:227], off
	s_waitcnt vmcnt(8)
	s_waitcnt lgkmcnt(0)
	s_setprio 1
	v_mfma_scale_f32_16x16x128_f8f6f4 v[158:161], v[2:9], v[194:201], v[158:161], v192, v192 op_sel_hi:[0,0,0]
	v_mfma_scale_f32_16x16x128_f8f6f4 v[154:157], v[10:17], v[194:201], v[154:157], v192, v192 op_sel_hi:[0,0,0]
	v_mfma_scale_f32_16x16x128_f8f6f4 v[142:145], v[2:9], v[202:209], v[142:145], v192, v192 op_sel_hi:[0,0,0]
	v_mfma_scale_f32_16x16x128_f8f6f4 v[138:141], v[10:17], v[202:209], v[138:141], v192, v192 op_sel_hi:[0,0,0]
	v_mfma_scale_f32_16x16x128_f8f6f4 v[126:129], v[2:9], v[210:217], v[126:129], v192, v192 op_sel_hi:[0,0,0]
	v_mfma_scale_f32_16x16x128_f8f6f4 v[122:125], v[10:17], v[210:217], v[122:125], v192, v192 op_sel_hi:[0,0,0]
	v_mfma_scale_f32_16x16x128_f8f6f4 v[110:113], v[2:9], v[218:225], v[110:113], v192, v192 op_sel_hi:[0,0,0]
	v_mfma_scale_f32_16x16x128_f8f6f4 v[106:109], v[10:17], v[218:225], v[106:109], v192, v192 op_sel_hi:[0,0,0]
	s_nop 3
	s_setprio 0
	s_setprio 1
	v_mfma_scale_f32_16x16x128_f8f6f4 v[150:153], v[18:25], v[194:201], v[150:153], v192, v192 op_sel_hi:[0,0,0]
	v_mfma_scale_f32_16x16x128_f8f6f4 v[146:149], v[26:33], v[194:201], v[146:149], v192, v192 op_sel_hi:[0,0,0]
	v_mfma_scale_f32_16x16x128_f8f6f4 v[134:137], v[18:25], v[202:209], v[134:137], v192, v192 op_sel_hi:[0,0,0]
	v_mfma_scale_f32_16x16x128_f8f6f4 v[130:133], v[26:33], v[202:209], v[130:133], v192, v192 op_sel_hi:[0,0,0]
	v_mfma_scale_f32_16x16x128_f8f6f4 v[118:121], v[18:25], v[210:217], v[118:121], v192, v192 op_sel_hi:[0,0,0]
	v_mfma_scale_f32_16x16x128_f8f6f4 v[114:117], v[26:33], v[210:217], v[114:117], v192, v192 op_sel_hi:[0,0,0]
	v_mfma_scale_f32_16x16x128_f8f6f4 v[102:105], v[18:25], v[218:225], v[102:105], v192, v192 op_sel_hi:[0,0,0]
	v_mfma_scale_f32_16x16x128_f8f6f4 v[98:101], v[26:33], v[218:225], v[98:101], v192, v192 op_sel_hi:[0,0,0]
	s_setprio 0
	s_barrier
	s_add_u32 s28, s28, 0x8000
	s_addc_u32 s29, s29, 0
	s_add_i32 s30, s69, s43
	v_lshl_add_u64 v[226:227], s[28:29], 0, v[164:165]
	s_mov_b32 m0, s30
	ds_read_b128 v[194:197], v191 offset:49152
	ds_read_b128 v[198:201], v191 offset:50176
	ds_read_b128 v[202:205], v191 offset:51200
	ds_read_b128 v[206:209], v191 offset:52224
	ds_read_b128 v[210:213], v191 offset:53248
	ds_read_b128 v[214:217], v191 offset:54272
	ds_read_b128 v[218:221], v191 offset:55296
	ds_read_b128 v[222:225], v191 offset:56320
	global_load_lds_dwordx4 v[226:227], off
	v_lshl_add_u64 v[226:227], s[28:29], 0, v[166:167]
	s_add_i32 m0, s30, 0x2000
	s_add_i32 s30, s70, s43
	global_load_lds_dwordx4 v[226:227], off
	v_lshl_add_u64 v[226:227], s[28:29], 0, v[178:179]
	s_mov_b32 m0, s30
	s_nop 0
	global_load_lds_dwordx4 v[226:227], off
	v_lshl_add_u64 v[226:227], s[28:29], 0, v[180:181]
	s_add_i32 m0, s30, 0x2000
	s_nop 0
	global_load_lds_dwordx4 v[226:227], off
	v_lshl_add_u64 v[226:227], s[26:27], 0, v[168:169]
	s_mov_b32 m0, s51
	s_nop 0
	global_load_lds_dwordx4 v[226:227], off
	v_lshl_add_u64 v[226:227], s[26:27], 0, v[170:171]
	s_mov_b32 m0, s52
	s_nop 0
	global_load_lds_dwordx4 v[226:227], off
	s_waitcnt vmcnt(8)
	s_waitcnt lgkmcnt(0)
	s_setprio 1
	v_mfma_scale_f32_16x16x128_f8f6f4 v[94:97], v[2:9], v[194:201], v[94:97], v192, v192 op_sel_hi:[0,0,0]
	v_mfma_scale_f32_16x16x128_f8f6f4 v[90:93], v[10:17], v[194:201], v[90:93], v192, v192 op_sel_hi:[0,0,0]
	v_mfma_scale_f32_16x16x128_f8f6f4 v[78:81], v[2:9], v[202:209], v[78:81], v192, v192 op_sel_hi:[0,0,0]
	v_mfma_scale_f32_16x16x128_f8f6f4 v[74:77], v[10:17], v[202:209], v[74:77], v192, v192 op_sel_hi:[0,0,0]
	v_mfma_scale_f32_16x16x128_f8f6f4 v[62:65], v[2:9], v[210:217], v[62:65], v192, v192 op_sel_hi:[0,0,0]
	v_mfma_scale_f32_16x16x128_f8f6f4 v[58:61], v[10:17], v[210:217], v[58:61], v192, v192 op_sel_hi:[0,0,0]
	v_mfma_scale_f32_16x16x128_f8f6f4 v[46:49], v[2:9], v[218:225], v[46:49], v192, v192 op_sel_hi:[0,0,0]
	v_mfma_scale_f32_16x16x128_f8f6f4 v[42:45], v[10:17], v[218:225], v[42:45], v192, v192 op_sel_hi:[0,0,0]
	s_nop 3
	s_setprio 0
	s_setprio 1
	v_mfma_scale_f32_16x16x128_f8f6f4 v[86:89], v[18:25], v[194:201], v[86:89], v192, v192 op_sel_hi:[0,0,0]
	v_mfma_scale_f32_16x16x128_f8f6f4 v[82:85], v[26:33], v[194:201], v[82:85], v192, v192 op_sel_hi:[0,0,0]
	v_mfma_scale_f32_16x16x128_f8f6f4 v[70:73], v[18:25], v[202:209], v[70:73], v192, v192 op_sel_hi:[0,0,0]
	v_mfma_scale_f32_16x16x128_f8f6f4 v[66:69], v[26:33], v[202:209], v[66:69], v192, v192 op_sel_hi:[0,0,0]
	v_mfma_scale_f32_16x16x128_f8f6f4 v[54:57], v[18:25], v[210:217], v[54:57], v192, v192 op_sel_hi:[0,0,0]
	v_mfma_scale_f32_16x16x128_f8f6f4 v[50:53], v[26:33], v[210:217], v[50:53], v192, v192 op_sel_hi:[0,0,0]
	v_mfma_scale_f32_16x16x128_f8f6f4 v[38:41], v[18:25], v[218:225], v[38:41], v192, v192 op_sel_hi:[0,0,0]
	v_mfma_scale_f32_16x16x128_f8f6f4 v[34:37], v[26:33], v[218:225], v[34:37], v192, v192 op_sel_hi:[0,0,0]
	s_setprio 0
	s_barrier
	s_add_i32 s68, s68, 2
	s_add_u32 s23, s23, 0x10000
	s_addc_u32 s67, s67, 0
	s_add_u32 s24, s24, 0x10000
	s_addc_u32 s25, s25, 0
	s_cmp_gt_u32 s68, 5
	s_cbranch_scc0 .LBB0_1138
	s_branch .Lfx_33571
; #define PG8_STAGE(bufoff, gbase, voff) do { _Pragma("unroll") for (int _i = 0; _i < 2; ++_i) \
;         __builtin_amdgcn_global_load_lds((const unsigned*)((const char*)(gbase) + (voff)[_i]), (PG8_LAS unsigned*)(lds + (bufoff) + ldsw + _i * 8192), 16, 0, 0); } while (0)
; #define PG8_WAIT_V(n) asm volatile("s_waitcnt vmcnt(" #n ")" ::: "memory")
; #define PG8_WAIT_L(n) asm volatile("s_waitcnt lgkmcnt(" #n ")" ::: "memory")
; #define PG8_BAR __builtin_amdgcn_s_barrier()
; #define PG8_SCHED __builtin_amdgcn_sched_barrier(0)
; template <class Epi, class Sched, bool ALIGN_EPI = true, bool F8 = false>
; __device__ __forceinline__ void gemm_phase(PG8_LAS unsigned char* lds, const Sched& S, const Epi& E) {
;     ...
;             PG8_LDB(B0, 0, 0); PG8_LDB(B1, 0, 1); PG8_SCHED; PG8_LDA(At, 0, 0); PG8_STAGE(PG8_SA(1, 1), a1, voffA[1]);
;             PG8_WAIT_V(8); PG8_WAIT_L(0); PG8_BAR; PG8_MMA(0, 0, At, B0); PG8_MMA(0, 1, At, B1); PG8_BAR; PG8_SCHED;
;             PG8_LDA(At, 0, 1); PG8_STAGE(PG8_SB(0, 0), b2, voffB[0]); PG8_STAGE(PG8_SB(0, 1), b2, voffB[1]); PG8_STAGE(PG8_SA(0, 0), a2, vA2[0]);
;             PG8_WAIT_V(8); PG8_WAIT_L(0); PG8_BAR; PG8_MMA(1, 0, At, B0); PG8_MMA(1, 1, At, B1); PG8_BAR; PG8_SCHED;
;             PG8_LDB(B0, 1, 0); PG8_LDB(B1, 1, 1); PG8_SCHED; PG8_LDA(At, 1, 0); PG8_STAGE(PG8_SA(0, 1), a2, vA2[1]);
;             PG8_WAIT_V(8); PG8_WAIT_L(0); PG8_BAR; PG8_MMA(0, 0, At, B0); PG8_MMA(0, 1, At, B1); PG8_BAR; PG8_SCHED;
.Lh1e_33571:
.Lh1_1138:
	ds_read_b128 v[18:21], v189
	ds_read_b128 v[22:25], v189 offset:1024
	ds_read_b128 v[26:29], v189 offset:2048
	ds_read_b128 v[30:33], v189 offset:3072
	ds_read_b128 v[2:5], v190
	ds_read_b128 v[6:9], v190 offset:1024
	ds_read_b128 v[10:13], v190 offset:2048
	ds_read_b128 v[14:17], v190 offset:3072
	s_add_u32 s26, s24, 0x8000
	s_addc_u32 s27, s25, 0
	s_cmp_eq_u32 s68, 4
	s_cselect_b32 s30, s16, s26
	s_cselect_b32 s31, s17, s27
	s_cselect_b32 s28, s18, s23
	s_cselect_b32 s29, s19, s67
	s_add_u32 s26, s30, 0x8000
	s_addc_u32 s27, s31, 0
	v_lshl_add_u64 v[226:227], s[24:25], 0, v[184:185]
	s_add_i32 m0, s44, 0xc000
	ds_read_b128 v[194:197], v191
	ds_read_b128 v[198:201], v191 offset:1024
	ds_read_b128 v[202:205], v191 offset:2048
	ds_read_b128 v[206:209], v191 offset:3072
	ds_read_b128 v[210:213], v191 offset:4096
	ds_read_b128 v[214:217], v191 offset:5120
	ds_read_b128 v[218:221], v191 offset:6144
	ds_read_b128 v[222:225], v191 offset:7168
	global_load_lds_dwordx4 v[226:227], off
	v_lshl_add_u64 v[226:227], s[24:25], 0, v[182:183]
	s_add_i32 m0, s44, 0xe000
	s_nop 0
	global_load_lds_dwordx4 v[226:227], off
	s_waitcnt vmcnt(8)
	s_waitcnt lgkmcnt(0)
	s_barrier
	s_setprio 2
	v_mfma_scale_f32_16x16x128_f8f6f4 v[158:161], v[18:25], v[194:201], v[158:161], v192, v192 op_sel_hi:[0,0,0]
	v_mfma_scale_f32_16x16x128_f8f6f4 v[154:157], v[26:33], v[194:201], v[154:157], v192, v192 op_sel_hi:[0,0,0]
	v_mfma_scale_f32_16x16x128_f8f6f4 v[142:145], v[18:25], v[202:209], v[142:145], v192, v192 op_sel_hi:[0,0,0]
	v_mfma_scale_f32_16x16x128_f8f6f4 v[138:141], v[26:33], v[202:209], v[138:141], v192, v192 op_sel_hi:[0,0,0]
	v_mfma_scale_f32_16x16x128_f8f6f4 v[126:129], v[18:25], v[210:217], v[126:129], v192, v192 op_sel_hi:[0,0,0]
	v_mfma_scale_f32_16x16x128_f8f6f4 v[122:125], v[26:33], v[210:217], v[122:125], v192, v192 op_sel_hi:[0,0,0]
	v_mfma_scale_f32_16x16x128_f8f6f4 v[110:113], v[18:25], v[218:225], v[110:113], v192, v192 op_sel_hi:[0,0,0]
	v_mfma_scale_f32_16x16x128_f8f6f4 v[106:109], v[26:33], v[218:225], v[106:109], v192, v192 op_sel_hi:[0,0,0]
	s_nop 3
	s_setprio 0
	s_setprio 2
	v_mfma_scale_f32_16x16x128_f8f6f4 v[150:153], v[2:9], v[194:201], v[150:153], v192, v192 op_sel_hi:[0,0,0]
	v_mfma_scale_f32_16x16x128_f8f6f4 v[146:149], v[10:17], v[194:201], v[146:149], v192, v192 op_sel_hi:[0,0,0]
	v_mfma_scale_f32_16x16x128_f8f6f4 v[134:137], v[2:9], v[202:209], v[134:137], v192, v192 op_sel_hi:[0,0,0]
	v_mfma_scale_f32_16x16x128_f8f6f4 v[130:133], v[10:17], v[202:209], v[130:133], v192, v192 op_sel_hi:[0,0,0]
	v_mfma_scale_f32_16x16x128_f8f6f4 v[118:121], v[2:9], v[210:217], v[118:121], v192, v192 op_sel_hi:[0,0,0]
	v_mfma_scale_f32_16x16x128_f8f6f4 v[114:117], v[10:17], v[210:217], v[114:117], v192, v192 op_sel_hi:[0,0,0]
	v_mfma_scale_f32_16x16x128_f8f6f4 v[102:105], v[2:9], v[218:225], v[102:105], v192, v192 op_sel_hi:[0,0,0]
	v_mfma_scale_f32_16x16x128_f8f6f4 v[98:101], v[10:17], v[218:225], v[98:101], v192, v192 op_sel_hi:[0,0,0]
	s_setprio 0
	s_add_i32 s69, s53, s43
	v_lshl_add_u64 v[226:227], s[28:29], 0, v[164:165]
	s_mov_b32 m0, s69
	ds_read_b128 v[194:197], v191 offset:16384
	ds_read_b128 v[198:201], v191 offset:17408
	ds_read_b128 v[202:205], v191 offset:18432
	ds_read_b128 v[206:209], v191 offset:19456
	ds_read_b128 v[210:213], v191 offset:20480
	ds_read_b128 v[214:217], v191 offset:21504
	ds_read_b128 v[218:221], v191 offset:22528
	ds_read_b128 v[222:225], v191 offset:23552
	global_load_lds_dwordx4 v[226:227], off
	v_lshl_add_u64 v[228:229], s[28:29], 0, v[166:167]
	s_add_i32 m0, s69, 0x2000
	s_add_i32 s69, s58, s43
	global_load_lds_dwordx4 v[228:229], off
	v_lshl_add_u64 v[226:227], v[226:227], 0, s[4:5]
	s_mov_b32 m0, s69
	s_nop 0
	global_load_lds_dwordx4 v[226:227], off
	v_lshl_add_u64 v[226:227], v[228:229], 0, s[4:5]
	s_add_i32 m0, s69, 0x2000
	s_nop 0
	global_load_lds_dwordx4 v[226:227], off
	v_lshl_add_u64 v[226:227], s[30:31], 0, v[168:169]
	s_mov_b32 m0, s44
	s_nop 0
	global_load_lds_dwordx4 v[226:227], off
	v_lshl_add_u64 v[226:227], s[30:31], 0, v[170:171]
	s_mov_b32 m0, s45
	s_nop 0
	global_load_lds_dwordx4 v[226:227], off
	s_waitcnt vmcnt(8)
	s_waitcnt lgkmcnt(0)
	s_barrier
	s_setprio 2
	v_mfma_scale_f32_16x16x128_f8f6f4 v[94:97], v[18:25], v[194:201], v[94:97], v192, v192 op_sel_hi:[0,0,0]
	v_mfma_scale_f32_16x16x128_f8f6f4 v[90:93], v[26:33], v[194:201], v[90:93], v192, v192 op_sel_hi:[0,0,0]
	v_mfma_scale_f32_16x16x128_f8f6f4 v[78:81], v[18:25], v[202:209], v[78:81], v192, v192 op_sel_hi:[0,0,0]
	v_mfma_scale_f32_16x16x128_f8f6f4 v[74:77], v[26:33], v[202:209], v[74:77], v192, v192 op_sel_hi:[0,0,0]
	v_mfma_scale_f32_16x16x128_f8f6f4 v[62:65], v[18:25], v[210:217], v[62:65], v192, v192 op_sel_hi:[0,0,0]
	v_mfma_scale_f32_16x16x128_f8f6f4 v[58:61], v[26:33], v[210:217], v[58:61], v192, v192 op_sel_hi:[0,0,0]
	v_mfma_scale_f32_16x16x128_f8f6f4 v[46:49], v[18:25], v[218:225], v[46:49], v192, v192 op_sel_hi:[0,0,0]
	v_mfma_scale_f32_16x16x128_f8f6f4 v[42:45], v[26:33], v[218:225], v[42:45], v192, v192 op_sel_hi:[0,0,0]
	s_nop 3
	s_setprio 0
	s_setprio 2
	v_mfma_scale_f32_16x16x128_f8f6f4 v[86:89], v[2:9], v[194:201], v[86:89], v192, v192 op_sel_hi:[0,0,0]
	v_mfma_scale_f32_16x16x128_f8f6f4 v[82:85], v[10:17], v[194:201], v[82:85], v192, v192 op_sel_hi:[0,0,0]
	v_mfma_scale_f32_16x16x128_f8f6f4 v[70:73], v[2:9], v[202:209], v[70:73], v192, v192 op_sel_hi:[0,0,0]
	v_mfma_scale_f32_16x16x128_f8f6f4 v[66:69], v[10:17], v[202:209], v[66:69], v192, v192 op_sel_hi:[0,0,0]
	v_mfma_scale_f32_16x16x128_f8f6f4 v[54:57], v[2:9], v[210:217], v[54:57], v192, v192 op_sel_hi:[0,0,0]
	v_mfma_scale_f32_16x16x128_f8f6f4 v[50:53], v[10:17], v[210:217], v[50:53], v192, v192 op_sel_hi:[0,0,0]
	v_mfma_scale_f32_16x16x128_f8f6f4 v[38:41], v[2:9], v[218:225], v[38:41], v192, v192 op_sel_hi:[0,0,0]
	v_mfma_scale_f32_16x16x128_f8f6f4 v[34:37], v[10:17], v[218:225], v[34:37], v192, v192 op_sel_hi:[0,0,0]
	s_setprio 0
	s_add_i32 s69, 0, 0x18000
	s_add_i32 s70, 0, 0x1c000
	v_add_u32_e32 v14, s69, v187
	v_add_u32_e32 v30, s70, v187
	ds_read_b128 v[2:5], v14
	ds_read_b128 v[6:9], v14 offset:1024
	ds_read_b128 v[10:13], v14 offset:2048
	ds_read_b128 v[14:17], v14 offset:3072
	ds_read_b128 v[18:21], v30
	ds_read_b128 v[22:25], v30 offset:1024
	ds_read_b128 v[26:29], v30 offset:2048
	ds_read_b128 v[30:33], v30 offset:3072
	s_mov_b32 m0, s46
	v_lshl_add_u64 v[226:227], s[30:31], 0, v[172:173]
	ds_read_b128 v[194:197], v191 offset:32768
	ds_read_b128 v[198:201], v191 offset:33792
	ds_read_b128 v[202:205], v191 offset:34816
	ds_read_b128 v[206:209], v191 offset:35840
	ds_read_b128 v[210:213], v191 offset:36864
	ds_read_b128 v[214:217], v191 offset:37888
	ds_read_b128 v[218:221], v191 offset:38912
	ds_read_b128 v[222:225], v191 offset:39936
	global_load_lds_dwordx4 v[226:227], off
	v_lshl_add_u64 v[226:227], s[30:31], 0, v[174:175]
	s_mov_b32 m0, s47
	s_nop 0
	global_load_lds_dwordx4 v[226:227], off
	s_waitcnt vmcnt(8)
	s_waitcnt lgkmcnt(0)
	s_barrier
; #define PG8_STAGE(bufoff, gbase, voff) do { _Pragma("unroll") for (int _i = 0; _i < 2; ++_i) \
;         __builtin_amdgcn_global_load_lds((const unsigned*)((const char*)(gbase) + (voff)[_i]), (PG8_LAS unsigned*)(lds + (bufoff) + ldsw + _i * 8192), 16, 0, 0); } while (0)
; #define PG8_WAIT_V(n) asm volatile("s_waitcnt vmcnt(" #n ")" ::: "memory")
; #define PG8_WAIT_L(n) asm volatile("s_waitcnt lgkmcnt(" #n ")" ::: "memory")
; #define PG8_BAR __builtin_amdgcn_s_barrier()
; #define PG8_SCHED __builtin_amdgcn_sched_barrier(0)
; template <class Epi, class Sched, bool ALIGN_EPI = true, bool F8 = false>
; __device__ __forceinline__ void gemm_phase(PG8_LAS unsigned char* lds, const Sched& S, const Epi& E) {
;     ...
;         for (int t = 0; t < nt; t += 2) {
;             const bool last = (t == nt - 2);
;             if constexpr (Sched::GATHER) { if (last && has_next) S.a_off(nxt, Rs, Cs, voffAn); }
;             const char* a1 = cA + (size_t)(t + 1) * kstep;
;             const char* a2 = last ? nA : cA + (size_t)(t + 2) * kstep; const char* b2 = last ? nB : cB + (size_t)(t + 2) * kstepB;
;     ...
;             PG8_WAIT_V(8); PG8_WAIT_L(0); PG8_BAR; PG8_MMA(0, 0, At, B0); PG8_MMA(0, 1, At, B1); PG8_BAR; PG8_SCHED;
;             PG8_LDA(At, 1, 1); PG8_STAGE(PG8_SB(1, 0), b3, voffB[0]); PG8_STAGE(PG8_SB(1, 1), b3, voffB[1]); PG8_STAGE(PG8_SA(1, 0), a3, vA2[0]);
;             PG8_WAIT_V(8); PG8_WAIT_L(0); PG8_BAR; PG8_MMA(1, 0, At, B0); PG8_MMA(1, 1, At, B1); PG8_BAR; PG8_SCHED;
	s_setprio 2
	v_mfma_scale_f32_16x16x128_f8f6f4 v[158:161], v[2:9], v[194:201], v[158:161], v192, v192 op_sel_hi:[0,0,0]
	v_mfma_scale_f32_16x16x128_f8f6f4 v[154:157], v[10:17], v[194:201], v[154:157], v192, v192 op_sel_hi:[0,0,0]
	v_mfma_scale_f32_16x16x128_f8f6f4 v[142:145], v[2:9], v[202:209], v[142:145], v192, v192 op_sel_hi:[0,0,0]
	v_mfma_scale_f32_16x16x128_f8f6f4 v[138:141], v[10:17], v[202:209], v[138:141], v192, v192 op_sel_hi:[0,0,0]
	v_mfma_scale_f32_16x16x128_f8f6f4 v[126:129], v[2:9], v[210:217], v[126:129], v192, v192 op_sel_hi:[0,0,0]
	v_mfma_scale_f32_16x16x128_f8f6f4 v[122:125], v[10:17], v[210:217], v[122:125], v192, v192 op_sel_hi:[0,0,0]
	v_mfma_scale_f32_16x16x128_f8f6f4 v[110:113], v[2:9], v[218:225], v[110:113], v192, v192 op_sel_hi:[0,0,0]
	v_mfma_scale_f32_16x16x128_f8f6f4 v[106:109], v[10:17], v[218:225], v[106:109], v192, v192 op_sel_hi:[0,0,0]
	s_nop 3
	s_setprio 0
	s_setprio 2
	v_mfma_scale_f32_16x16x128_f8f6f4 v[150:153], v[18:25], v[194:201], v[150:153], v192, v192 op_sel_hi:[0,0,0]
	v_mfma_scale_f32_16x16x128_f8f6f4 v[146:149], v[26:33], v[194:201], v[146:149], v192, v192 op_sel_hi:[0,0,0]
	v_mfma_scale_f32_16x16x128_f8f6f4 v[134:137], v[18:25], v[202:209], v[134:137], v192, v192 op_sel_hi:[0,0,0]
	v_mfma_scale_f32_16x16x128_f8f6f4 v[130:133], v[26:33], v[202:209], v[130:133], v192, v192 op_sel_hi:[0,0,0]
	v_mfma_scale_f32_16x16x128_f8f6f4 v[118:121], v[18:25], v[210:217], v[118:121], v192, v192 op_sel_hi:[0,0,0]
	v_mfma_scale_f32_16x16x128_f8f6f4 v[114:117], v[26:33], v[210:217], v[114:117], v192, v192 op_sel_hi:[0,0,0]
	v_mfma_scale_f32_16x16x128_f8f6f4 v[102:105], v[18:25], v[218:225], v[102:105], v192, v192 op_sel_hi:[0,0,0]
	v_mfma_scale_f32_16x16x128_f8f6f4 v[98:101], v[26:33], v[218:225], v[98:101], v192, v192 op_sel_hi:[0,0,0]
	s_setprio 0
	s_add_u32 s28, s28, 0x8000
	s_addc_u32 s29, s29, 0
	s_add_i32 s30, s69, s43
	v_lshl_add_u64 v[226:227], s[28:29], 0, v[164:165]
	s_mov_b32 m0, s30
	ds_read_b128 v[194:197], v191 offset:49152
	ds_read_b128 v[198:201], v191 offset:50176
	ds_read_b128 v[202:205], v191 offset:51200
	ds_read_b128 v[206:209], v191 offset:52224
	ds_read_b128 v[210:213], v191 offset:53248
	ds_read_b128 v[214:217], v191 offset:54272
	ds_read_b128 v[218:221], v191 offset:55296
	ds_read_b128 v[222:225], v191 offset:56320
	global_load_lds_dwordx4 v[226:227], off
	v_lshl_add_u64 v[226:227], s[28:29], 0, v[166:167]
	s_add_i32 m0, s30, 0x2000
	s_add_i32 s30, s70, s43
	global_load_lds_dwordx4 v[226:227], off
	v_lshl_add_u64 v[226:227], s[28:29], 0, v[178:179]
	s_mov_b32 m0, s30
	s_nop 0
	global_load_lds_dwordx4 v[226:227], off
	v_lshl_add_u64 v[226:227], s[28:29], 0, v[180:181]
	s_add_i32 m0, s30, 0x2000
	s_nop 0
	global_load_lds_dwordx4 v[226:227], off
	v_lshl_add_u64 v[226:227], s[26:27], 0, v[168:169]
	s_mov_b32 m0, s51
	s_nop 0
	global_load_lds_dwordx4 v[226:227], off
	v_lshl_add_u64 v[226:227], s[26:27], 0, v[170:171]
	s_mov_b32 m0, s52
	s_nop 0
	global_load_lds_dwordx4 v[226:227], off
	s_waitcnt vmcnt(8)
	s_waitcnt lgkmcnt(0)
	s_barrier
	s_setprio 2
	v_mfma_scale_f32_16x16x128_f8f6f4 v[94:97], v[2:9], v[194:201], v[94:97], v192, v192 op_sel_hi:[0,0,0]
	v_mfma_scale_f32_16x16x128_f8f6f4 v[90:93], v[10:17], v[194:201], v[90:93], v192, v192 op_sel_hi:[0,0,0]
	v_mfma_scale_f32_16x16x128_f8f6f4 v[78:81], v[2:9], v[202:209], v[78:81], v192, v192 op_sel_hi:[0,0,0]
	v_mfma_scale_f32_16x16x128_f8f6f4 v[74:77], v[10:17], v[202:209], v[74:77], v192, v192 op_sel_hi:[0,0,0]
	v_mfma_scale_f32_16x16x128_f8f6f4 v[62:65], v[2:9], v[210:217], v[62:65], v192, v192 op_sel_hi:[0,0,0]
	v_mfma_scale_f32_16x16x128_f8f6f4 v[58:61], v[10:17], v[210:217], v[58:61], v192, v192 op_sel_hi:[0,0,0]
	v_mfma_scale_f32_16x16x128_f8f6f4 v[46:49], v[2:9], v[218:225], v[46:49], v192, v192 op_sel_hi:[0,0,0]
	v_mfma_scale_f32_16x16x128_f8f6f4 v[42:45], v[10:17], v[218:225], v[42:45], v192, v192 op_sel_hi:[0,0,0]
	s_nop 3
	s_setprio 0
	s_setprio 2
	v_mfma_scale_f32_16x16x128_f8f6f4 v[86:89], v[18:25], v[194:201], v[86:89], v192, v192 op_sel_hi:[0,0,0]
	v_mfma_scale_f32_16x16x128_f8f6f4 v[82:85], v[26:33], v[194:201], v[82:85], v192, v192 op_sel_hi:[0,0,0]
	v_mfma_scale_f32_16x16x128_f8f6f4 v[70:73], v[18:25], v[202:209], v[70:73], v192, v192 op_sel_hi:[0,0,0]
	v_mfma_scale_f32_16x16x128_f8f6f4 v[66:69], v[26:33], v[202:209], v[66:69], v192, v192 op_sel_hi:[0,0,0]
	v_mfma_scale_f32_16x16x128_f8f6f4 v[54:57], v[18:25], v[210:217], v[54:57], v192, v192 op_sel_hi:[0,0,0]
	v_mfma_scale_f32_16x16x128_f8f6f4 v[50:53], v[26:33], v[210:217], v[50:53], v192, v192 op_sel_hi:[0,0,0]
	v_mfma_scale_f32_16x16x128_f8f6f4 v[38:41], v[18:25], v[218:225], v[38:41], v192, v192 op_sel_hi:[0,0,0]
	v_mfma_scale_f32_16x16x128_f8f6f4 v[34:37], v[26:33], v[218:225], v[34:37], v192, v192 op_sel_hi:[0,0,0]
	s_setprio 0
	s_add_i32 s68, s68, 2
	s_add_u32 s23, s23, 0x10000
	s_addc_u32 s67, s67, 0
	s_add_u32 s24, s24, 0x10000
	s_addc_u32 s25, s25, 0
	s_cmp_gt_u32 s68, 5
	s_cbranch_scc0 .Lh1_1138
